# back-edge rotation (guide 7.11) on the four GEMM K-loops: loop-back barrier becomes the loop head, exit test / loop-carried s_mov / back branch moved in front of it
# baseline (speedup 1.0000x reference)
;     __device__ __forceinline__ const char* b_ptr(const Unit& u) const { return (const char*)Bt + ((size_t)u.pn * BM * K + u.koff) * 2; }
;     __device__ __forceinline__ const char* b_ptr(const Unit& u) const { return (const char*)Bt + ((size_t)u.e * bstride + (size_t)u.pn * BM * K) * 2; }
; template <class Epi, class Sched>
; __device__ __forceinline__ void gemm_phase(LAS unsigned char* lds, const bf16_t* Abase, const int K, const Sched& S, const Epi& E, const int wvid) {
;     ...
;         const bool has_next = S.next(ui + 1, nxt);
;         const char* nB = has_next ? S.b_ptr(nxt) : cB;
;         const int nt = cur.kt;
;         for (int t = 0; t < nt; t += 2) {
;     ...
;         for (int a = 0; a < 2; ++a)
; #pragma unroll
;             for (int b = 0; b < 2; ++b)
; #pragma unroll
;                 for (int m = 0; m < 4; ++m)
; #pragma unroll
;                     for (int n = 0; n < 2; ++n) acc[a][b][m][n] = (f32x4){0.f, 0.f, 0.f, 0.f};
;         cur = nxt; cB = nB; ++ui;
.LBB0_124:
	s_ashr_i32 s25, s24, 31
	s_lshl_b64 s[26:27], s[24:25], 19
	s_add_u32 s26, s38, s26
	s_addc_u32 s27, s39, s27
	s_and_b64 s[28:29], s[0:1], exec
	s_cselect_b32 s25, s27, s5
	s_cselect_b32 s58, s26, s4
	s_add_u32 s59, s4, 0x100
	v_mov_b32_e32 v2, 0
	s_addc_u32 s60, s5, 0
	s_mov_b32 s61, -2
	s_mov_b64 s[4:5], 0
	v_mov_b32_e32 v3, v2
	v_mov_b32_e32 v4, v2
	v_mov_b32_e32 v5, v2
	v_mov_b32_e32 v6, v2
	v_mov_b32_e32 v7, v2
	v_mov_b32_e32 v8, v2
	v_mov_b32_e32 v9, v2
	v_mov_b32_e32 v18, v2
	v_mov_b32_e32 v19, v2
	v_mov_b32_e32 v20, v2
	v_mov_b32_e32 v21, v2
	v_mov_b32_e32 v22, v2
	v_mov_b32_e32 v23, v2
	v_mov_b32_e32 v24, v2
	v_mov_b32_e32 v25, v2
	v_mov_b32_e32 v34, v2
	v_mov_b32_e32 v35, v2
	v_mov_b32_e32 v36, v2
	v_mov_b32_e32 v37, v2
	v_mov_b32_e32 v38, v2
	v_mov_b32_e32 v39, v2
	v_mov_b32_e32 v40, v2
	v_mov_b32_e32 v41, v2
	v_mov_b32_e32 v50, v2
	v_mov_b32_e32 v51, v2
	v_mov_b32_e32 v52, v2
	v_mov_b32_e32 v53, v2
	v_mov_b32_e32 v54, v2
	v_mov_b32_e32 v55, v2
	v_mov_b32_e32 v56, v2
	v_mov_b32_e32 v57, v2
	v_mov_b32_e32 v10, v2
	v_mov_b32_e32 v11, v2
	v_mov_b32_e32 v12, v2
	v_mov_b32_e32 v13, v2
	v_mov_b32_e32 v14, v2
	v_mov_b32_e32 v15, v2
	v_mov_b32_e32 v16, v2
	v_mov_b32_e32 v17, v2
	v_mov_b32_e32 v26, v2
	v_mov_b32_e32 v27, v2
	v_mov_b32_e32 v28, v2
	v_mov_b32_e32 v29, v2
	v_mov_b32_e32 v30, v2
	v_mov_b32_e32 v31, v2
	v_mov_b32_e32 v32, v2
	v_mov_b32_e32 v33, v2
	v_mov_b32_e32 v42, v2
	v_mov_b32_e32 v43, v2
	v_mov_b32_e32 v44, v2
	v_mov_b32_e32 v45, v2
	v_mov_b32_e32 v46, v2
	v_mov_b32_e32 v47, v2
	v_mov_b32_e32 v48, v2
	v_mov_b32_e32 v49, v2
	v_mov_b32_e32 v58, v2
	v_mov_b32_e32 v59, v2
	v_mov_b32_e32 v60, v2
	v_mov_b32_e32 v61, v2
	v_mov_b32_e32 v62, v2
	v_mov_b32_e32 v63, v2
	v_mov_b32_e32 v64, v2
	v_mov_b32_e32 v65, v2
	v_mov_b32_e32 v66, v2
	v_mov_b32_e32 v67, v2
	v_mov_b32_e32 v68, v2
	v_mov_b32_e32 v69, v2
	v_mov_b32_e32 v70, v2
	v_mov_b32_e32 v71, v2
	v_mov_b32_e32 v72, v2
	v_mov_b32_e32 v73, v2
	v_mov_b32_e32 v74, v2
	v_mov_b32_e32 v75, v2
	v_mov_b32_e32 v76, v2
	v_mov_b32_e32 v77, v2
	v_mov_b32_e32 v78, v2
	v_mov_b32_e32 v79, v2
	v_mov_b32_e32 v80, v2
	v_mov_b32_e32 v81, v2
	v_mov_b32_e32 v90, v2
	v_mov_b32_e32 v91, v2
	v_mov_b32_e32 v92, v2
	v_mov_b32_e32 v93, v2
	v_mov_b32_e32 v94, v2
	v_mov_b32_e32 v95, v2
	v_mov_b32_e32 v96, v2
	v_mov_b32_e32 v97, v2
	v_mov_b32_e32 v106, v2
	v_mov_b32_e32 v107, v2
	v_mov_b32_e32 v108, v2
	v_mov_b32_e32 v109, v2
	v_mov_b32_e32 v110, v2
	v_mov_b32_e32 v111, v2
	v_mov_b32_e32 v112, v2
	v_mov_b32_e32 v113, v2
	v_mov_b32_e32 v82, v2
	v_mov_b32_e32 v83, v2
	v_mov_b32_e32 v84, v2
	v_mov_b32_e32 v85, v2
	v_mov_b32_e32 v86, v2
	v_mov_b32_e32 v87, v2
	v_mov_b32_e32 v88, v2
	v_mov_b32_e32 v89, v2
	v_mov_b32_e32 v98, v2
	v_mov_b32_e32 v99, v2
	v_mov_b32_e32 v100, v2
	v_mov_b32_e32 v101, v2
	v_mov_b32_e32 v102, v2
	v_mov_b32_e32 v103, v2
	v_mov_b32_e32 v104, v2
	v_mov_b32_e32 v105, v2
	v_mov_b32_e32 v114, v2
	v_mov_b32_e32 v115, v2
	v_mov_b32_e32 v116, v2
	v_mov_b32_e32 v117, v2
	v_mov_b32_e32 v118, v2
	v_mov_b32_e32 v119, v2
	v_mov_b32_e32 v120, v2
	v_mov_b32_e32 v121, v2
	v_mov_b32_e32 v122, v2
	v_mov_b32_e32 v123, v2
	v_mov_b32_e32 v124, v2
	v_mov_b32_e32 v125, v2
	v_mov_b32_e32 v126, v2
	v_mov_b32_e32 v127, v2
	v_mov_b32_e32 v128, v2
	v_mov_b32_e32 v129, v2
	s_branch .LBB0_125
.Lkhead0:
	s_barrier
; #define PG8_STAGE(bufoff, gbase, voff) do { _Pragma("unroll") for (int _i = 0; _i < 2; ++_i) \
;         __builtin_amdgcn_global_load_lds((const unsigned*)((const char*)(gbase) + (voff)[_i]), (LAS unsigned*)(lds + (bufoff) + ldsw + _i * 8192), 16, 0, 0); } while (0)
; #define PG8_LDA(dst, b, h) do { _Pragma("unroll") for (int m = 0; m < 4; ++m) _Pragma("unroll") for (int k = 0; k < 2; ++k) dst[m][k] = *(const LAS bf16x8*)(lds + PG8_SA(b, h) + aoff + m * 2048 + k * 1024); } while (0)
; #define PG8_LDB(dst, b, h) do { _Pragma("unroll") for (int n = 0; n < 2; ++n) _Pragma("unroll") for (int k = 0; k < 2; ++k) dst[n][k] = *(const LAS bf16x8*)(lds + PG8_SB(b, h) + boff + n * 2048 + k * 1024); } while (0)
; #define PG8_MMA(ai, bj, At, Bt) do { __builtin_amdgcn_s_setprio(1); _Pragma("unroll") for (int m = 0; m < 4; ++m) _Pragma("unroll") for (int n = 0; n < 2; ++n) _Pragma("unroll") for (int k = 0; k < 2; ++k) \
;         acc[ai][bj][m][n] = __builtin_amdgcn_mfma_f32_16x16x32_bf16(Bt[n][k], At[m][k], acc[ai][bj][m][n], 0, 0, 0); __builtin_amdgcn_s_setprio(0); } while (0)
; #define PG8_WAIT_L(n) asm volatile("s_waitcnt lgkmcnt(" #n ")" ::: "memory")
; #define PG8_BAR __builtin_amdgcn_s_barrier()
; #define PG8_SCHED __builtin_amdgcn_sched_barrier(0)
; #define PG8_AOFF(u) do { const int _t = lt_tid(wvid); _Pragma("unroll") for (int _i = 0; _i < 2; ++_i) { int _R, _C; stage_rc(_t * 16 + _i * 8192, _R, _C); \
;         _Pragma("unroll") for (int _h = 0; _h < 2; ++_h) voffA[_h][_i] = (S.a_row(u, _h * HALF + _R) * (unsigned)K + (unsigned)(_C + (u).koff)) * 2u; } } while (0)
; template <class Epi, class Sched>
; __device__ __forceinline__ void gemm_phase(LAS unsigned char* lds, const bf16_t* Abase, const int K, const Sched& S, const Epi& E, const int wvid) {
;     ...
;             const bool last = (t == nt - 2);
;             const char* a1 = Ab + (size_t)(t + 1) * kstep;
;             PG8_LDB(B0, 0, 0); PG8_SCHED; PG8_LDA(At, 0, 0); PG8_STAGE(PG8_SA(1, 1), a1, voffA[1]);
;             PG8_WAIT_L(8); PG8_BAR; PG8_WAIT_L(0); PG8_MMA(0, 0, At, B0); PG8_BAR; PG8_SCHED;
;             if (last && has_next) PG8_AOFF(nxt);
.LBB0_125:
	ds_read_b128 v[130:133], v193
	ds_read_b128 v[134:137], v193 offset:1024
	ds_read_b128 v[138:141], v193 offset:2048
	ds_read_b128 v[142:145], v193 offset:3072
	s_cmp_eq_u32 s61, 12
	s_cselect_b64 s[30:31], -1, 0
	s_add_i32 m0, s17, 0xc000
	s_add_u32 s28, s22, s4
	s_addc_u32 s29, s23, s5
	ds_read_b128 v[170:173], v194
	ds_read_b128 v[174:177], v194 offset:1024
	ds_read_b128 v[162:165], v194 offset:2048
	ds_read_b128 v[166:169], v194 offset:3072
	ds_read_b128 v[154:157], v194 offset:4096
	ds_read_b128 v[158:161], v194 offset:5120
	ds_read_b128 v[146:149], v194 offset:6144
	ds_read_b128 v[150:153], v194 offset:7168
	global_load_lds_dwordx4 v182, s[28:29]
	s_add_i32 m0, s17, 0xe000
	s_nop 0
	global_load_lds_dwordx4 v186, s[28:29]
	s_waitcnt lgkmcnt(8)
	s_barrier
	s_waitcnt lgkmcnt(0)
	s_waitcnt lgkmcnt(0)
	v_mfma_f32_16x16x32_bf16 v[126:129], v[130:133], v[170:173], v[126:129]
	v_mfma_f32_16x16x32_bf16 v[122:125], v[138:141], v[170:173], v[122:125]
	v_mfma_f32_16x16x32_bf16 v[118:121], v[130:133], v[162:165], v[118:121]
	v_mfma_f32_16x16x32_bf16 v[114:117], v[138:141], v[162:165], v[114:117]
	v_mfma_f32_16x16x32_bf16 v[102:105], v[130:133], v[154:157], v[102:105]
	v_mfma_f32_16x16x32_bf16 v[98:101], v[138:141], v[154:157], v[98:101]
	v_mfma_f32_16x16x32_bf16 v[86:89], v[130:133], v[146:149], v[86:89]
	v_mfma_f32_16x16x32_bf16 v[82:85], v[138:141], v[146:149], v[82:85]
	v_mfma_f32_16x16x32_bf16 v[126:129], v[134:137], v[174:177], v[126:129]
	v_mfma_f32_16x16x32_bf16 v[122:125], v[142:145], v[174:177], v[122:125]
	v_mfma_f32_16x16x32_bf16 v[118:121], v[134:137], v[166:169], v[118:121]
	v_mfma_f32_16x16x32_bf16 v[114:117], v[142:145], v[166:169], v[114:117]
	v_mfma_f32_16x16x32_bf16 v[102:105], v[134:137], v[158:161], v[102:105]
	v_mfma_f32_16x16x32_bf16 v[98:101], v[142:145], v[158:161], v[98:101]
	v_mfma_f32_16x16x32_bf16 v[86:89], v[134:137], v[150:153], v[86:89]
	v_mfma_f32_16x16x32_bf16 v[82:85], v[142:145], v[150:153], v[82:85]
	s_barrier
	s_and_b64 s[28:29], s[0:1], s[30:31]
	s_andn2_b64 vcc, exec, s[28:29]
	s_cbranch_vccnz .LBB0_127
	v_mbcnt_lo_u32_b32 v0, -1, 0
	v_mbcnt_hi_u32_b32 v0, -1, v0
	s_nop 0
	v_or_b32_e32 v0, s75, v0
	v_ashrrev_i32_e32 v183, 31, v0
	v_lshrrev_b32_e32 v183, 26, v183
	v_lshlrev_b32_e32 v182, 4, v0
	v_add_u32_e32 v183, v0, v183
	v_bfe_i32 v0, v0, 27, 1
	v_lshrrev_b32_e32 v0, 22, v0
	v_add_u32_e32 v0, v182, v0
	v_and_b32_e32 v0, 0xfffffc00, v0
	v_sub_u32_e32 v0, v182, v0
	v_lshrrev_b32_e32 v184, 4, v0
	v_bitop3_b32 v0, v184, v0, 32 bitop3:0x6c
	v_ashrrev_i32_e32 v185, 31, v0
	v_lshrrev_b32_e32 v185, 26, v185
	v_ashrrev_i32_e32 v183, 6, v183
	v_add_u32_e32 v185, v0, v185
	v_lshlrev_b32_e32 v184, 3, v183
	v_lshrrev_b32_e32 v186, 6, v185
	v_and_b32_e32 v185, 0xc0, v185
	v_and_b32_e32 v184, 0x1ffff0, v184
	v_lshlrev_b32_e32 v183, 5, v183
	v_sub_u32_e32 v0, v0, v185
	v_and_b32_e32 v183, 32, v183
	v_ashrrev_i16_sdwa v0, v216, sext(v0) dst_sel:DWORD dst_unused:UNUSED_PAD src0_sel:DWORD src1_sel:BYTE_0
	v_add_u32_e32 v184, s56, v184
	v_add_u32_e32 v182, 0x2000, v182
	v_add_u32_sdwa v0, v183, sext(v0) dst_sel:DWORD dst_unused:UNUSED_PAD src0_sel:DWORD src1_sel:WORD_0
	v_add_lshl_u32 v183, v184, v186, 11
	v_ashrrev_i32_e32 v184, 31, v182
	v_lshrrev_b32_e32 v184, 22, v184
	v_add_u32_e32 v184, v182, v184
	v_ashrrev_i32_e32 v184, 10, v184
	v_mul_i32_i24_e32 v185, 0x400, v184
	v_sub_u32_e32 v182, v182, v185
	v_lshrrev_b32_e32 v185, 4, v182
	v_bitop3_b32 v182, v185, v182, 32 bitop3:0x6c
	v_ashrrev_i32_e32 v186, 31, v182
	v_lshrrev_b32_e32 v186, 26, v186
	v_add_u32_e32 v186, v182, v186
	v_lshlrev_b32_e32 v185, 3, v184
	v_lshrrev_b32_e32 v187, 6, v186
	v_and_b32_e32 v186, 0xc0, v186
	v_and_b32_e32 v185, 0x1ffff0, v185
	v_lshlrev_b32_e32 v184, 5, v184
	v_sub_u32_e32 v182, v182, v186
	v_and_b32_e32 v184, 32, v184
	v_ashrrev_i16_sdwa v182, v216, sext(v182) dst_sel:DWORD dst_unused:UNUSED_PAD src0_sel:DWORD src1_sel:BYTE_0
	v_add_u32_e32 v185, s56, v185
	v_lshl_add_u32 v183, v0, 1, v183
	v_add_u32_sdwa v182, v184, sext(v182) dst_sel:DWORD dst_unused:UNUSED_PAD src0_sel:DWORD src1_sel:WORD_0
	v_add_lshl_u32 v184, v185, v187, 11
	v_add_u32_e32 v0, 0x40000, v183
	v_lshl_add_u32 v184, v182, 1, v184
	v_add_u32_e32 v186, 0x40000, v184
	v_mov_b32_e32 v187, v1
	v_mov_b64_e32 v[188:189], v[0:1]
	v_mov_b32_e32 v182, v0
	v_mov_b32_e32 v0, v183
	s_branch .LBB0_128

; #define PG8_STAGE(bufoff, gbase, voff) do { _Pragma("unroll") for (int _i = 0; _i < 2; ++_i) \
;         __builtin_amdgcn_global_load_lds((const unsigned*)((const char*)(gbase) + (voff)[_i]), (LAS unsigned*)(lds + (bufoff) + ldsw + _i * 8192), 16, 0, 0); } while (0)
; #define PG8_LDA(dst, b, h) do { _Pragma("unroll") for (int m = 0; m < 4; ++m) _Pragma("unroll") for (int k = 0; k < 2; ++k) dst[m][k] = *(const LAS bf16x8*)(lds + PG8_SA(b, h) + aoff + m * 2048 + k * 1024); } while (0)
; #define PG8_LDB(dst, b, h) do { _Pragma("unroll") for (int n = 0; n < 2; ++n) _Pragma("unroll") for (int k = 0; k < 2; ++k) dst[n][k] = *(const LAS bf16x8*)(lds + PG8_SB(b, h) + boff + n * 2048 + k * 1024); } while (0)
; #define PG8_MMA(ai, bj, At, Bt) do { __builtin_amdgcn_s_setprio(1); _Pragma("unroll") for (int m = 0; m < 4; ++m) _Pragma("unroll") for (int n = 0; n < 2; ++n) _Pragma("unroll") for (int k = 0; k < 2; ++k) \
;         acc[ai][bj][m][n] = __builtin_amdgcn_mfma_f32_16x16x32_bf16(Bt[n][k], At[m][k], acc[ai][bj][m][n], 0, 0, 0); __builtin_amdgcn_s_setprio(0); } while (0)
; #define PG8_WAIT_V(n) asm volatile("s_waitcnt vmcnt(" #n ")" ::: "memory")
; #define PG8_WAIT_L(n) asm volatile("s_waitcnt lgkmcnt(" #n ")" ::: "memory")
; #define PG8_BAR __builtin_amdgcn_s_barrier()
; #define PG8_SCHED __builtin_amdgcn_sched_barrier(0)
; template <class Epi, class Sched>
; __device__ __forceinline__ void gemm_phase(LAS unsigned char* lds, const bf16_t* Abase, const int K, const Sched& S, const Epi& E, const int wvid) {
;     ...
;             const char* a2 = last ? Ab : Ab + (size_t)(t + 2) * kstep; const char* b2 = last ? nB : cB + (size_t)(t + 2) * kstep;
;             const char* a3 = a2 + kstep; const char* b3 = b2 + kstep;
;             PG8_LDB(B1, 0, 1); PG8_STAGE(PG8_SB(0, 0), b2, voffB);
;             PG8_BAR; PG8_WAIT_L(0); PG8_MMA(0, 1, At, B1); PG8_BAR;
;             PG8_LDA(At, 0, 1); PG8_STAGE(PG8_SA(0, 0), a2, voffA[0]);
;             PG8_BAR; PG8_WAIT_L(0); PG8_MMA(1, 0, At, B0); PG8_BAR; PG8_SCHED;
;             PG8_STAGE(PG8_SB(0, 1), b2 + hstep, voffB);
;             PG8_WAIT_V(6); PG8_BAR; PG8_MMA(1, 1, At, B1); PG8_BAR;
;             PG8_LDB(B0, 1, 0); PG8_SCHED; PG8_LDA(At, 1, 0); PG8_STAGE(PG8_SA(0, 1), a2, voffA[1]);
.LBB0_128:
	s_add_u32 s28, s4, 0x100
	s_addc_u32 s29, s5, 0
	s_and_b64 s[34:35], s[30:31], exec
	s_cselect_b32 s34, 0, s28
	s_cselect_b32 s35, 0, s29
	s_add_u32 s34, s10, s34
	s_addc_u32 s35, s11, s35
	s_add_u32 s62, s59, s4
	s_addc_u32 s63, s60, s5
	s_add_i32 s64, 0, 0x14000
	s_and_b64 s[4:5], s[30:31], exec
	s_cselect_b32 s5, s25, s63
	s_cselect_b32 s4, s58, s62
	s_mov_b32 m0, s42
	v_add_u32_e32 v183, s64, v192
	v_lshl_add_u64 v[200:201], s[4:5], 0, v[178:179]
	ds_read_b128 v[196:199], v183
	ds_read_b128 v[224:227], v183 offset:1024
	ds_read_b128 v[228:231], v183 offset:2048
	ds_read_b128 v[232:235], v183 offset:3072
	global_load_lds_dwordx4 v[200:201], off
	v_lshl_add_u64 v[202:203], s[4:5], 0, v[180:181]
	s_mov_b32 m0, s43
	s_nop 0
	global_load_lds_dwordx4 v[202:203], off
	s_barrier
	s_waitcnt lgkmcnt(0)
	s_waitcnt lgkmcnt(0)
	v_mfma_f32_16x16x32_bf16 v[110:113], v[196:199], v[170:173], v[110:113]
	v_mfma_f32_16x16x32_bf16 v[106:109], v[228:231], v[170:173], v[106:109]
	v_mfma_f32_16x16x32_bf16 v[94:97], v[196:199], v[162:165], v[94:97]
	v_mfma_f32_16x16x32_bf16 v[90:93], v[228:231], v[162:165], v[90:93]
	v_mfma_f32_16x16x32_bf16 v[78:81], v[196:199], v[154:157], v[78:81]
	v_mfma_f32_16x16x32_bf16 v[74:77], v[228:231], v[154:157], v[74:77]
	v_mfma_f32_16x16x32_bf16 v[70:73], v[196:199], v[146:149], v[70:73]
	v_mfma_f32_16x16x32_bf16 v[66:69], v[228:231], v[146:149], v[66:69]
	v_mfma_f32_16x16x32_bf16 v[110:113], v[224:227], v[174:177], v[110:113]
	v_mfma_f32_16x16x32_bf16 v[106:109], v[232:235], v[174:177], v[106:109]
	v_mfma_f32_16x16x32_bf16 v[94:97], v[224:227], v[166:169], v[94:97]
	v_mfma_f32_16x16x32_bf16 v[90:93], v[232:235], v[166:169], v[90:93]
	v_mfma_f32_16x16x32_bf16 v[78:81], v[224:227], v[158:161], v[78:81]
	v_mfma_f32_16x16x32_bf16 v[74:77], v[232:235], v[158:161], v[74:77]
	v_mfma_f32_16x16x32_bf16 v[70:73], v[224:227], v[150:153], v[70:73]
	v_mfma_f32_16x16x32_bf16 v[66:69], v[232:235], v[150:153], v[66:69]
	s_mov_b32 m0, s17
	s_barrier
	ds_read_b128 v[146:149], v194 offset:16384
	ds_read_b128 v[150:153], v194 offset:17408
	ds_read_b128 v[154:157], v194 offset:18432
	ds_read_b128 v[158:161], v194 offset:19456
	ds_read_b128 v[162:165], v194 offset:20480
	ds_read_b128 v[166:169], v194 offset:21504
	ds_read_b128 v[170:173], v194 offset:22528
	ds_read_b128 v[174:177], v194 offset:23552
	global_load_lds_dwordx4 v0, s[34:35]
	s_mov_b32 m0, s46
	v_mov_b32_e32 v185, v1
	global_load_lds_dwordx4 v184, s[34:35]
	s_barrier
	s_waitcnt lgkmcnt(0)
	v_lshl_add_u64 v[206:207], s[34:35], 0, v[0:1]
	v_lshl_add_u64 v[208:209], s[34:35], 0, v[184:185]
	s_waitcnt lgkmcnt(0)
	v_mfma_f32_16x16x32_bf16 v[62:65], v[130:133], v[146:149], v[62:65]
	v_mfma_f32_16x16x32_bf16 v[58:61], v[138:141], v[146:149], v[58:61]
	v_mfma_f32_16x16x32_bf16 v[46:49], v[130:133], v[154:157], v[46:49]
	v_mfma_f32_16x16x32_bf16 v[42:45], v[138:141], v[154:157], v[42:45]
	v_mfma_f32_16x16x32_bf16 v[30:33], v[130:133], v[162:165], v[30:33]
	v_mfma_f32_16x16x32_bf16 v[26:29], v[138:141], v[162:165], v[26:29]
	v_mfma_f32_16x16x32_bf16 v[14:17], v[130:133], v[170:173], v[14:17]
	v_mfma_f32_16x16x32_bf16 v[10:13], v[138:141], v[170:173], v[10:13]
	v_mfma_f32_16x16x32_bf16 v[62:65], v[134:137], v[150:153], v[62:65]
	v_mfma_f32_16x16x32_bf16 v[58:61], v[142:145], v[150:153], v[58:61]
	v_mfma_f32_16x16x32_bf16 v[46:49], v[134:137], v[158:161], v[46:49]
	v_mfma_f32_16x16x32_bf16 v[42:45], v[142:145], v[158:161], v[42:45]
	v_mfma_f32_16x16x32_bf16 v[30:33], v[134:137], v[166:169], v[30:33]
	v_mfma_f32_16x16x32_bf16 v[26:29], v[142:145], v[166:169], v[26:29]
	v_mfma_f32_16x16x32_bf16 v[14:17], v[134:137], v[174:177], v[14:17]
	v_mfma_f32_16x16x32_bf16 v[10:13], v[142:145], v[174:177], v[10:13]
	s_barrier
	s_add_u32 s30, s4, 0x40000
	s_addc_u32 s31, s5, 0
	s_add_i32 s62, s64, s40
	v_lshl_add_u64 v[130:131], s[30:31], 0, v[178:179]
	s_mov_b32 m0, s62
	s_nop 0
	global_load_lds_dwordx4 v[130:131], off
	v_lshl_add_u64 v[130:131], s[30:31], 0, v[180:181]
	s_add_i32 m0, s62, 0x2000
	s_nop 0
	global_load_lds_dwordx4 v[130:131], off
	s_waitcnt vmcnt(6)
	s_barrier
	v_mfma_f32_16x16x32_bf16 v[54:57], v[196:199], v[146:149], v[54:57]
	v_mfma_f32_16x16x32_bf16 v[50:53], v[228:231], v[146:149], v[50:53]
	v_mfma_f32_16x16x32_bf16 v[38:41], v[196:199], v[154:157], v[38:41]
	v_mfma_f32_16x16x32_bf16 v[34:37], v[228:231], v[154:157], v[34:37]
	v_mfma_f32_16x16x32_bf16 v[22:25], v[196:199], v[162:165], v[22:25]
	v_mfma_f32_16x16x32_bf16 v[18:21], v[228:231], v[162:165], v[18:21]
	v_mfma_f32_16x16x32_bf16 v[6:9], v[196:199], v[170:173], v[6:9]
	v_mfma_f32_16x16x32_bf16 v[2:5], v[228:231], v[170:173], v[2:5]
	v_mfma_f32_16x16x32_bf16 v[54:57], v[224:227], v[150:153], v[54:57]
	v_mfma_f32_16x16x32_bf16 v[50:53], v[232:235], v[150:153], v[50:53]
	v_mfma_f32_16x16x32_bf16 v[38:41], v[224:227], v[158:161], v[38:41]
	v_mfma_f32_16x16x32_bf16 v[34:37], v[232:235], v[158:161], v[34:37]
	v_mfma_f32_16x16x32_bf16 v[22:25], v[224:227], v[166:169], v[22:25]
	v_mfma_f32_16x16x32_bf16 v[18:21], v[232:235], v[166:169], v[18:21]
	v_mfma_f32_16x16x32_bf16 v[6:9], v[224:227], v[174:177], v[6:9]
	v_mfma_f32_16x16x32_bf16 v[2:5], v[232:235], v[174:177], v[2:5]
	s_add_i32 s30, 0, 0x18000
	v_add_u32_e32 v142, s30, v192
	s_barrier
	ds_read_b128 v[130:133], v142
	ds_read_b128 v[134:137], v142 offset:1024
	ds_read_b128 v[138:141], v142 offset:2048
	ds_read_b128 v[142:145], v142 offset:3072
	s_mov_b32 m0, s47
	v_lshl_add_u64 v[188:189], s[34:35], 0, v[188:189]
	ds_read_b128 v[146:149], v194 offset:32768
	ds_read_b128 v[150:153], v194 offset:33792
	ds_read_b128 v[154:157], v194 offset:34816
	ds_read_b128 v[158:161], v194 offset:35840
	ds_read_b128 v[162:165], v194 offset:36864
	ds_read_b128 v[166:169], v194 offset:37888
	ds_read_b128 v[170:173], v194 offset:38912
	ds_read_b128 v[174:177], v194 offset:39936
	global_load_lds_dwordx4 v[188:189], off
	v_lshl_add_u64 v[188:189], s[34:35], 0, v[186:187]
	s_mov_b32 m0, s48
	s_nop 0
	global_load_lds_dwordx4 v[188:189], off
	s_waitcnt lgkmcnt(8)
	s_barrier
; #define PG8_STAGE(bufoff, gbase, voff) do { _Pragma("unroll") for (int _i = 0; _i < 2; ++_i) \
;         __builtin_amdgcn_global_load_lds((const unsigned*)((const char*)(gbase) + (voff)[_i]), (LAS unsigned*)(lds + (bufoff) + ldsw + _i * 8192), 16, 0, 0); } while (0)
; #define PG8_LDA(dst, b, h) do { _Pragma("unroll") for (int m = 0; m < 4; ++m) _Pragma("unroll") for (int k = 0; k < 2; ++k) dst[m][k] = *(const LAS bf16x8*)(lds + PG8_SA(b, h) + aoff + m * 2048 + k * 1024); } while (0)
; #define PG8_LDB(dst, b, h) do { _Pragma("unroll") for (int n = 0; n < 2; ++n) _Pragma("unroll") for (int k = 0; k < 2; ++k) dst[n][k] = *(const LAS bf16x8*)(lds + PG8_SB(b, h) + boff + n * 2048 + k * 1024); } while (0)
; #define PG8_MMA(ai, bj, At, Bt) do { __builtin_amdgcn_s_setprio(1); _Pragma("unroll") for (int m = 0; m < 4; ++m) _Pragma("unroll") for (int n = 0; n < 2; ++n) _Pragma("unroll") for (int k = 0; k < 2; ++k) \
;         acc[ai][bj][m][n] = __builtin_amdgcn_mfma_f32_16x16x32_bf16(Bt[n][k], At[m][k], acc[ai][bj][m][n], 0, 0, 0); __builtin_amdgcn_s_setprio(0); } while (0)
; #define PG8_WAIT_V(n) asm volatile("s_waitcnt vmcnt(" #n ")" ::: "memory")
; #define PG8_WAIT_L(n) asm volatile("s_waitcnt lgkmcnt(" #n ")" ::: "memory")
; #define PG8_BAR __builtin_amdgcn_s_barrier()
; #define PG8_SCHED __builtin_amdgcn_sched_barrier(0)
; template <class Epi, class Sched>
; __device__ __forceinline__ void gemm_phase(LAS unsigned char* lds, const bf16_t* Abase, const int K, const Sched& S, const Epi& E, const int wvid) {
;     ...
;             PG8_LDB(B0, 1, 0); PG8_SCHED; PG8_LDA(At, 1, 0); PG8_STAGE(PG8_SA(0, 1), a2, voffA[1]);
;             PG8_WAIT_L(8); PG8_BAR; PG8_WAIT_L(0); PG8_MMA(0, 0, At, B0); PG8_BAR; PG8_SCHED;
;             PG8_LDB(B1, 1, 1); PG8_STAGE(PG8_SB(1, 0), b3, voffB);
;             PG8_BAR; PG8_WAIT_L(0); PG8_MMA(0, 1, At, B1); PG8_BAR;
;             PG8_LDA(At, 1, 1); PG8_STAGE(PG8_SA(1, 0), a3, voffA[0]);
;             PG8_BAR; PG8_WAIT_L(0); PG8_MMA(1, 0, At, B0); PG8_BAR; PG8_SCHED;
;             PG8_STAGE(PG8_SB(1, 1), b3 + hstep, voffB);
;             PG8_WAIT_V(6); PG8_BAR; PG8_MMA(1, 1, At, B1); PG8_BAR;
;         }
	s_waitcnt lgkmcnt(0)
	s_waitcnt lgkmcnt(0)
	v_mfma_f32_16x16x32_bf16 v[126:129], v[130:133], v[146:149], v[126:129]
	v_mfma_f32_16x16x32_bf16 v[122:125], v[138:141], v[146:149], v[122:125]
	v_mfma_f32_16x16x32_bf16 v[118:121], v[130:133], v[154:157], v[118:121]
	v_mfma_f32_16x16x32_bf16 v[114:117], v[138:141], v[154:157], v[114:117]
	v_mfma_f32_16x16x32_bf16 v[102:105], v[130:133], v[162:165], v[102:105]
	v_mfma_f32_16x16x32_bf16 v[98:101], v[138:141], v[162:165], v[98:101]
	v_mfma_f32_16x16x32_bf16 v[86:89], v[130:133], v[170:173], v[86:89]
	v_mfma_f32_16x16x32_bf16 v[82:85], v[138:141], v[170:173], v[82:85]
	v_mfma_f32_16x16x32_bf16 v[126:129], v[134:137], v[150:153], v[126:129]
	v_mfma_f32_16x16x32_bf16 v[122:125], v[142:145], v[150:153], v[122:125]
	v_mfma_f32_16x16x32_bf16 v[118:121], v[134:137], v[158:161], v[118:121]
	v_mfma_f32_16x16x32_bf16 v[114:117], v[142:145], v[158:161], v[114:117]
	v_mfma_f32_16x16x32_bf16 v[102:105], v[134:137], v[166:169], v[102:105]
	v_mfma_f32_16x16x32_bf16 v[98:101], v[142:145], v[166:169], v[98:101]
	v_mfma_f32_16x16x32_bf16 v[86:89], v[134:137], v[174:177], v[86:89]
	v_mfma_f32_16x16x32_bf16 v[82:85], v[142:145], v[174:177], v[82:85]
	s_barrier
	s_add_i32 s31, 0, 0x1c000
	s_add_i32 s30, s30, s40
	v_add_u32_e32 v183, s31, v192
	v_lshl_add_u64 v[188:189], v[200:201], 0, s[12:13]
	s_mov_b32 m0, s30
	ds_read_b128 v[196:199], v183
	ds_read_b128 v[224:227], v183 offset:1024
	ds_read_b128 v[228:231], v183 offset:2048
	ds_read_b128 v[232:235], v183 offset:3072
	global_load_lds_dwordx4 v[188:189], off
	v_lshl_add_u64 v[188:189], v[202:203], 0, s[12:13]
	s_add_i32 m0, s30, 0x2000
	s_nop 0
	global_load_lds_dwordx4 v[188:189], off
	s_barrier
	s_waitcnt lgkmcnt(0)
	s_waitcnt lgkmcnt(0)
	v_mfma_f32_16x16x32_bf16 v[110:113], v[196:199], v[146:149], v[110:113]
	v_mfma_f32_16x16x32_bf16 v[106:109], v[228:231], v[146:149], v[106:109]
	v_mfma_f32_16x16x32_bf16 v[94:97], v[196:199], v[154:157], v[94:97]
	v_mfma_f32_16x16x32_bf16 v[90:93], v[228:231], v[154:157], v[90:93]
	v_mfma_f32_16x16x32_bf16 v[78:81], v[196:199], v[162:165], v[78:81]
	v_mfma_f32_16x16x32_bf16 v[74:77], v[228:231], v[162:165], v[74:77]
	v_mfma_f32_16x16x32_bf16 v[70:73], v[196:199], v[170:173], v[70:73]
	v_mfma_f32_16x16x32_bf16 v[66:69], v[228:231], v[170:173], v[66:69]
	v_mfma_f32_16x16x32_bf16 v[110:113], v[224:227], v[150:153], v[110:113]
	v_mfma_f32_16x16x32_bf16 v[106:109], v[232:235], v[150:153], v[106:109]
	v_mfma_f32_16x16x32_bf16 v[94:97], v[224:227], v[158:161], v[94:97]
	v_mfma_f32_16x16x32_bf16 v[90:93], v[232:235], v[158:161], v[90:93]
	v_mfma_f32_16x16x32_bf16 v[78:81], v[224:227], v[166:169], v[78:81]
	v_mfma_f32_16x16x32_bf16 v[74:77], v[232:235], v[166:169], v[74:77]
	v_mfma_f32_16x16x32_bf16 v[70:73], v[224:227], v[174:177], v[70:73]
	v_mfma_f32_16x16x32_bf16 v[66:69], v[232:235], v[174:177], v[66:69]
	s_mov_b32 m0, s52
	v_lshl_add_u64 v[188:189], v[206:207], 0, s[12:13]
	s_barrier
	ds_read_b128 v[146:149], v194 offset:49152
	ds_read_b128 v[150:153], v194 offset:50176
	ds_read_b128 v[154:157], v194 offset:51200
	ds_read_b128 v[158:161], v194 offset:52224
	ds_read_b128 v[162:165], v194 offset:53248
	ds_read_b128 v[166:169], v194 offset:54272
	ds_read_b128 v[170:173], v194 offset:55296
	ds_read_b128 v[174:177], v194 offset:56320
	global_load_lds_dwordx4 v[188:189], off
	v_lshl_add_u64 v[188:189], v[208:209], 0, s[12:13]
	s_mov_b32 m0, s53
	s_nop 0
	global_load_lds_dwordx4 v[188:189], off
	s_barrier
	s_waitcnt lgkmcnt(0)
	s_waitcnt lgkmcnt(0)
	v_mfma_f32_16x16x32_bf16 v[62:65], v[130:133], v[146:149], v[62:65]
	v_mfma_f32_16x16x32_bf16 v[58:61], v[138:141], v[146:149], v[58:61]
	v_mfma_f32_16x16x32_bf16 v[46:49], v[130:133], v[154:157], v[46:49]
	v_mfma_f32_16x16x32_bf16 v[42:45], v[138:141], v[154:157], v[42:45]
	v_mfma_f32_16x16x32_bf16 v[30:33], v[130:133], v[162:165], v[30:33]
	v_mfma_f32_16x16x32_bf16 v[26:29], v[138:141], v[162:165], v[26:29]
	v_mfma_f32_16x16x32_bf16 v[14:17], v[130:133], v[170:173], v[14:17]
	v_mfma_f32_16x16x32_bf16 v[10:13], v[138:141], v[170:173], v[10:13]
	v_mfma_f32_16x16x32_bf16 v[62:65], v[134:137], v[150:153], v[62:65]
	v_mfma_f32_16x16x32_bf16 v[58:61], v[142:145], v[150:153], v[58:61]
	v_mfma_f32_16x16x32_bf16 v[46:49], v[134:137], v[158:161], v[46:49]
	v_mfma_f32_16x16x32_bf16 v[42:45], v[142:145], v[158:161], v[42:45]
	v_mfma_f32_16x16x32_bf16 v[30:33], v[134:137], v[166:169], v[30:33]
	v_mfma_f32_16x16x32_bf16 v[26:29], v[142:145], v[166:169], v[26:29]
	v_mfma_f32_16x16x32_bf16 v[14:17], v[134:137], v[174:177], v[14:17]
	v_mfma_f32_16x16x32_bf16 v[10:13], v[142:145], v[174:177], v[10:13]
	s_barrier
	s_add_u32 s4, s4, 0x40080
	s_addc_u32 s5, s5, 0
	s_add_i32 s30, s31, s40
	v_lshl_add_u64 v[130:131], s[4:5], 0, v[178:179]
	s_mov_b32 m0, s30
	s_nop 0
	global_load_lds_dwordx4 v[130:131], off
	v_lshl_add_u64 v[130:131], s[4:5], 0, v[180:181]
	s_add_i32 m0, s30, 0x2000
	s_nop 0
	global_load_lds_dwordx4 v[130:131], off
	s_waitcnt vmcnt(6)
	s_barrier
	v_mfma_f32_16x16x32_bf16 v[54:57], v[196:199], v[146:149], v[54:57]
	v_mfma_f32_16x16x32_bf16 v[50:53], v[228:231], v[146:149], v[50:53]
	v_mfma_f32_16x16x32_bf16 v[38:41], v[196:199], v[154:157], v[38:41]
	v_mfma_f32_16x16x32_bf16 v[34:37], v[228:231], v[154:157], v[34:37]
	v_mfma_f32_16x16x32_bf16 v[22:25], v[196:199], v[162:165], v[22:25]
	v_mfma_f32_16x16x32_bf16 v[18:21], v[228:231], v[162:165], v[18:21]
	v_mfma_f32_16x16x32_bf16 v[6:9], v[196:199], v[170:173], v[6:9]
	v_mfma_f32_16x16x32_bf16 v[2:5], v[228:231], v[170:173], v[2:5]
	v_mfma_f32_16x16x32_bf16 v[54:57], v[224:227], v[150:153], v[54:57]
	v_mfma_f32_16x16x32_bf16 v[50:53], v[232:235], v[150:153], v[50:53]
	v_mfma_f32_16x16x32_bf16 v[38:41], v[224:227], v[158:161], v[38:41]
	v_mfma_f32_16x16x32_bf16 v[34:37], v[232:235], v[158:161], v[34:37]
	v_mfma_f32_16x16x32_bf16 v[22:25], v[224:227], v[166:169], v[22:25]
	v_mfma_f32_16x16x32_bf16 v[18:21], v[232:235], v[166:169], v[18:21]
	v_mfma_f32_16x16x32_bf16 v[6:9], v[224:227], v[174:177], v[6:9]
	v_mfma_f32_16x16x32_bf16 v[2:5], v[232:235], v[174:177], v[2:5]
	s_add_i32 s61, s61, 2
	s_cmp_gt_u32 s61, 13
	s_cbranch_scc1 .Lkexit0
	s_mov_b64 s[4:5], s[28:29]
	s_branch .Lkhead0
; __device__ __forceinline__ unsigned cvt_pk_bf16(float lo, float hi) { f32x2c v = {lo, hi}; bf16x2c b = __builtin_convertvector(v, bf16x2c); return __builtin_bit_cast(unsigned, b); }
;     __device__ __forceinline__ void operator()(const f32x4 (&acc)[2][2][4][2], const Unit& u, int wr, int wc, int fr, int fq) const {
;         const int row0 = u.row0 + wr * 64 + fr, col0 = u.pn * BM + wc * 32 + 8 * fq;
; #pragma unroll
;         for (int ai = 0; ai < 2; ++ai)
; #pragma unroll
;             for (int m = 0; m < 4; ++m) { const int row = row0 + ai * HALF + m * 16; bf16_t* rowp = O + (size_t)row * INW + col0;
;                 const int b = row / LT, t = row - b * LT; const int tp = (t & ~12) | ((t & 4) << 1) | ((t & 8) >> 1);
; #pragma unroll
;                 for (int bj = 0; bj < 2; ++bj) { const f32x4 v0 = acc[ai][bj][m][0], v1 = acc[ai][bj][m][1];
;                     u32x4 w; w.x = cvt_pk_bf16(v0[0], v0[1]); w.y = cvt_pk_bf16(v0[2], v0[3]); w.z = cvt_pk_bf16(v1[0], v1[1]); w.w = cvt_pk_bf16(v1[2], v1[3]);
;                     *(u32x4*)(rowp + bj * HALF) = w;
;                     const int c = col0 + bj * HALF;
;                     if (row < T && (u.pn == 4 || (u.pn == 1 && bj == 1))) {
;                         bf16_t* vt = u.pn == 4 ? VTD + ((size_t)(b * 4 + ((c - C_VD) >> 6)) * 64 + ((c - C_VD) & 63)) * LTP + tp
;                                                : VTA + ((size_t)(b * 2 + ((c - C_VA) >> 6)) * 64 + ((c - C_VA) & 63)) * LTP + tp;
;                         const unsigned ww[4] = {w.x, w.y, w.z, w.w};
; #pragma unroll
;                         for (int e = 0; e < 4; ++e) { vt[(size_t)(2 * e) * LTP] = (bf16_t)ww[e]; vt[(size_t)(2 * e + 1) * LTP] = (bf16_t)(ww[e] >> 16); } } } }
.Lkexit0:
	s_barrier
.LBB0_130:
	v_add_u32_e32 v137, s57, v190
	v_lshlrev_b32_e32 v132, 1, v137
	s_lshl_b32 s0, s16, 8
	v_and_b32_e32 v132, 8, v132
	v_lshrrev_b32_e32 v133, 1, v137
	s_or_b32 s25, s0, s51
	v_and_or_b32 v138, v133, 4, v132
	v_mov_b64_e32 v[132:133], s[18:19]
	v_or_b32_e32 v130, s25, v191
	v_mad_i64_i32 v[132:133], s[4:5], v137, s97, v[132:133]
	v_ashrrev_i32_e32 v131, 31, v130
	s_mov_b32 s4, 0x7f807f81
	v_lshl_add_u64 v[134:135], v[130:131], 1, v[132:133]
	v_mul_hi_i32 v132, v137, s4
	v_lshrrev_b32_e32 v133, 31, v132
	v_ashrrev_i32_e32 v132, 11, v132
	s_cmp_lg_u32 s16, 4
	v_add_u32_e32 v139, v132, v133
	s_movk_i32 s4, 0xeff0
	s_cselect_b64 s[0:1], -1, 0
	s_cmp_eq_u32 s16, 4
	v_mad_i32_i24 v132, v139, s4, v137
	s_mov_b32 s4, 0x8080
	s_cselect_b64 s[28:29], -1, 0
	v_and_or_b32 v132, v132, -13, v138
	v_cmp_gt_i32_e64 s[4:5], s4, v137
	v_bitop3_b32 v136, s25, 56, v191 bitop3:0xc8
	v_ashrrev_i32_e32 v133, 31, v132
	v_lshlrev_b32_e32 v140, 2, v139
	v_cvt_pk_bf16_f32 v126, v126, v127
	v_cvt_pk_bf16_f32 v127, v128, v129
	v_cvt_pk_bf16_f32 v128, v122, v123
	v_cvt_pk_bf16_f32 v129, v124, v125
	s_and_b64 s[30:31], s[4:5], s[28:29]
	global_store_dwordx4 v[134:135], v[126:129], off
	s_and_saveexec_b64 s[28:29], s[30:31]
	s_cbranch_execz .LBB0_132
	s_add_i32 s30, s25, 0xfffffc00
	s_lshr_b32 s30, s30, 6
	v_or_b32_e32 v122, s30, v140
	v_ashrrev_i32_e32 v124, 31, v122
	v_lshl_or_b32 v125, v122, 6, v136
	v_mov_b64_e32 v[122:123], s[20:21]
	s_movk_i32 s34, 0x2080
	v_mad_u64_u32 v[122:123], s[30:31], v125, s34, v[122:123]
	v_mad_i32_i24 v123, v124, s34, v123
	v_lshl_add_u64 v[122:123], v[132:133], 1, v[122:123]
	s_movk_i32 s30, 0x2000
	v_add_co_u32_e32 v124, vcc, s30, v122
	s_movk_i32 s30, 0x4000
	s_nop 0
	v_addc_co_u32_e32 v125, vcc, 0, v123, vcc
	global_store_short_d16_hi v[124:125], v126, off offset:128
	v_add_co_u32_e32 v124, vcc, s30, v122
	s_movk_i32 s30, 0x6000
	s_nop 0
	v_addc_co_u32_e32 v125, vcc, 0, v123, vcc
	global_store_short v[124:125], v127, off offset:256
	v_add_co_u32_e32 v124, vcc, s30, v122
	global_store_short v[122:123], v126, off
	s_nop 0
	v_addc_co_u32_e32 v125, vcc, 0, v123, vcc
	global_store_short_d16_hi v[124:125], v127, off offset:384
	v_add_co_u32_e32 v124, vcc, 0x8000, v122
	s_nop 1
	v_addc_co_u32_e32 v125, vcc, 0, v123, vcc
	global_store_short v[124:125], v128, off offset:512
	v_add_co_u32_e32 v124, vcc, 0xa000, v122
	s_nop 1
	v_addc_co_u32_e32 v125, vcc, 0, v123, vcc
	global_store_short_d16_hi v[124:125], v128, off offset:640
	v_add_co_u32_e32 v124, vcc, 0xc000, v122
	s_nop 1
	v_addc_co_u32_e32 v125, vcc, 0, v123, vcc
	v_add_co_u32_e32 v122, vcc, 0xe000, v122
	global_store_short v[124:125], v129, off offset:768
	s_nop 0
	v_addc_co_u32_e32 v123, vcc, 0, v123, vcc
	global_store_short_d16_hi v[122:123], v129, off offset:896

;     __device__ __forceinline__ const char* b_ptr(const Unit& u) const { return (const char*)Bt + ((size_t)u.pn * BM * K + u.koff) * 2; }
;     __device__ __forceinline__ const char* b_ptr(const Unit& u) const { return (const char*)Bt + ((size_t)u.e * bstride + (size_t)u.pn * BM * K) * 2; }
; template <class Epi, class Sched>
; __device__ __forceinline__ void gemm_phase(LAS unsigned char* lds, const bf16_t* Abase, const int K, const Sched& S, const Epi& E, const int wvid) {
;     ...
;         const bool has_next = S.next(ui + 1, nxt);
;         const char* nB = has_next ? S.b_ptr(nxt) : cB;
;         const int nt = cur.kt;
;         for (int t = 0; t < nt; t += 2) {
;             const bool last = (t == nt - 2);
;     ...
; #pragma unroll
;         for (int a = 0; a < 2; ++a)
; #pragma unroll
;             for (int b = 0; b < 2; ++b)
; #pragma unroll
;                 for (int m = 0; m < 4; ++m)
; #pragma unroll
;                     for (int n = 0; n < 2; ++n) acc[a][b][m][n] = (f32x4){0.f, 0.f, 0.f, 0.f};
;         cur = nxt; cB = nB; ++ui;
.LBB0_1001:
	s_ashr_i32 s11, s10, 31
	s_ashr_i32 s17, s16, 31
	s_xor_b64 s[20:21], s[24:25], -1
	s_lshl_b64 s[18:19], s[10:11], 19
	s_lshl_b64 s[28:29], s[16:17], 1
	s_add_u32 s11, s38, s18
	s_addc_u32 s17, s39, s19
	s_add_u32 s18, s11, s28
	s_addc_u32 s19, s17, s29
	s_and_b64 s[28:29], s[24:25], exec
	s_cselect_b32 s11, s19, s27
	s_cselect_b32 s17, s18, s26
	s_add_u32 s23, s26, 0x100
	v_mov_b32_e32 v2, 0
	s_addc_u32 s58, s27, 0
	s_add_i32 s59, s57, -2
	s_mov_b32 s60, 0
	s_mov_b64 s[26:27], 0
	v_mov_b32_e32 v3, v2
	v_mov_b32_e32 v4, v2
	v_mov_b32_e32 v5, v2
	v_mov_b32_e32 v6, v2
	v_mov_b32_e32 v7, v2
	v_mov_b32_e32 v8, v2
	v_mov_b32_e32 v9, v2
	v_mov_b32_e32 v10, v2
	v_mov_b32_e32 v11, v2
	v_mov_b32_e32 v12, v2
	v_mov_b32_e32 v13, v2
	v_mov_b32_e32 v14, v2
	v_mov_b32_e32 v15, v2
	v_mov_b32_e32 v16, v2
	v_mov_b32_e32 v17, v2
	v_mov_b32_e32 v22, v2
	v_mov_b32_e32 v23, v2
	v_mov_b32_e32 v24, v2
	v_mov_b32_e32 v25, v2
	v_mov_b32_e32 v30, v2
	v_mov_b32_e32 v31, v2
	v_mov_b32_e32 v32, v2
	v_mov_b32_e32 v33, v2
	v_mov_b32_e32 v38, v2
	v_mov_b32_e32 v39, v2
	v_mov_b32_e32 v40, v2
	v_mov_b32_e32 v41, v2
	v_mov_b32_e32 v46, v2
	v_mov_b32_e32 v47, v2
	v_mov_b32_e32 v48, v2
	v_mov_b32_e32 v49, v2
	v_mov_b32_e32 v18, v2
	v_mov_b32_e32 v19, v2
	v_mov_b32_e32 v20, v2
	v_mov_b32_e32 v21, v2
	v_mov_b32_e32 v26, v2
	v_mov_b32_e32 v27, v2
	v_mov_b32_e32 v28, v2
	v_mov_b32_e32 v29, v2
	v_mov_b32_e32 v34, v2
	v_mov_b32_e32 v35, v2
	v_mov_b32_e32 v36, v2
	v_mov_b32_e32 v37, v2
	v_mov_b32_e32 v42, v2
	v_mov_b32_e32 v43, v2
	v_mov_b32_e32 v44, v2
	v_mov_b32_e32 v45, v2
	v_mov_b32_e32 v50, v2
	v_mov_b32_e32 v51, v2
	v_mov_b32_e32 v52, v2
	v_mov_b32_e32 v53, v2
	v_mov_b32_e32 v54, v2
	v_mov_b32_e32 v55, v2
	v_mov_b32_e32 v56, v2
	v_mov_b32_e32 v57, v2
	v_mov_b32_e32 v58, v2
	v_mov_b32_e32 v59, v2
	v_mov_b32_e32 v60, v2
	v_mov_b32_e32 v61, v2
	v_mov_b32_e32 v62, v2
	v_mov_b32_e32 v63, v2
	v_mov_b32_e32 v64, v2
	v_mov_b32_e32 v65, v2
	v_mov_b32_e32 v66, v2
	v_mov_b32_e32 v67, v2
	s_waitcnt vmcnt(0)
	v_mov_b32_e32 v68, v2
	v_mov_b32_e32 v69, v2
	v_mov_b32_e32 v70, v2
	v_mov_b32_e32 v71, v2
	v_mov_b32_e32 v72, v2
	v_mov_b32_e32 v73, v2
	v_mov_b32_e32 v74, v2
	v_mov_b32_e32 v75, v2
	v_mov_b32_e32 v76, v2
	v_mov_b32_e32 v77, v2
	v_mov_b32_e32 v78, v2
	v_mov_b32_e32 v79, v2
	v_mov_b32_e32 v80, v2
	v_mov_b32_e32 v81, v2
	v_mov_b32_e32 v82, v2
	v_mov_b32_e32 v83, v2
	v_mov_b32_e32 v84, v2
	v_mov_b32_e32 v85, v2
	v_mov_b32_e32 v86, v2
	v_mov_b32_e32 v87, v2
	v_mov_b32_e32 v88, v2
	v_mov_b32_e32 v89, v2
	v_mov_b32_e32 v90, v2
	v_mov_b32_e32 v91, v2
	v_mov_b32_e32 v92, v2
	v_mov_b32_e32 v93, v2
	v_mov_b32_e32 v94, v2
	v_mov_b32_e32 v95, v2
	v_mov_b32_e32 v96, v2
	v_mov_b32_e32 v97, v2
	v_mov_b32_e32 v98, v2
	v_mov_b32_e32 v99, v2
	v_mov_b32_e32 v100, v2
	v_mov_b32_e32 v101, v2
	v_mov_b32_e32 v102, v2
	v_mov_b32_e32 v103, v2
	v_mov_b32_e32 v104, v2
	v_mov_b32_e32 v105, v2
	v_mov_b32_e32 v106, v2
	v_mov_b32_e32 v107, v2
	v_mov_b32_e32 v108, v2
	v_mov_b32_e32 v109, v2
	v_mov_b32_e32 v110, v2
	v_mov_b32_e32 v111, v2
	v_mov_b32_e32 v112, v2
	v_mov_b32_e32 v113, v2
	v_mov_b32_e32 v114, v2
	v_mov_b32_e32 v115, v2
	v_mov_b32_e32 v116, v2
	v_mov_b32_e32 v117, v2
	v_mov_b32_e32 v118, v2
	v_mov_b32_e32 v119, v2
	v_mov_b32_e32 v120, v2
	v_mov_b32_e32 v121, v2
	v_mov_b32_e32 v122, v2
	v_mov_b32_e32 v123, v2
	v_mov_b32_e32 v124, v2
	v_mov_b32_e32 v125, v2
	v_mov_b32_e32 v126, v2
	v_mov_b32_e32 v127, v2
	v_mov_b32_e32 v128, v2
	v_mov_b32_e32 v129, v2
	s_branch .LBB0_1002
.Lkhead1:
	s_barrier
; #define PG8_STAGE(bufoff, gbase, voff) do { _Pragma("unroll") for (int _i = 0; _i < 2; ++_i) \
;         __builtin_amdgcn_global_load_lds((const unsigned*)((const char*)(gbase) + (voff)[_i]), (LAS unsigned*)(lds + (bufoff) + ldsw + _i * 8192), 16, 0, 0); } while (0)
; #define PG8_LDA(dst, b, h) do { _Pragma("unroll") for (int m = 0; m < 4; ++m) _Pragma("unroll") for (int k = 0; k < 2; ++k) dst[m][k] = *(const LAS bf16x8*)(lds + PG8_SA(b, h) + aoff + m * 2048 + k * 1024); } while (0)
; #define PG8_LDB(dst, b, h) do { _Pragma("unroll") for (int n = 0; n < 2; ++n) _Pragma("unroll") for (int k = 0; k < 2; ++k) dst[n][k] = *(const LAS bf16x8*)(lds + PG8_SB(b, h) + boff + n * 2048 + k * 1024); } while (0)
; #define PG8_MMA(ai, bj, At, Bt) do { __builtin_amdgcn_s_setprio(1); _Pragma("unroll") for (int m = 0; m < 4; ++m) _Pragma("unroll") for (int n = 0; n < 2; ++n) _Pragma("unroll") for (int k = 0; k < 2; ++k) \
;         acc[ai][bj][m][n] = __builtin_amdgcn_mfma_f32_16x16x32_bf16(Bt[n][k], At[m][k], acc[ai][bj][m][n], 0, 0, 0); __builtin_amdgcn_s_setprio(0); } while (0)
; #define PG8_WAIT_L(n) asm volatile("s_waitcnt lgkmcnt(" #n ")" ::: "memory")
; #define PG8_BAR __builtin_amdgcn_s_barrier()
; #define PG8_SCHED __builtin_amdgcn_sched_barrier(0)
; #define PG8_AOFF(u) do { const int _t = lt_tid(wvid); _Pragma("unroll") for (int _i = 0; _i < 2; ++_i) { int _R, _C; stage_rc(_t * 16 + _i * 8192, _R, _C); \
;         _Pragma("unroll") for (int _h = 0; _h < 2; ++_h) voffA[_h][_i] = (S.a_row(u, _h * HALF + _R) * (unsigned)K + (unsigned)(_C + (u).koff)) * 2u; } } while (0)
; template <class Epi, class Sched>
; __device__ __forceinline__ void gemm_phase(LAS unsigned char* lds, const bf16_t* Abase, const int K, const Sched& S, const Epi& E, const int wvid) {
;     ...
;             PG8_LDB(B0, 0, 0); PG8_SCHED; PG8_LDA(At, 0, 0); PG8_STAGE(PG8_SA(1, 1), a1, voffA[1]);
;             PG8_WAIT_L(8); PG8_BAR; PG8_WAIT_L(0); PG8_MMA(0, 0, At, B0); PG8_BAR; PG8_SCHED;
;             if (last && has_next) PG8_AOFF(nxt);
.LBB0_1002:
	v_add_u32_e32 v130, 0, v194
	v_add_u32_e32 v142, 0x10000, v130
	ds_read_b128 v[130:133], v142
	ds_read_b128 v[134:137], v142 offset:1024
	ds_read_b128 v[138:141], v142 offset:2048
	ds_read_b128 v[142:145], v142 offset:3072
	s_cmp_eq_u32 s59, s60
	s_cselect_b64 s[30:31], -1, 0
	s_add_i32 m0, s42, 0xc000
	s_add_u32 s28, s6, s26
	s_addc_u32 s29, s7, s27
	ds_read_b128 v[170:173], v195
	ds_read_b128 v[174:177], v195 offset:1024
	ds_read_b128 v[162:165], v195 offset:2048
	ds_read_b128 v[166:169], v195 offset:3072
	ds_read_b128 v[154:157], v195 offset:4096
	ds_read_b128 v[158:161], v195 offset:5120
	ds_read_b128 v[146:149], v195 offset:6144
	ds_read_b128 v[150:153], v195 offset:7168
	global_load_lds_dwordx4 v182, s[28:29]
	s_add_i32 m0, s42, 0xe000
	s_nop 0
	global_load_lds_dwordx4 v186, s[28:29]
	s_waitcnt lgkmcnt(8)
	s_barrier
	s_waitcnt lgkmcnt(0)
	s_waitcnt lgkmcnt(0)
	v_mfma_f32_16x16x32_bf16 v[126:129], v[130:133], v[170:173], v[126:129]
	v_mfma_f32_16x16x32_bf16 v[122:125], v[138:141], v[170:173], v[122:125]
	v_mfma_f32_16x16x32_bf16 v[118:121], v[130:133], v[162:165], v[118:121]
	v_mfma_f32_16x16x32_bf16 v[114:117], v[138:141], v[162:165], v[114:117]
	v_mfma_f32_16x16x32_bf16 v[110:113], v[130:133], v[154:157], v[110:113]
	v_mfma_f32_16x16x32_bf16 v[106:109], v[138:141], v[154:157], v[106:109]
	v_mfma_f32_16x16x32_bf16 v[102:105], v[130:133], v[146:149], v[102:105]
	v_mfma_f32_16x16x32_bf16 v[98:101], v[138:141], v[146:149], v[98:101]
	v_mfma_f32_16x16x32_bf16 v[126:129], v[134:137], v[174:177], v[126:129]
	v_mfma_f32_16x16x32_bf16 v[122:125], v[142:145], v[174:177], v[122:125]
	v_mfma_f32_16x16x32_bf16 v[118:121], v[134:137], v[166:169], v[118:121]
	v_mfma_f32_16x16x32_bf16 v[114:117], v[142:145], v[166:169], v[114:117]
	v_mfma_f32_16x16x32_bf16 v[110:113], v[134:137], v[158:161], v[110:113]
	v_mfma_f32_16x16x32_bf16 v[106:109], v[142:145], v[158:161], v[106:109]
	v_mfma_f32_16x16x32_bf16 v[102:105], v[134:137], v[150:153], v[102:105]
	v_mfma_f32_16x16x32_bf16 v[98:101], v[142:145], v[150:153], v[98:101]
	s_barrier
	s_and_b64 s[28:29], s[24:25], s[30:31]
	s_andn2_b64 vcc, exec, s[28:29]
	s_cbranch_vccnz .LBB0_1004
	v_mbcnt_lo_u32_b32 v0, -1, 0
	v_mbcnt_hi_u32_b32 v0, -1, v0
	s_nop 0
	v_or_b32_e32 v0, s75, v0
	v_ashrrev_i32_e32 v183, 31, v0
	v_lshrrev_b32_e32 v183, 26, v183
	v_lshlrev_b32_e32 v182, 4, v0
	v_add_u32_e32 v183, v0, v183
	v_bfe_i32 v0, v0, 27, 1
	v_lshrrev_b32_e32 v0, 22, v0
	v_add_u32_e32 v0, v182, v0
	v_and_b32_e32 v0, 0xfffffc00, v0
	v_sub_u32_e32 v0, v182, v0
	v_lshrrev_b32_e32 v184, 4, v0
	v_bitop3_b32 v0, v184, v0, 32 bitop3:0x6c
	v_ashrrev_i32_e32 v185, 31, v0
	v_lshrrev_b32_e32 v185, 26, v185
	v_add_u32_e32 v185, v0, v185
	v_ashrrev_i32_e32 v183, 6, v183
	v_lshrrev_b32_e32 v186, 6, v185
	v_and_b32_e32 v185, 0xc0, v185
	v_lshlrev_b32_e32 v184, 3, v183
	v_sub_u32_e32 v0, v0, v185
	v_and_b32_e32 v184, 0x1ffff0, v184
	v_lshlrev_b32_e32 v183, 5, v183
	v_ashrrev_i16_sdwa v0, v216, sext(v0) dst_sel:DWORD dst_unused:UNUSED_PAD src0_sel:DWORD src1_sel:BYTE_0
	v_and_b32_e32 v183, 32, v183
	v_bfe_i32 v0, v0, 0, 16
	v_add_u32_e32 v184, s55, v184
	v_add_u32_e32 v182, 0x2000, v182
	v_add3_u32 v0, v183, s16, v0
	v_add_lshl_u32 v183, v184, v186, 11
	v_ashrrev_i32_e32 v184, 31, v182
	v_lshrrev_b32_e32 v184, 22, v184
	v_add_u32_e32 v184, v182, v184
	v_ashrrev_i32_e32 v184, 10, v184
	v_mul_i32_i24_e32 v185, 0x400, v184
	v_sub_u32_e32 v182, v182, v185
	v_lshrrev_b32_e32 v185, 4, v182
	v_bitop3_b32 v182, v185, v182, 32 bitop3:0x6c
	v_ashrrev_i32_e32 v186, 31, v182
	v_lshrrev_b32_e32 v186, 26, v186
	v_add_u32_e32 v186, v182, v186
	v_lshrrev_b32_e32 v187, 6, v186
	v_and_b32_e32 v186, 0xc0, v186
	v_lshlrev_b32_e32 v185, 3, v184
	v_sub_u32_e32 v182, v182, v186
	v_and_b32_e32 v185, 0x1ffff0, v185
	v_lshlrev_b32_e32 v184, 5, v184
	v_ashrrev_i16_sdwa v182, v216, sext(v182) dst_sel:DWORD dst_unused:UNUSED_PAD src0_sel:DWORD src1_sel:BYTE_0
	v_and_b32_e32 v184, 32, v184
	v_bfe_i32 v182, v182, 0, 16
	v_add_u32_e32 v185, s55, v185
	v_lshl_add_u32 v183, v0, 1, v183
	v_add3_u32 v182, v184, s16, v182
	v_add_lshl_u32 v184, v185, v187, 11
	v_add_u32_e32 v0, 0x40000, v183
	v_lshl_add_u32 v184, v182, 1, v184
	v_add_u32_e32 v186, 0x40000, v184
	v_mov_b32_e32 v187, v1
	v_mov_b64_e32 v[192:193], v[0:1]
	v_mov_b32_e32 v182, v0
	v_mov_b32_e32 v0, v183
	s_branch .LBB0_1005

; #define PG8_STAGE(bufoff, gbase, voff) do { _Pragma("unroll") for (int _i = 0; _i < 2; ++_i) \
;         __builtin_amdgcn_global_load_lds((const unsigned*)((const char*)(gbase) + (voff)[_i]), (LAS unsigned*)(lds + (bufoff) + ldsw + _i * 8192), 16, 0, 0); } while (0)
; #define PG8_LDA(dst, b, h) do { _Pragma("unroll") for (int m = 0; m < 4; ++m) _Pragma("unroll") for (int k = 0; k < 2; ++k) dst[m][k] = *(const LAS bf16x8*)(lds + PG8_SA(b, h) + aoff + m * 2048 + k * 1024); } while (0)
; #define PG8_LDB(dst, b, h) do { _Pragma("unroll") for (int n = 0; n < 2; ++n) _Pragma("unroll") for (int k = 0; k < 2; ++k) dst[n][k] = *(const LAS bf16x8*)(lds + PG8_SB(b, h) + boff + n * 2048 + k * 1024); } while (0)
; #define PG8_MMA(ai, bj, At, Bt) do { __builtin_amdgcn_s_setprio(1); _Pragma("unroll") for (int m = 0; m < 4; ++m) _Pragma("unroll") for (int n = 0; n < 2; ++n) _Pragma("unroll") for (int k = 0; k < 2; ++k) \
;         acc[ai][bj][m][n] = __builtin_amdgcn_mfma_f32_16x16x32_bf16(Bt[n][k], At[m][k], acc[ai][bj][m][n], 0, 0, 0); __builtin_amdgcn_s_setprio(0); } while (0)
; #define PG8_WAIT_V(n) asm volatile("s_waitcnt vmcnt(" #n ")" ::: "memory")
; #define PG8_WAIT_L(n) asm volatile("s_waitcnt lgkmcnt(" #n ")" ::: "memory")
; #define PG8_BAR __builtin_amdgcn_s_barrier()
; #define PG8_SCHED __builtin_amdgcn_sched_barrier(0)
; template <class Epi, class Sched>
; __device__ __forceinline__ void gemm_phase(LAS unsigned char* lds, const bf16_t* Abase, const int K, const Sched& S, const Epi& E, const int wvid) {
;     ...
;             const char* a2 = last ? Ab : Ab + (size_t)(t + 2) * kstep; const char* b2 = last ? nB : cB + (size_t)(t + 2) * kstep;
;             const char* a3 = a2 + kstep; const char* b3 = b2 + kstep;
;             PG8_LDB(B1, 0, 1); PG8_STAGE(PG8_SB(0, 0), b2, voffB);
;             PG8_BAR; PG8_WAIT_L(0); PG8_MMA(0, 1, At, B1); PG8_BAR;
;             PG8_LDA(At, 0, 1); PG8_STAGE(PG8_SA(0, 0), a2, voffA[0]);
;             PG8_BAR; PG8_WAIT_L(0); PG8_MMA(1, 0, At, B0); PG8_BAR; PG8_SCHED;
;             PG8_STAGE(PG8_SB(0, 1), b2 + hstep, voffB);
;             PG8_WAIT_V(6); PG8_BAR; PG8_MMA(1, 1, At, B1); PG8_BAR;
;             PG8_LDB(B0, 1, 0); PG8_SCHED; PG8_LDA(At, 1, 0); PG8_STAGE(PG8_SA(0, 1), a2, voffA[1]);
.LBB0_1005:
	s_add_i32 s60, s60, 2
	s_add_u32 s28, s26, 0x100
	s_addc_u32 s29, s27, 0
	s_and_b64 s[34:35], s[30:31], exec
	s_cselect_b32 s34, 0, s28
	s_cselect_b32 s35, 0, s29
	s_add_u32 s34, s0, s34
	s_addc_u32 s35, s1, s35
	s_add_u32 s61, s23, s26
	s_addc_u32 s62, s58, s27
	s_add_i32 s63, 0, 0x14000
	s_and_b64 s[26:27], s[30:31], exec
	s_cselect_b32 s27, s11, s62
	s_cselect_b32 s26, s17, s61
	s_mov_b32 m0, s43
	v_add_u32_e32 v183, s63, v194
	v_lshl_add_u64 v[224:225], s[26:27], 0, v[178:179]
	ds_read_b128 v[196:199], v183
	ds_read_b128 v[200:203], v183 offset:1024
	ds_read_b128 v[206:209], v183 offset:2048
	ds_read_b128 v[210:213], v183 offset:3072
	global_load_lds_dwordx4 v[224:225], off
	v_lshl_add_u64 v[226:227], s[26:27], 0, v[180:181]
	s_mov_b32 m0, s46
	s_nop 0
	global_load_lds_dwordx4 v[226:227], off
	s_barrier
	s_waitcnt lgkmcnt(0)
	s_waitcnt lgkmcnt(0)
	v_mfma_f32_16x16x32_bf16 v[94:97], v[196:199], v[170:173], v[94:97]
	v_mfma_f32_16x16x32_bf16 v[90:93], v[206:209], v[170:173], v[90:93]
	v_mfma_f32_16x16x32_bf16 v[86:89], v[196:199], v[162:165], v[86:89]
	v_mfma_f32_16x16x32_bf16 v[82:85], v[206:209], v[162:165], v[82:85]
	v_mfma_f32_16x16x32_bf16 v[78:81], v[196:199], v[154:157], v[78:81]
	v_mfma_f32_16x16x32_bf16 v[74:77], v[206:209], v[154:157], v[74:77]
	v_mfma_f32_16x16x32_bf16 v[70:73], v[196:199], v[146:149], v[70:73]
	v_mfma_f32_16x16x32_bf16 v[66:69], v[206:209], v[146:149], v[66:69]
	v_mfma_f32_16x16x32_bf16 v[94:97], v[200:203], v[174:177], v[94:97]
	v_mfma_f32_16x16x32_bf16 v[90:93], v[210:213], v[174:177], v[90:93]
	v_mfma_f32_16x16x32_bf16 v[86:89], v[200:203], v[166:169], v[86:89]
	v_mfma_f32_16x16x32_bf16 v[82:85], v[210:213], v[166:169], v[82:85]
	v_mfma_f32_16x16x32_bf16 v[78:81], v[200:203], v[158:161], v[78:81]
	v_mfma_f32_16x16x32_bf16 v[74:77], v[210:213], v[158:161], v[74:77]
	v_mfma_f32_16x16x32_bf16 v[70:73], v[200:203], v[150:153], v[70:73]
	v_mfma_f32_16x16x32_bf16 v[66:69], v[210:213], v[150:153], v[66:69]
	s_mov_b32 m0, s42
	s_barrier
	ds_read_b128 v[146:149], v195 offset:16384
	ds_read_b128 v[150:153], v195 offset:17408
	ds_read_b128 v[154:157], v195 offset:18432
	ds_read_b128 v[158:161], v195 offset:19456
	ds_read_b128 v[162:165], v195 offset:20480
	ds_read_b128 v[166:169], v195 offset:21504
	ds_read_b128 v[170:173], v195 offset:22528
	ds_read_b128 v[174:177], v195 offset:23552
	global_load_lds_dwordx4 v0, s[34:35]
	s_mov_b32 m0, s47
	v_mov_b32_e32 v185, v1
	global_load_lds_dwordx4 v184, s[34:35]
	s_barrier
	s_waitcnt lgkmcnt(0)
	v_lshl_add_u64 v[228:229], s[34:35], 0, v[0:1]
	v_lshl_add_u64 v[230:231], s[34:35], 0, v[184:185]
	s_waitcnt lgkmcnt(0)
	v_mfma_f32_16x16x32_bf16 v[62:65], v[130:133], v[146:149], v[62:65]
	v_mfma_f32_16x16x32_bf16 v[58:61], v[138:141], v[146:149], v[58:61]
	v_mfma_f32_16x16x32_bf16 v[54:57], v[130:133], v[154:157], v[54:57]
	v_mfma_f32_16x16x32_bf16 v[50:53], v[138:141], v[154:157], v[50:53]
	v_mfma_f32_16x16x32_bf16 v[42:45], v[130:133], v[162:165], v[42:45]
	v_mfma_f32_16x16x32_bf16 v[34:37], v[138:141], v[162:165], v[34:37]
	v_mfma_f32_16x16x32_bf16 v[26:29], v[130:133], v[170:173], v[26:29]
	v_mfma_f32_16x16x32_bf16 v[18:21], v[138:141], v[170:173], v[18:21]
	v_mfma_f32_16x16x32_bf16 v[62:65], v[134:137], v[150:153], v[62:65]
	v_mfma_f32_16x16x32_bf16 v[58:61], v[142:145], v[150:153], v[58:61]
	v_mfma_f32_16x16x32_bf16 v[54:57], v[134:137], v[158:161], v[54:57]
	v_mfma_f32_16x16x32_bf16 v[50:53], v[142:145], v[158:161], v[50:53]
	v_mfma_f32_16x16x32_bf16 v[42:45], v[134:137], v[166:169], v[42:45]
	v_mfma_f32_16x16x32_bf16 v[34:37], v[142:145], v[166:169], v[34:37]
	v_mfma_f32_16x16x32_bf16 v[26:29], v[134:137], v[174:177], v[26:29]
	v_mfma_f32_16x16x32_bf16 v[18:21], v[142:145], v[174:177], v[18:21]
	s_barrier
	s_add_u32 s30, s26, 0x40000
	s_addc_u32 s31, s27, 0
	s_add_i32 s61, s63, s40
	v_lshl_add_u64 v[130:131], s[30:31], 0, v[178:179]
	s_mov_b32 m0, s61
	s_nop 0
	global_load_lds_dwordx4 v[130:131], off
	v_lshl_add_u64 v[130:131], s[30:31], 0, v[180:181]
	s_add_i32 m0, s61, 0x2000
	s_nop 0
	global_load_lds_dwordx4 v[130:131], off
	s_waitcnt vmcnt(6)
	s_barrier
	v_mfma_f32_16x16x32_bf16 v[46:49], v[196:199], v[146:149], v[46:49]
	v_mfma_f32_16x16x32_bf16 v[38:41], v[206:209], v[146:149], v[38:41]
	v_mfma_f32_16x16x32_bf16 v[30:33], v[196:199], v[154:157], v[30:33]
	v_mfma_f32_16x16x32_bf16 v[22:25], v[206:209], v[154:157], v[22:25]
	v_mfma_f32_16x16x32_bf16 v[14:17], v[196:199], v[162:165], v[14:17]
	v_mfma_f32_16x16x32_bf16 v[10:13], v[206:209], v[162:165], v[10:13]
	v_mfma_f32_16x16x32_bf16 v[6:9], v[196:199], v[170:173], v[6:9]
	v_mfma_f32_16x16x32_bf16 v[2:5], v[206:209], v[170:173], v[2:5]
	v_mfma_f32_16x16x32_bf16 v[46:49], v[200:203], v[150:153], v[46:49]
	v_mfma_f32_16x16x32_bf16 v[38:41], v[210:213], v[150:153], v[38:41]
	v_mfma_f32_16x16x32_bf16 v[30:33], v[200:203], v[158:161], v[30:33]
	v_mfma_f32_16x16x32_bf16 v[22:25], v[210:213], v[158:161], v[22:25]
	v_mfma_f32_16x16x32_bf16 v[14:17], v[200:203], v[166:169], v[14:17]
	v_mfma_f32_16x16x32_bf16 v[10:13], v[210:213], v[166:169], v[10:13]
	v_mfma_f32_16x16x32_bf16 v[6:9], v[200:203], v[174:177], v[6:9]
	v_mfma_f32_16x16x32_bf16 v[2:5], v[210:213], v[174:177], v[2:5]
	s_add_i32 s30, 0, 0x18000
	v_add_u32_e32 v142, s30, v194
	s_barrier
; #define PG8_STAGE(bufoff, gbase, voff) do { _Pragma("unroll") for (int _i = 0; _i < 2; ++_i) \
;         __builtin_amdgcn_global_load_lds((const unsigned*)((const char*)(gbase) + (voff)[_i]), (LAS unsigned*)(lds + (bufoff) + ldsw + _i * 8192), 16, 0, 0); } while (0)
; #define PG8_LDA(dst, b, h) do { _Pragma("unroll") for (int m = 0; m < 4; ++m) _Pragma("unroll") for (int k = 0; k < 2; ++k) dst[m][k] = *(const LAS bf16x8*)(lds + PG8_SA(b, h) + aoff + m * 2048 + k * 1024); } while (0)
; #define PG8_LDB(dst, b, h) do { _Pragma("unroll") for (int n = 0; n < 2; ++n) _Pragma("unroll") for (int k = 0; k < 2; ++k) dst[n][k] = *(const LAS bf16x8*)(lds + PG8_SB(b, h) + boff + n * 2048 + k * 1024); } while (0)
; #define PG8_MMA(ai, bj, At, Bt) do { __builtin_amdgcn_s_setprio(1); _Pragma("unroll") for (int m = 0; m < 4; ++m) _Pragma("unroll") for (int n = 0; n < 2; ++n) _Pragma("unroll") for (int k = 0; k < 2; ++k) \
;         acc[ai][bj][m][n] = __builtin_amdgcn_mfma_f32_16x16x32_bf16(Bt[n][k], At[m][k], acc[ai][bj][m][n], 0, 0, 0); __builtin_amdgcn_s_setprio(0); } while (0)
; #define PG8_WAIT_V(n) asm volatile("s_waitcnt vmcnt(" #n ")" ::: "memory")
; #define PG8_WAIT_L(n) asm volatile("s_waitcnt lgkmcnt(" #n ")" ::: "memory")
; #define PG8_BAR __builtin_amdgcn_s_barrier()
; #define PG8_SCHED __builtin_amdgcn_sched_barrier(0)
; template <class Epi, class Sched>
; __device__ __forceinline__ void gemm_phase(LAS unsigned char* lds, const bf16_t* Abase, const int K, const Sched& S, const Epi& E, const int wvid) {
;     ...
;             PG8_LDB(B0, 1, 0); PG8_SCHED; PG8_LDA(At, 1, 0); PG8_STAGE(PG8_SA(0, 1), a2, voffA[1]);
;             PG8_WAIT_L(8); PG8_BAR; PG8_WAIT_L(0); PG8_MMA(0, 0, At, B0); PG8_BAR; PG8_SCHED;
;             PG8_LDB(B1, 1, 1); PG8_STAGE(PG8_SB(1, 0), b3, voffB);
;             PG8_BAR; PG8_WAIT_L(0); PG8_MMA(0, 1, At, B1); PG8_BAR;
;             PG8_LDA(At, 1, 1); PG8_STAGE(PG8_SA(1, 0), a3, voffA[0]);
;             PG8_BAR; PG8_WAIT_L(0); PG8_MMA(1, 0, At, B0); PG8_BAR; PG8_SCHED;
;             PG8_STAGE(PG8_SB(1, 1), b3 + hstep, voffB);
;             PG8_WAIT_V(6); PG8_BAR; PG8_MMA(1, 1, At, B1); PG8_BAR;
;         }
	ds_read_b128 v[130:133], v142
	ds_read_b128 v[134:137], v142 offset:1024
	ds_read_b128 v[138:141], v142 offset:2048
	ds_read_b128 v[142:145], v142 offset:3072
	s_mov_b32 m0, s48
	v_lshl_add_u64 v[192:193], s[34:35], 0, v[192:193]
	ds_read_b128 v[146:149], v195 offset:32768
	ds_read_b128 v[150:153], v195 offset:33792
	ds_read_b128 v[154:157], v195 offset:34816
	ds_read_b128 v[158:161], v195 offset:35840
	ds_read_b128 v[162:165], v195 offset:36864
	ds_read_b128 v[166:169], v195 offset:37888
	ds_read_b128 v[170:173], v195 offset:38912
	ds_read_b128 v[174:177], v195 offset:39936
	global_load_lds_dwordx4 v[192:193], off
	v_lshl_add_u64 v[192:193], s[34:35], 0, v[186:187]
	s_mov_b32 m0, s49
	s_nop 0
	global_load_lds_dwordx4 v[192:193], off
	s_waitcnt lgkmcnt(8)
	s_barrier
	s_waitcnt lgkmcnt(0)
	s_waitcnt lgkmcnt(0)
	v_mfma_f32_16x16x32_bf16 v[126:129], v[130:133], v[146:149], v[126:129]
	v_mfma_f32_16x16x32_bf16 v[122:125], v[138:141], v[146:149], v[122:125]
	v_mfma_f32_16x16x32_bf16 v[118:121], v[130:133], v[154:157], v[118:121]
	v_mfma_f32_16x16x32_bf16 v[114:117], v[138:141], v[154:157], v[114:117]
	v_mfma_f32_16x16x32_bf16 v[110:113], v[130:133], v[162:165], v[110:113]
	v_mfma_f32_16x16x32_bf16 v[106:109], v[138:141], v[162:165], v[106:109]
	v_mfma_f32_16x16x32_bf16 v[102:105], v[130:133], v[170:173], v[102:105]
	v_mfma_f32_16x16x32_bf16 v[98:101], v[138:141], v[170:173], v[98:101]
	v_mfma_f32_16x16x32_bf16 v[126:129], v[134:137], v[150:153], v[126:129]
	v_mfma_f32_16x16x32_bf16 v[122:125], v[142:145], v[150:153], v[122:125]
	v_mfma_f32_16x16x32_bf16 v[118:121], v[134:137], v[158:161], v[118:121]
	v_mfma_f32_16x16x32_bf16 v[114:117], v[142:145], v[158:161], v[114:117]
	v_mfma_f32_16x16x32_bf16 v[110:113], v[134:137], v[166:169], v[110:113]
	v_mfma_f32_16x16x32_bf16 v[106:109], v[142:145], v[166:169], v[106:109]
	v_mfma_f32_16x16x32_bf16 v[102:105], v[134:137], v[174:177], v[102:105]
	v_mfma_f32_16x16x32_bf16 v[98:101], v[142:145], v[174:177], v[98:101]
	s_barrier
	s_add_i32 s31, 0, 0x1c000
	s_add_i32 s30, s30, s40
	v_add_u32_e32 v183, s31, v194
	v_lshl_add_u64 v[192:193], v[224:225], 0, s[12:13]
	s_mov_b32 m0, s30
	ds_read_b128 v[196:199], v183
	ds_read_b128 v[200:203], v183 offset:1024
	ds_read_b128 v[206:209], v183 offset:2048
	ds_read_b128 v[210:213], v183 offset:3072
	global_load_lds_dwordx4 v[192:193], off
	v_lshl_add_u64 v[192:193], v[226:227], 0, s[12:13]
	s_add_i32 m0, s30, 0x2000
	s_nop 0
	global_load_lds_dwordx4 v[192:193], off
	s_barrier
	s_waitcnt lgkmcnt(0)
	s_waitcnt lgkmcnt(0)
	v_mfma_f32_16x16x32_bf16 v[94:97], v[196:199], v[146:149], v[94:97]
	v_mfma_f32_16x16x32_bf16 v[90:93], v[206:209], v[146:149], v[90:93]
	v_mfma_f32_16x16x32_bf16 v[86:89], v[196:199], v[154:157], v[86:89]
	v_mfma_f32_16x16x32_bf16 v[82:85], v[206:209], v[154:157], v[82:85]
	v_mfma_f32_16x16x32_bf16 v[78:81], v[196:199], v[162:165], v[78:81]
	v_mfma_f32_16x16x32_bf16 v[74:77], v[206:209], v[162:165], v[74:77]
	v_mfma_f32_16x16x32_bf16 v[70:73], v[196:199], v[170:173], v[70:73]
	v_mfma_f32_16x16x32_bf16 v[66:69], v[206:209], v[170:173], v[66:69]
	v_mfma_f32_16x16x32_bf16 v[94:97], v[200:203], v[150:153], v[94:97]
	v_mfma_f32_16x16x32_bf16 v[90:93], v[210:213], v[150:153], v[90:93]
	v_mfma_f32_16x16x32_bf16 v[86:89], v[200:203], v[158:161], v[86:89]
	v_mfma_f32_16x16x32_bf16 v[82:85], v[210:213], v[158:161], v[82:85]
	v_mfma_f32_16x16x32_bf16 v[78:81], v[200:203], v[166:169], v[78:81]
	v_mfma_f32_16x16x32_bf16 v[74:77], v[210:213], v[166:169], v[74:77]
	v_mfma_f32_16x16x32_bf16 v[70:73], v[200:203], v[174:177], v[70:73]
	v_mfma_f32_16x16x32_bf16 v[66:69], v[210:213], v[174:177], v[66:69]
	s_mov_b32 m0, s51
	v_lshl_add_u64 v[192:193], v[228:229], 0, s[12:13]
	s_barrier
	ds_read_b128 v[146:149], v195 offset:49152
	ds_read_b128 v[150:153], v195 offset:50176
	ds_read_b128 v[154:157], v195 offset:51200
	ds_read_b128 v[158:161], v195 offset:52224
	ds_read_b128 v[162:165], v195 offset:53248
	ds_read_b128 v[166:169], v195 offset:54272
	ds_read_b128 v[170:173], v195 offset:55296
	ds_read_b128 v[174:177], v195 offset:56320
	global_load_lds_dwordx4 v[192:193], off
	v_lshl_add_u64 v[192:193], v[230:231], 0, s[12:13]
	s_mov_b32 m0, s52
	s_nop 0
	global_load_lds_dwordx4 v[192:193], off
	s_barrier
	s_waitcnt lgkmcnt(0)
	s_waitcnt lgkmcnt(0)
	v_mfma_f32_16x16x32_bf16 v[62:65], v[130:133], v[146:149], v[62:65]
	v_mfma_f32_16x16x32_bf16 v[58:61], v[138:141], v[146:149], v[58:61]
	v_mfma_f32_16x16x32_bf16 v[54:57], v[130:133], v[154:157], v[54:57]
	v_mfma_f32_16x16x32_bf16 v[50:53], v[138:141], v[154:157], v[50:53]
	v_mfma_f32_16x16x32_bf16 v[42:45], v[130:133], v[162:165], v[42:45]
	v_mfma_f32_16x16x32_bf16 v[34:37], v[138:141], v[162:165], v[34:37]
	v_mfma_f32_16x16x32_bf16 v[26:29], v[130:133], v[170:173], v[26:29]
	v_mfma_f32_16x16x32_bf16 v[18:21], v[138:141], v[170:173], v[18:21]
	v_mfma_f32_16x16x32_bf16 v[62:65], v[134:137], v[150:153], v[62:65]
	v_mfma_f32_16x16x32_bf16 v[58:61], v[142:145], v[150:153], v[58:61]
	v_mfma_f32_16x16x32_bf16 v[54:57], v[134:137], v[158:161], v[54:57]
	v_mfma_f32_16x16x32_bf16 v[50:53], v[142:145], v[158:161], v[50:53]
	v_mfma_f32_16x16x32_bf16 v[42:45], v[134:137], v[166:169], v[42:45]
	v_mfma_f32_16x16x32_bf16 v[34:37], v[142:145], v[166:169], v[34:37]
	v_mfma_f32_16x16x32_bf16 v[26:29], v[134:137], v[174:177], v[26:29]
	v_mfma_f32_16x16x32_bf16 v[18:21], v[142:145], v[174:177], v[18:21]
	s_barrier
	s_add_u32 s26, s26, 0x40080
	s_addc_u32 s27, s27, 0
	s_add_i32 s30, s31, s40
	v_lshl_add_u64 v[130:131], s[26:27], 0, v[178:179]
	s_mov_b32 m0, s30
	s_nop 0
	global_load_lds_dwordx4 v[130:131], off
	v_lshl_add_u64 v[130:131], s[26:27], 0, v[180:181]
	s_add_i32 m0, s30, 0x2000
	s_nop 0
	global_load_lds_dwordx4 v[130:131], off
	s_waitcnt vmcnt(6)
	s_barrier
	v_mfma_f32_16x16x32_bf16 v[46:49], v[196:199], v[146:149], v[46:49]
	v_mfma_f32_16x16x32_bf16 v[38:41], v[206:209], v[146:149], v[38:41]
	v_mfma_f32_16x16x32_bf16 v[30:33], v[196:199], v[154:157], v[30:33]
	v_mfma_f32_16x16x32_bf16 v[22:25], v[206:209], v[154:157], v[22:25]
	v_mfma_f32_16x16x32_bf16 v[14:17], v[196:199], v[162:165], v[14:17]
	v_mfma_f32_16x16x32_bf16 v[10:13], v[206:209], v[162:165], v[10:13]
	v_mfma_f32_16x16x32_bf16 v[6:9], v[196:199], v[170:173], v[6:9]
	v_mfma_f32_16x16x32_bf16 v[2:5], v[206:209], v[170:173], v[2:5]
	v_mfma_f32_16x16x32_bf16 v[46:49], v[200:203], v[150:153], v[46:49]
	v_mfma_f32_16x16x32_bf16 v[38:41], v[210:213], v[150:153], v[38:41]
	v_mfma_f32_16x16x32_bf16 v[30:33], v[200:203], v[158:161], v[30:33]
	v_mfma_f32_16x16x32_bf16 v[22:25], v[210:213], v[158:161], v[22:25]
	v_mfma_f32_16x16x32_bf16 v[14:17], v[200:203], v[166:169], v[14:17]
	v_mfma_f32_16x16x32_bf16 v[10:13], v[210:213], v[166:169], v[10:13]
	v_mfma_f32_16x16x32_bf16 v[6:9], v[200:203], v[174:177], v[6:9]
	v_mfma_f32_16x16x32_bf16 v[2:5], v[210:213], v[174:177], v[2:5]
	s_cmp_ge_i32 s60, s57
	s_cbranch_scc1 .Lkexit1
	s_mov_b64 s[26:27], s[28:29]
	s_branch .Lkhead1
; __device__ __forceinline__ float bflo(unsigned w) { return __uint_as_float(w << 16); }
; __device__ __forceinline__ float bfhi(unsigned w) { return __uint_as_float(w & 0xFFFF0000u); }
; __device__ __forceinline__ unsigned cvt_pk_bf16(float lo, float hi) { f32x2c v = {lo, hi}; bf16x2c b = __builtin_convertvector(v, bf16x2c); return __builtin_bit_cast(unsigned, b); }
;     __device__ __forceinline__ void operator()(const f32x4 (&acc)[2][2][4][2], const Unit& u, int wr, int wc, int fr, int fq) const {
;     ...
;         if (u.kt * BK < Kfull) {
;             float* zp = ZP + ((size_t)u.e * BM + (wr * 64 + fr)) * D + col0;
; #pragma unroll
;             for (int ai = 0; ai < 2; ++ai)
; #pragma unroll
;                 for (int m = 0; m < 4; ++m)
; #pragma unroll
;                     for (int bj = 0; bj < 2; ++bj) { float* q = zp + (size_t)(ai * HALF + m * 16) * D + bj * HALF; *(f32x4*)q = acc[ai][bj][m][0]; *(f32x4*)(q + 4) = acc[ai][bj][m][1]; }
;             return;
;         }
; #pragma unroll
;         for (int ai = 0; ai < 2; ++ai)
; #pragma unroll
;             for (int m = 0; m < 4; ++m) { const size_t ro = (size_t)(row0 + ai * HALF + m * 16) * D + col0;
; #pragma unroll
;                 for (int bj = 0; bj < 2; ++bj) { const u32x4 h = *(const u32x4*)(hb + ro + bj * HALF); const f32x4 v0 = acc[ai][bj][m][0], v1 = acc[ai][bj][m][1];
;                     u32x4 w; w.x = cvt_pk_bf16(v0[0] + ALPHA * bflo(h.x), v0[1] + ALPHA * bfhi(h.x)); w.y = cvt_pk_bf16(v0[2] + ALPHA * bflo(h.y), v0[3] + ALPHA * bfhi(h.y));
;                     w.z = cvt_pk_bf16(v1[0] + ALPHA * bflo(h.z), v1[1] + ALPHA * bfhi(h.z)); w.w = cvt_pk_bf16(v1[2] + ALPHA * bflo(h.w), v1[3] + ALPHA * bfhi(h.w));
;                     *(u32x4*)(Z + ro + bj * HALF) = w; } }
.Lkexit1:
	s_barrier
.LBB0_1007:
	v_lshl_or_b32 v130, s22, 8, v189
	s_mov_b64 s[22:23], -1
	s_cmp_lt_i32 s57, 16
	v_ashrrev_i32_e32 v131, 31, v130
	s_cbranch_scc1 .LBB0_1009
	v_add_u32_e32 v132, s9, v188
	v_ashrrev_i32_e32 v133, 31, v132
	v_lshlrev_b64 v[132:133], 10, v[132:133]
	v_lshl_add_u64 v[132:133], v[132:133], 0, v[130:131]
	v_lshlrev_b64 v[132:133], 1, v[132:133]
	v_lshl_add_u64 v[138:139], s[4:5], 0, v[132:133]
	v_lshl_add_u64 v[140:141], s[2:3], 0, v[132:133]
	v_mov_b64_e32 v[142:143], v[138:139]
	global_load_dwordx4 v[144:147], v[142:143], off
	global_load_dwordx4 v[148:151], v[142:143], off offset:256
	v_add_co_u32_e32 v142, vcc, 0x8000, v142
	s_nop 1
	v_addc_co_u32_e32 v143, vcc, 0, v143, vcc
	global_load_dwordx4 v[152:155], v[142:143], off
	global_load_dwordx4 v[156:159], v[142:143], off offset:256
	v_add_co_u32_e32 v142, vcc, 0x8000, v142
	s_nop 1
	v_addc_co_u32_e32 v143, vcc, 0, v143, vcc
	global_load_dwordx4 v[160:163], v[142:143], off
	global_load_dwordx4 v[164:167], v[142:143], off offset:256
	v_add_co_u32_e32 v142, vcc, 0x8000, v142
	s_nop 1
	v_addc_co_u32_e32 v143, vcc, 0, v143, vcc
	global_load_dwordx4 v[168:171], v[142:143], off
	global_load_dwordx4 v[172:175], v[142:143], off offset:256
	v_add_co_u32_e32 v142, vcc, 0x28000, v142
	s_nop 1
	v_addc_co_u32_e32 v143, vcc, 0, v143, vcc
	s_waitcnt vmcnt(7)
	v_lshlrev_b32_e32 v134, 16, v144
	v_and_b32_e32 v135, 0xffff0000, v144
	v_pk_fma_f32 v[134:135], v[134:135], s[88:89], v[126:127] op_sel_hi:[1,0,1]
	s_nop 0
	v_cvt_pk_bf16_f32 v144, v134, v135
	v_lshlrev_b32_e32 v134, 16, v145
	v_and_b32_e32 v135, 0xffff0000, v145
	v_pk_fma_f32 v[134:135], v[134:135], s[88:89], v[128:129] op_sel_hi:[1,0,1]
	s_nop 0
	v_cvt_pk_bf16_f32 v145, v134, v135
	v_lshlrev_b32_e32 v134, 16, v146
	v_and_b32_e32 v135, 0xffff0000, v146
	v_pk_fma_f32 v[134:135], v[134:135], s[88:89], v[122:123] op_sel_hi:[1,0,1]
	s_nop 0
	v_cvt_pk_bf16_f32 v146, v134, v135
	v_lshlrev_b32_e32 v134, 16, v147
	v_and_b32_e32 v135, 0xffff0000, v147
	v_pk_fma_f32 v[134:135], v[134:135], s[88:89], v[124:125] op_sel_hi:[1,0,1]
	s_nop 0
	v_cvt_pk_bf16_f32 v147, v134, v135
	global_store_dwordx4 v[140:141], v[144:147], off
	s_nop 1
	global_load_dwordx4 v[144:147], v[142:143], off
	s_waitcnt vmcnt(8)
	v_lshlrev_b32_e32 v134, 16, v148
	v_and_b32_e32 v135, 0xffff0000, v148
	v_pk_fma_f32 v[134:135], v[134:135], s[88:89], v[94:95] op_sel_hi:[1,0,1]
	s_nop 0
	v_cvt_pk_bf16_f32 v148, v134, v135
	v_lshlrev_b32_e32 v134, 16, v149
	v_and_b32_e32 v135, 0xffff0000, v149
	v_pk_fma_f32 v[134:135], v[134:135], s[88:89], v[96:97] op_sel_hi:[1,0,1]
	s_nop 0
	v_cvt_pk_bf16_f32 v149, v134, v135
	v_lshlrev_b32_e32 v134, 16, v150
	v_and_b32_e32 v135, 0xffff0000, v150
	v_pk_fma_f32 v[134:135], v[134:135], s[88:89], v[90:91] op_sel_hi:[1,0,1]
	s_nop 0
	v_cvt_pk_bf16_f32 v150, v134, v135
	v_lshlrev_b32_e32 v134, 16, v151
	v_and_b32_e32 v135, 0xffff0000, v151
	v_pk_fma_f32 v[134:135], v[134:135], s[88:89], v[92:93] op_sel_hi:[1,0,1]
	s_nop 0
	v_cvt_pk_bf16_f32 v151, v134, v135
	global_store_dwordx4 v[140:141], v[148:151], off offset:256
	v_add_co_u32_e32 v140, vcc, 0x8000, v140
	s_nop 1
	v_addc_co_u32_e32 v141, vcc, 0, v141, vcc
	global_load_dwordx4 v[148:151], v[142:143], off offset:256
	v_add_co_u32_e32 v142, vcc, 0x8000, v142
	s_nop 1
	v_addc_co_u32_e32 v143, vcc, 0, v143, vcc
	s_waitcnt vmcnt(9)
	v_lshlrev_b32_e32 v134, 16, v152
	v_and_b32_e32 v135, 0xffff0000, v152
	v_pk_fma_f32 v[134:135], v[134:135], s[88:89], v[118:119] op_sel_hi:[1,0,1]
	s_nop 0
	v_cvt_pk_bf16_f32 v152, v134, v135
	v_lshlrev_b32_e32 v134, 16, v153
	v_and_b32_e32 v135, 0xffff0000, v153
	v_pk_fma_f32 v[134:135], v[134:135], s[88:89], v[120:121] op_sel_hi:[1,0,1]
	s_nop 0
	v_cvt_pk_bf16_f32 v153, v134, v135
	v_lshlrev_b32_e32 v134, 16, v154
	v_and_b32_e32 v135, 0xffff0000, v154
	v_pk_fma_f32 v[134:135], v[134:135], s[88:89], v[114:115] op_sel_hi:[1,0,1]
	s_nop 0
	v_cvt_pk_bf16_f32 v154, v134, v135
	v_lshlrev_b32_e32 v134, 16, v155
	v_and_b32_e32 v135, 0xffff0000, v155
	v_pk_fma_f32 v[134:135], v[134:135], s[88:89], v[116:117] op_sel_hi:[1,0,1]
	s_nop 0
	v_cvt_pk_bf16_f32 v155, v134, v135
	global_store_dwordx4 v[140:141], v[152:155], off
	s_nop 1
	global_load_dwordx4 v[152:155], v[142:143], off
	s_waitcnt vmcnt(10)
	v_lshlrev_b32_e32 v134, 16, v156
	v_and_b32_e32 v135, 0xffff0000, v156
	v_pk_fma_f32 v[134:135], v[134:135], s[88:89], v[86:87] op_sel_hi:[1,0,1]
	s_nop 0
	v_cvt_pk_bf16_f32 v156, v134, v135
	v_lshlrev_b32_e32 v134, 16, v157
	v_and_b32_e32 v135, 0xffff0000, v157
	v_pk_fma_f32 v[134:135], v[134:135], s[88:89], v[88:89] op_sel_hi:[1,0,1]
	s_nop 0
	v_cvt_pk_bf16_f32 v157, v134, v135
	v_lshlrev_b32_e32 v134, 16, v158
	v_and_b32_e32 v135, 0xffff0000, v158
	v_pk_fma_f32 v[134:135], v[134:135], s[88:89], v[82:83] op_sel_hi:[1,0,1]
	s_nop 0
	v_cvt_pk_bf16_f32 v158, v134, v135
	v_lshlrev_b32_e32 v134, 16, v159
	v_and_b32_e32 v135, 0xffff0000, v159
	v_pk_fma_f32 v[134:135], v[134:135], s[88:89], v[84:85] op_sel_hi:[1,0,1]
	s_nop 0
	v_cvt_pk_bf16_f32 v159, v134, v135
	global_store_dwordx4 v[140:141], v[156:159], off offset:256
	v_add_co_u32_e32 v140, vcc, 0x8000, v140
	s_nop 1
	v_addc_co_u32_e32 v141, vcc, 0, v141, vcc
	global_load_dwordx4 v[156:159], v[142:143], off offset:256
	v_add_co_u32_e32 v142, vcc, 0x8000, v142
	s_nop 1
	v_addc_co_u32_e32 v143, vcc, 0, v143, vcc
	s_waitcnt vmcnt(11)
; __device__ __forceinline__ float bflo(unsigned w) { return __uint_as_float(w << 16); }
; __device__ __forceinline__ float bfhi(unsigned w) { return __uint_as_float(w & 0xFFFF0000u); }
; __device__ __forceinline__ unsigned cvt_pk_bf16(float lo, float hi) { f32x2c v = {lo, hi}; bf16x2c b = __builtin_convertvector(v, bf16x2c); return __builtin_bit_cast(unsigned, b); }
;     __device__ __forceinline__ void operator()(const f32x4 (&acc)[2][2][4][2], const Unit& u, int wr, int wc, int fr, int fq) const {
;     ...
; #pragma unroll
;         for (int ai = 0; ai < 2; ++ai)
; #pragma unroll
;             for (int m = 0; m < 4; ++m) { const size_t ro = (size_t)(row0 + ai * HALF + m * 16) * D + col0;
; #pragma unroll
;                 for (int bj = 0; bj < 2; ++bj) { const u32x4 h = *(const u32x4*)(hb + ro + bj * HALF); const f32x4 v0 = acc[ai][bj][m][0], v1 = acc[ai][bj][m][1];
;                     u32x4 w; w.x = cvt_pk_bf16(v0[0] + ALPHA * bflo(h.x), v0[1] + ALPHA * bfhi(h.x)); w.y = cvt_pk_bf16(v0[2] + ALPHA * bflo(h.y), v0[3] + ALPHA * bfhi(h.y));
;                     w.z = cvt_pk_bf16(v1[0] + ALPHA * bflo(h.z), v1[1] + ALPHA * bfhi(h.z)); w.w = cvt_pk_bf16(v1[2] + ALPHA * bflo(h.w), v1[3] + ALPHA * bfhi(h.w));
;                     *(u32x4*)(Z + ro + bj * HALF) = w; } }
	v_lshlrev_b32_e32 v134, 16, v160
	v_and_b32_e32 v135, 0xffff0000, v160
	v_pk_fma_f32 v[134:135], v[134:135], s[88:89], v[110:111] op_sel_hi:[1,0,1]
	s_nop 0
	v_cvt_pk_bf16_f32 v160, v134, v135
	v_lshlrev_b32_e32 v134, 16, v161
	v_and_b32_e32 v135, 0xffff0000, v161
	v_pk_fma_f32 v[134:135], v[134:135], s[88:89], v[112:113] op_sel_hi:[1,0,1]
	s_nop 0
	v_cvt_pk_bf16_f32 v161, v134, v135
	v_lshlrev_b32_e32 v134, 16, v162
	v_and_b32_e32 v135, 0xffff0000, v162
	v_pk_fma_f32 v[134:135], v[134:135], s[88:89], v[106:107] op_sel_hi:[1,0,1]
	s_nop 0
	v_cvt_pk_bf16_f32 v162, v134, v135
	v_lshlrev_b32_e32 v134, 16, v163
	v_and_b32_e32 v135, 0xffff0000, v163
	v_pk_fma_f32 v[134:135], v[134:135], s[88:89], v[108:109] op_sel_hi:[1,0,1]
	s_nop 0
	v_cvt_pk_bf16_f32 v163, v134, v135
	global_store_dwordx4 v[140:141], v[160:163], off
	s_nop 1
	global_load_dwordx4 v[160:163], v[142:143], off
	s_waitcnt vmcnt(12)
	v_lshlrev_b32_e32 v134, 16, v164
	v_and_b32_e32 v135, 0xffff0000, v164
	v_pk_fma_f32 v[134:135], v[134:135], s[88:89], v[78:79] op_sel_hi:[1,0,1]
	s_nop 0
	v_cvt_pk_bf16_f32 v164, v134, v135
	v_lshlrev_b32_e32 v134, 16, v165
	v_and_b32_e32 v135, 0xffff0000, v165
	v_pk_fma_f32 v[134:135], v[134:135], s[88:89], v[80:81] op_sel_hi:[1,0,1]
	s_nop 0
	v_cvt_pk_bf16_f32 v165, v134, v135
	v_lshlrev_b32_e32 v134, 16, v166
	v_and_b32_e32 v135, 0xffff0000, v166
	v_pk_fma_f32 v[134:135], v[134:135], s[88:89], v[74:75] op_sel_hi:[1,0,1]
	s_nop 0
	v_cvt_pk_bf16_f32 v166, v134, v135
	v_lshlrev_b32_e32 v134, 16, v167
	v_and_b32_e32 v135, 0xffff0000, v167
	v_pk_fma_f32 v[134:135], v[134:135], s[88:89], v[76:77] op_sel_hi:[1,0,1]
	s_nop 0
	v_cvt_pk_bf16_f32 v167, v134, v135
	global_store_dwordx4 v[140:141], v[164:167], off offset:256
	v_add_co_u32_e32 v140, vcc, 0x8000, v140
	s_nop 1
	v_addc_co_u32_e32 v141, vcc, 0, v141, vcc
	global_load_dwordx4 v[164:167], v[142:143], off offset:256
	v_add_co_u32_e32 v142, vcc, 0x8000, v142
	s_nop 1
	v_addc_co_u32_e32 v143, vcc, 0, v143, vcc
	s_waitcnt vmcnt(13)
	v_lshlrev_b32_e32 v134, 16, v168
	v_and_b32_e32 v135, 0xffff0000, v168
	v_pk_fma_f32 v[134:135], v[134:135], s[88:89], v[102:103] op_sel_hi:[1,0,1]
	s_nop 0
	v_cvt_pk_bf16_f32 v168, v134, v135
	v_lshlrev_b32_e32 v134, 16, v169
	v_and_b32_e32 v135, 0xffff0000, v169
	v_pk_fma_f32 v[134:135], v[134:135], s[88:89], v[104:105] op_sel_hi:[1,0,1]
	s_nop 0
	v_cvt_pk_bf16_f32 v169, v134, v135
	v_lshlrev_b32_e32 v134, 16, v170
	v_and_b32_e32 v135, 0xffff0000, v170
	v_pk_fma_f32 v[134:135], v[134:135], s[88:89], v[98:99] op_sel_hi:[1,0,1]
	s_nop 0
	v_cvt_pk_bf16_f32 v170, v134, v135
	v_lshlrev_b32_e32 v134, 16, v171
	v_and_b32_e32 v135, 0xffff0000, v171
	v_pk_fma_f32 v[134:135], v[134:135], s[88:89], v[100:101] op_sel_hi:[1,0,1]
	s_nop 0
	v_cvt_pk_bf16_f32 v171, v134, v135
	global_store_dwordx4 v[140:141], v[168:171], off
	s_nop 1
	global_load_dwordx4 v[168:171], v[142:143], off
	s_waitcnt vmcnt(14)
	v_lshlrev_b32_e32 v134, 16, v172
	v_and_b32_e32 v135, 0xffff0000, v172
	v_pk_fma_f32 v[134:135], v[134:135], s[88:89], v[70:71] op_sel_hi:[1,0,1]
	s_nop 0
	v_cvt_pk_bf16_f32 v172, v134, v135
	v_lshlrev_b32_e32 v134, 16, v173
	v_and_b32_e32 v135, 0xffff0000, v173
	v_pk_fma_f32 v[134:135], v[134:135], s[88:89], v[72:73] op_sel_hi:[1,0,1]
	s_nop 0
	v_cvt_pk_bf16_f32 v173, v134, v135
	v_lshlrev_b32_e32 v134, 16, v174
	v_and_b32_e32 v135, 0xffff0000, v174
	v_pk_fma_f32 v[134:135], v[134:135], s[88:89], v[66:67] op_sel_hi:[1,0,1]
	s_nop 0
	v_cvt_pk_bf16_f32 v174, v134, v135
	v_lshlrev_b32_e32 v134, 16, v175
	v_and_b32_e32 v135, 0xffff0000, v175
	v_pk_fma_f32 v[134:135], v[134:135], s[88:89], v[68:69] op_sel_hi:[1,0,1]
	s_nop 0
	v_cvt_pk_bf16_f32 v175, v134, v135
	global_store_dwordx4 v[140:141], v[172:175], off offset:256
	v_add_co_u32_e32 v140, vcc, 0x28000, v140
	s_nop 1
	v_addc_co_u32_e32 v141, vcc, 0, v141, vcc
	global_load_dwordx4 v[172:175], v[142:143], off offset:256
	s_waitcnt vmcnt(14)
	v_lshlrev_b32_e32 v134, 16, v144
	v_and_b32_e32 v135, 0xffff0000, v144
	v_pk_fma_f32 v[134:135], v[134:135], s[88:89], v[62:63] op_sel_hi:[1,0,1]
	s_nop 0
	v_cvt_pk_bf16_f32 v144, v134, v135
	v_lshlrev_b32_e32 v134, 16, v145
	v_and_b32_e32 v135, 0xffff0000, v145
	v_pk_fma_f32 v[134:135], v[134:135], s[88:89], v[64:65] op_sel_hi:[1,0,1]
	s_nop 0
	v_cvt_pk_bf16_f32 v145, v134, v135
	v_lshlrev_b32_e32 v134, 16, v146
	v_and_b32_e32 v135, 0xffff0000, v146
	v_pk_fma_f32 v[134:135], v[134:135], s[88:89], v[58:59] op_sel_hi:[1,0,1]
	s_nop 0
	v_cvt_pk_bf16_f32 v146, v134, v135
	v_lshlrev_b32_e32 v134, 16, v147
	v_and_b32_e32 v135, 0xffff0000, v147
	v_pk_fma_f32 v[134:135], v[134:135], s[88:89], v[60:61] op_sel_hi:[1,0,1]
	s_nop 0
	v_cvt_pk_bf16_f32 v147, v134, v135
	global_store_dwordx4 v[140:141], v[144:147], off
	s_nop 1
	s_waitcnt vmcnt(13)
	v_lshlrev_b32_e32 v134, 16, v148
	v_and_b32_e32 v135, 0xffff0000, v148
	v_pk_fma_f32 v[134:135], v[134:135], s[88:89], v[46:47] op_sel_hi:[1,0,1]
	s_nop 0
	v_cvt_pk_bf16_f32 v148, v134, v135
	v_lshlrev_b32_e32 v134, 16, v149
	v_and_b32_e32 v135, 0xffff0000, v149
	v_pk_fma_f32 v[134:135], v[134:135], s[88:89], v[48:49] op_sel_hi:[1,0,1]
	s_nop 0
	v_cvt_pk_bf16_f32 v149, v134, v135
	v_lshlrev_b32_e32 v134, 16, v150
	v_and_b32_e32 v135, 0xffff0000, v150
	v_pk_fma_f32 v[134:135], v[134:135], s[88:89], v[38:39] op_sel_hi:[1,0,1]
	s_nop 0
	v_cvt_pk_bf16_f32 v150, v134, v135
	v_lshlrev_b32_e32 v134, 16, v151
	v_and_b32_e32 v135, 0xffff0000, v151
	v_pk_fma_f32 v[134:135], v[134:135], s[88:89], v[40:41] op_sel_hi:[1,0,1]
	s_nop 0
	v_cvt_pk_bf16_f32 v151, v134, v135
	global_store_dwordx4 v[140:141], v[148:151], off offset:256
	v_add_co_u32_e32 v140, vcc, 0x8000, v140
	s_nop 1
	v_addc_co_u32_e32 v141, vcc, 0, v141, vcc
	s_waitcnt vmcnt(12)
; __device__ __forceinline__ float bflo(unsigned w) { return __uint_as_float(w << 16); }
; __device__ __forceinline__ float bfhi(unsigned w) { return __uint_as_float(w & 0xFFFF0000u); }
; __device__ __forceinline__ unsigned cvt_pk_bf16(float lo, float hi) { f32x2c v = {lo, hi}; bf16x2c b = __builtin_convertvector(v, bf16x2c); return __builtin_bit_cast(unsigned, b); }
;     __device__ __forceinline__ void operator()(const f32x4 (&acc)[2][2][4][2], const Unit& u, int wr, int wc, int fr, int fq) const {
;     ...
; #pragma unroll
;         for (int ai = 0; ai < 2; ++ai)
; #pragma unroll
;             for (int m = 0; m < 4; ++m) { const size_t ro = (size_t)(row0 + ai * HALF + m * 16) * D + col0;
; #pragma unroll
;                 for (int bj = 0; bj < 2; ++bj) { const u32x4 h = *(const u32x4*)(hb + ro + bj * HALF); const f32x4 v0 = acc[ai][bj][m][0], v1 = acc[ai][bj][m][1];
;                     u32x4 w; w.x = cvt_pk_bf16(v0[0] + ALPHA * bflo(h.x), v0[1] + ALPHA * bfhi(h.x)); w.y = cvt_pk_bf16(v0[2] + ALPHA * bflo(h.y), v0[3] + ALPHA * bfhi(h.y));
;                     w.z = cvt_pk_bf16(v1[0] + ALPHA * bflo(h.z), v1[1] + ALPHA * bfhi(h.z)); w.w = cvt_pk_bf16(v1[2] + ALPHA * bflo(h.w), v1[3] + ALPHA * bfhi(h.w));
;                     *(u32x4*)(Z + ro + bj * HALF) = w; } }
	v_lshlrev_b32_e32 v134, 16, v152
	v_and_b32_e32 v135, 0xffff0000, v152
	v_pk_fma_f32 v[134:135], v[134:135], s[88:89], v[54:55] op_sel_hi:[1,0,1]
	s_nop 0
	v_cvt_pk_bf16_f32 v152, v134, v135
	v_lshlrev_b32_e32 v134, 16, v153
	v_and_b32_e32 v135, 0xffff0000, v153
	v_pk_fma_f32 v[134:135], v[134:135], s[88:89], v[56:57] op_sel_hi:[1,0,1]
	s_nop 0
	v_cvt_pk_bf16_f32 v153, v134, v135
	v_lshlrev_b32_e32 v134, 16, v154
	v_and_b32_e32 v135, 0xffff0000, v154
	v_pk_fma_f32 v[134:135], v[134:135], s[88:89], v[50:51] op_sel_hi:[1,0,1]
	s_nop 0
	v_cvt_pk_bf16_f32 v154, v134, v135
	v_lshlrev_b32_e32 v134, 16, v155
	v_and_b32_e32 v135, 0xffff0000, v155
	v_pk_fma_f32 v[134:135], v[134:135], s[88:89], v[52:53] op_sel_hi:[1,0,1]
	s_nop 0
	v_cvt_pk_bf16_f32 v155, v134, v135
	global_store_dwordx4 v[140:141], v[152:155], off
	s_nop 1
	s_waitcnt vmcnt(11)
	v_lshlrev_b32_e32 v134, 16, v156
	v_and_b32_e32 v135, 0xffff0000, v156
	v_pk_fma_f32 v[134:135], v[134:135], s[88:89], v[30:31] op_sel_hi:[1,0,1]
	s_nop 0
	v_cvt_pk_bf16_f32 v156, v134, v135
	v_lshlrev_b32_e32 v134, 16, v157
	v_and_b32_e32 v135, 0xffff0000, v157
	v_pk_fma_f32 v[134:135], v[134:135], s[88:89], v[32:33] op_sel_hi:[1,0,1]
	s_nop 0
	v_cvt_pk_bf16_f32 v157, v134, v135
	v_lshlrev_b32_e32 v134, 16, v158
	v_and_b32_e32 v135, 0xffff0000, v158
	v_pk_fma_f32 v[134:135], v[134:135], s[88:89], v[22:23] op_sel_hi:[1,0,1]
	s_nop 0
	v_cvt_pk_bf16_f32 v158, v134, v135
	v_lshlrev_b32_e32 v134, 16, v159
	v_and_b32_e32 v135, 0xffff0000, v159
	v_pk_fma_f32 v[134:135], v[134:135], s[88:89], v[24:25] op_sel_hi:[1,0,1]
	s_nop 0
	v_cvt_pk_bf16_f32 v159, v134, v135
	global_store_dwordx4 v[140:141], v[156:159], off offset:256
	v_add_co_u32_e32 v140, vcc, 0x8000, v140
	s_nop 1
	v_addc_co_u32_e32 v141, vcc, 0, v141, vcc
	s_waitcnt vmcnt(10)
	v_lshlrev_b32_e32 v134, 16, v160
	v_and_b32_e32 v135, 0xffff0000, v160
	v_pk_fma_f32 v[134:135], v[134:135], s[88:89], v[42:43] op_sel_hi:[1,0,1]
	s_nop 0
	v_cvt_pk_bf16_f32 v160, v134, v135
	v_lshlrev_b32_e32 v134, 16, v161
	v_and_b32_e32 v135, 0xffff0000, v161
	v_pk_fma_f32 v[134:135], v[134:135], s[88:89], v[44:45] op_sel_hi:[1,0,1]
	s_nop 0
	v_cvt_pk_bf16_f32 v161, v134, v135
	v_lshlrev_b32_e32 v134, 16, v162
	v_and_b32_e32 v135, 0xffff0000, v162
	v_pk_fma_f32 v[134:135], v[134:135], s[88:89], v[34:35] op_sel_hi:[1,0,1]
	s_nop 0
	v_cvt_pk_bf16_f32 v162, v134, v135
	v_lshlrev_b32_e32 v134, 16, v163
	v_and_b32_e32 v135, 0xffff0000, v163
	v_pk_fma_f32 v[134:135], v[134:135], s[88:89], v[36:37] op_sel_hi:[1,0,1]
	s_nop 0
	v_cvt_pk_bf16_f32 v163, v134, v135
	global_store_dwordx4 v[140:141], v[160:163], off
	s_nop 1
	s_waitcnt vmcnt(9)
	v_lshlrev_b32_e32 v134, 16, v164
	v_and_b32_e32 v135, 0xffff0000, v164
	v_pk_fma_f32 v[134:135], v[134:135], s[88:89], v[14:15] op_sel_hi:[1,0,1]
	s_nop 0
	v_cvt_pk_bf16_f32 v164, v134, v135
	v_lshlrev_b32_e32 v134, 16, v165
	v_and_b32_e32 v135, 0xffff0000, v165
	v_pk_fma_f32 v[134:135], v[134:135], s[88:89], v[16:17] op_sel_hi:[1,0,1]
	s_nop 0
	v_cvt_pk_bf16_f32 v165, v134, v135
	v_lshlrev_b32_e32 v134, 16, v166
	v_and_b32_e32 v135, 0xffff0000, v166
	v_pk_fma_f32 v[134:135], v[134:135], s[88:89], v[10:11] op_sel_hi:[1,0,1]
	s_nop 0
	v_cvt_pk_bf16_f32 v166, v134, v135
	v_lshlrev_b32_e32 v134, 16, v167
	v_and_b32_e32 v135, 0xffff0000, v167
	v_pk_fma_f32 v[134:135], v[134:135], s[88:89], v[12:13] op_sel_hi:[1,0,1]
	s_nop 0
	v_cvt_pk_bf16_f32 v167, v134, v135
	global_store_dwordx4 v[140:141], v[164:167], off offset:256
	v_add_co_u32_e32 v140, vcc, 0x8000, v140
	s_nop 1
	v_addc_co_u32_e32 v141, vcc, 0, v141, vcc
	s_waitcnt vmcnt(8)
	v_lshlrev_b32_e32 v134, 16, v168
	v_and_b32_e32 v135, 0xffff0000, v168
	v_pk_fma_f32 v[134:135], v[134:135], s[88:89], v[26:27] op_sel_hi:[1,0,1]
	s_nop 0
	v_cvt_pk_bf16_f32 v168, v134, v135
	v_lshlrev_b32_e32 v134, 16, v169
	v_and_b32_e32 v135, 0xffff0000, v169
	v_pk_fma_f32 v[134:135], v[134:135], s[88:89], v[28:29] op_sel_hi:[1,0,1]
	s_nop 0
	v_cvt_pk_bf16_f32 v169, v134, v135
	v_lshlrev_b32_e32 v134, 16, v170
	v_and_b32_e32 v135, 0xffff0000, v170
	v_pk_fma_f32 v[134:135], v[134:135], s[88:89], v[18:19] op_sel_hi:[1,0,1]
	s_nop 0
	v_cvt_pk_bf16_f32 v170, v134, v135
	v_lshlrev_b32_e32 v134, 16, v171
	v_and_b32_e32 v135, 0xffff0000, v171
	v_pk_fma_f32 v[134:135], v[134:135], s[88:89], v[20:21] op_sel_hi:[1,0,1]
	s_nop 0
	v_cvt_pk_bf16_f32 v171, v134, v135
	global_store_dwordx4 v[140:141], v[168:171], off
	s_nop 1
	s_waitcnt vmcnt(7)
	v_lshlrev_b32_e32 v134, 16, v172
	v_and_b32_e32 v135, 0xffff0000, v172
	v_pk_fma_f32 v[134:135], v[134:135], s[88:89], v[6:7] op_sel_hi:[1,0,1]
	s_nop 0
	v_cvt_pk_bf16_f32 v172, v134, v135
	v_lshlrev_b32_e32 v134, 16, v173
	v_and_b32_e32 v135, 0xffff0000, v173
	v_pk_fma_f32 v[134:135], v[134:135], s[88:89], v[8:9] op_sel_hi:[1,0,1]
	s_nop 0
	v_cvt_pk_bf16_f32 v173, v134, v135
	v_lshlrev_b32_e32 v134, 16, v174
	v_and_b32_e32 v135, 0xffff0000, v174
	v_pk_fma_f32 v[134:135], v[134:135], s[88:89], v[2:3] op_sel_hi:[1,0,1]
	s_nop 0
	v_cvt_pk_bf16_f32 v174, v134, v135
	v_lshlrev_b32_e32 v134, 16, v175
	v_and_b32_e32 v135, 0xffff0000, v175
	v_pk_fma_f32 v[134:135], v[134:135], s[88:89], v[4:5] op_sel_hi:[1,0,1]
	s_nop 0
	v_cvt_pk_bf16_f32 v175, v134, v135
	global_store_dwordx4 v[140:141], v[172:175], off offset:256
	s_nop 1
	s_mov_b64 s[22:23], 0

;     __device__ __forceinline__ const char* b_ptr(const Unit& u) const { return (const char*)Bt + ((size_t)u.pn * BM * K + u.koff) * 2; }
;     __device__ __forceinline__ const char* b_ptr(const Unit& u) const { return (const char*)Bt + ((size_t)u.e * bstride + (size_t)u.pn * BM * K) * 2; }
; template <class Epi, class Sched>
; __device__ __forceinline__ void gemm_phase(LAS unsigned char* lds, const bf16_t* Abase, const int K, const Sched& S, const Epi& E, const int wvid) {
;     ...
;         const bool has_next = S.next(ui + 1, nxt);
;         const char* nB = has_next ? S.b_ptr(nxt) : cB;
;         const int nt = cur.kt;
;         for (int t = 0; t < nt; t += 2) {
;             const bool last = (t == nt - 2);
;     ...
; #pragma unroll
;         for (int a = 0; a < 2; ++a)
; #pragma unroll
;             for (int b = 0; b < 2; ++b)
; #pragma unroll
;                 for (int m = 0; m < 4; ++m)
; #pragma unroll
;                     for (int n = 0; n < 2; ++n) acc[a][b][m][n] = (f32x4){0.f, 0.f, 0.f, 0.f};
;         cur = nxt; cB = nB; ++ui;
.LBB0_1208:
	s_ashr_i32 s23, s22, 31
	s_lshl_b64 s[4:5], s[22:23], 19
	v_ashrrev_i32_e32 v191, 31, v190
	s_add_u32 s4, s36, s4
	v_lshlrev_b64 v[4:5], 21, v[190:191]
	s_addc_u32 s5, s37, s5
	v_lshl_add_u64 v[194:195], s[4:5], 0, v[4:5]
	s_mov_b64 s[4:5], 0x100
	v_cndmask_b32_e64 v229, v2, v194, s[0:1]
	v_lshl_add_u64 v[196:197], v[2:3], 0, s[4:5]
	v_mov_b32_e32 v2, 0
	v_cndmask_b32_e64 v191, v3, v195, s[0:1]
	v_add_u32_e32 v230, -1, v193
	v_add_u32_e32 v231, 0x80, v227
	s_mov_b32 s23, -2
	s_mov_b64 s[26:27], 0
	v_mov_b32_e32 v3, v2
	v_mov_b32_e32 v4, v2
	v_mov_b32_e32 v5, v2
	v_mov_b32_e32 v6, v2
	v_mov_b32_e32 v7, v2
	v_mov_b32_e32 v8, v2
	v_mov_b32_e32 v9, v2
	v_mov_b32_e32 v18, v2
	v_mov_b32_e32 v19, v2
	v_mov_b32_e32 v20, v2
	v_mov_b32_e32 v21, v2
	v_mov_b32_e32 v22, v2
	v_mov_b32_e32 v23, v2
	v_mov_b32_e32 v24, v2
	v_mov_b32_e32 v25, v2
	v_mov_b32_e32 v34, v2
	v_mov_b32_e32 v35, v2
	v_mov_b32_e32 v36, v2
	v_mov_b32_e32 v37, v2
	v_mov_b32_e32 v38, v2
	v_mov_b32_e32 v39, v2
	v_mov_b32_e32 v40, v2
	v_mov_b32_e32 v41, v2
	v_mov_b32_e32 v50, v2
	v_mov_b32_e32 v51, v2
	v_mov_b32_e32 v52, v2
	v_mov_b32_e32 v53, v2
	v_mov_b32_e32 v54, v2
	v_mov_b32_e32 v55, v2
	v_mov_b32_e32 v56, v2
	v_mov_b32_e32 v57, v2
	v_mov_b32_e32 v10, v2
	v_mov_b32_e32 v11, v2
	v_mov_b32_e32 v12, v2
	v_mov_b32_e32 v13, v2
	v_mov_b32_e32 v14, v2
	v_mov_b32_e32 v15, v2
	v_mov_b32_e32 v16, v2
	v_mov_b32_e32 v17, v2
	v_mov_b32_e32 v26, v2
	v_mov_b32_e32 v27, v2
	v_mov_b32_e32 v28, v2
	v_mov_b32_e32 v29, v2
	v_mov_b32_e32 v30, v2
	v_mov_b32_e32 v31, v2
	v_mov_b32_e32 v32, v2
	v_mov_b32_e32 v33, v2
	v_mov_b32_e32 v42, v2
	v_mov_b32_e32 v43, v2
	v_mov_b32_e32 v44, v2
	v_mov_b32_e32 v45, v2
	v_mov_b32_e32 v46, v2
	v_mov_b32_e32 v47, v2
	v_mov_b32_e32 v48, v2
	v_mov_b32_e32 v49, v2
	v_mov_b32_e32 v58, v2
	v_mov_b32_e32 v59, v2
	v_mov_b32_e32 v60, v2
	v_mov_b32_e32 v61, v2
	v_mov_b32_e32 v62, v2
	v_mov_b32_e32 v63, v2
	v_mov_b32_e32 v64, v2
	v_mov_b32_e32 v65, v2
	v_mov_b32_e32 v66, v2
	v_mov_b32_e32 v67, v2
	v_mov_b32_e32 v68, v2
	v_mov_b32_e32 v69, v2
	v_mov_b32_e32 v70, v2
	v_mov_b32_e32 v71, v2
	v_mov_b32_e32 v72, v2
	v_mov_b32_e32 v73, v2
	v_mov_b32_e32 v74, v2
	v_mov_b32_e32 v75, v2
	v_mov_b32_e32 v76, v2
	v_mov_b32_e32 v77, v2
	v_mov_b32_e32 v78, v2
	v_mov_b32_e32 v79, v2
	v_mov_b32_e32 v80, v2
	v_mov_b32_e32 v81, v2
	v_mov_b32_e32 v82, v2
	v_mov_b32_e32 v83, v2
	v_mov_b32_e32 v84, v2
	v_mov_b32_e32 v85, v2
	v_mov_b32_e32 v86, v2
	v_mov_b32_e32 v87, v2
	v_mov_b32_e32 v88, v2
	v_mov_b32_e32 v89, v2
	v_mov_b32_e32 v98, v2
	v_mov_b32_e32 v99, v2
	v_mov_b32_e32 v100, v2
	v_mov_b32_e32 v101, v2
	v_mov_b32_e32 v102, v2
	v_mov_b32_e32 v103, v2
	v_mov_b32_e32 v104, v2
	v_mov_b32_e32 v105, v2
	v_mov_b32_e32 v90, v2
	v_mov_b32_e32 v91, v2
	v_mov_b32_e32 v92, v2
	v_mov_b32_e32 v93, v2
	v_mov_b32_e32 v94, v2
	v_mov_b32_e32 v95, v2
	v_mov_b32_e32 v96, v2
	v_mov_b32_e32 v97, v2
	v_mov_b32_e32 v106, v2
	v_mov_b32_e32 v107, v2
	v_mov_b32_e32 v108, v2
	v_mov_b32_e32 v109, v2
	v_mov_b32_e32 v110, v2
	v_mov_b32_e32 v111, v2
	v_mov_b32_e32 v112, v2
	v_mov_b32_e32 v113, v2
	v_mov_b32_e32 v114, v2
	v_mov_b32_e32 v115, v2
	v_mov_b32_e32 v116, v2
	v_mov_b32_e32 v117, v2
	v_mov_b32_e32 v118, v2
	v_mov_b32_e32 v119, v2
	v_mov_b32_e32 v120, v2
	v_mov_b32_e32 v121, v2
	v_mov_b32_e32 v122, v2
	v_mov_b32_e32 v123, v2
	v_mov_b32_e32 v124, v2
	v_mov_b32_e32 v125, v2
	v_mov_b32_e32 v126, v2
	v_mov_b32_e32 v127, v2
	v_mov_b32_e32 v128, v2
	v_mov_b32_e32 v129, v2
	s_branch .LBB0_1209
.Lkhead2:
	s_barrier
; #define PG8_STAGE(bufoff, gbase, voff) do { _Pragma("unroll") for (int _i = 0; _i < 2; ++_i) \
;         __builtin_amdgcn_global_load_lds((const unsigned*)((const char*)(gbase) + (voff)[_i]), (LAS unsigned*)(lds + (bufoff) + ldsw + _i * 8192), 16, 0, 0); } while (0)
; #define PG8_LDA(dst, b, h) do { _Pragma("unroll") for (int m = 0; m < 4; ++m) _Pragma("unroll") for (int k = 0; k < 2; ++k) dst[m][k] = *(const LAS bf16x8*)(lds + PG8_SA(b, h) + aoff + m * 2048 + k * 1024); } while (0)
; #define PG8_LDB(dst, b, h) do { _Pragma("unroll") for (int n = 0; n < 2; ++n) _Pragma("unroll") for (int k = 0; k < 2; ++k) dst[n][k] = *(const LAS bf16x8*)(lds + PG8_SB(b, h) + boff + n * 2048 + k * 1024); } while (0)
; #define PG8_MMA(ai, bj, At, Bt) do { __builtin_amdgcn_s_setprio(1); _Pragma("unroll") for (int m = 0; m < 4; ++m) _Pragma("unroll") for (int n = 0; n < 2; ++n) _Pragma("unroll") for (int k = 0; k < 2; ++k) \
;         acc[ai][bj][m][n] = __builtin_amdgcn_mfma_f32_16x16x32_bf16(Bt[n][k], At[m][k], acc[ai][bj][m][n], 0, 0, 0); __builtin_amdgcn_s_setprio(0); } while (0)
; #define PG8_WAIT_L(n) asm volatile("s_waitcnt lgkmcnt(" #n ")" ::: "memory")
; #define PG8_BAR __builtin_amdgcn_s_barrier()
; #define PG8_SCHED __builtin_amdgcn_sched_barrier(0)
; #define PG8_AOFF(u) do { const int _t = lt_tid(wvid); _Pragma("unroll") for (int _i = 0; _i < 2; ++_i) { int _R, _C; stage_rc(_t * 16 + _i * 8192, _R, _C); \
;         _Pragma("unroll") for (int _h = 0; _h < 2; ++_h) voffA[_h][_i] = (S.a_row(u, _h * HALF + _R) * (unsigned)K + (unsigned)(_C + (u).koff)) * 2u; } } while (0)
; template <class Epi, class Sched>
; __device__ __forceinline__ void gemm_phase(LAS unsigned char* lds, const bf16_t* Abase, const int K, const Sched& S, const Epi& E, const int wvid) {
;     ...
;             PG8_LDB(B0, 0, 0); PG8_SCHED; PG8_LDA(At, 0, 0); PG8_STAGE(PG8_SA(1, 1), a1, voffA[1]);
;             PG8_WAIT_L(8); PG8_BAR; PG8_WAIT_L(0); PG8_MMA(0, 0, At, B0); PG8_BAR; PG8_SCHED;
;             if (last && has_next) PG8_AOFF(nxt);
.LBB0_1209:
	v_add_u32_e32 v130, 0, v224
	v_add_u32_e32 v142, 0x10000, v130
	ds_read_b128 v[130:133], v142
	ds_read_b128 v[134:137], v142 offset:1024
	ds_read_b128 v[138:141], v142 offset:2048
	ds_read_b128 v[142:145], v142 offset:3072
	s_cmp_eq_u32 s23, 12
	s_cselect_b64 s[4:5], -1, 0
	s_add_i32 m0, s25, 0xc000
	s_add_u32 s28, s20, s26
	s_addc_u32 s29, s21, s27
	ds_read_b128 v[170:173], v226
	ds_read_b128 v[174:177], v226 offset:1024
	ds_read_b128 v[162:165], v226 offset:2048
	ds_read_b128 v[166:169], v226 offset:3072
	ds_read_b128 v[154:157], v226 offset:4096
	ds_read_b128 v[158:161], v226 offset:5120
	ds_read_b128 v[146:149], v226 offset:6144
	ds_read_b128 v[150:153], v226 offset:7168
	global_load_lds_dwordx4 v186, s[28:29]
	s_add_i32 m0, s25, 0xe000
	s_nop 0
	global_load_lds_dwordx4 v188, s[28:29]
	s_waitcnt lgkmcnt(8)
	s_barrier
	s_waitcnt lgkmcnt(0)
	s_waitcnt lgkmcnt(0)
	v_mfma_f32_16x16x32_bf16 v[126:129], v[130:133], v[170:173], v[126:129]
	v_mfma_f32_16x16x32_bf16 v[122:125], v[138:141], v[170:173], v[122:125]
	v_mfma_f32_16x16x32_bf16 v[118:121], v[130:133], v[162:165], v[118:121]
	v_mfma_f32_16x16x32_bf16 v[114:117], v[138:141], v[162:165], v[114:117]
	v_mfma_f32_16x16x32_bf16 v[110:113], v[130:133], v[154:157], v[110:113]
	v_mfma_f32_16x16x32_bf16 v[106:109], v[138:141], v[154:157], v[106:109]
	v_mfma_f32_16x16x32_bf16 v[94:97], v[130:133], v[146:149], v[94:97]
	v_mfma_f32_16x16x32_bf16 v[90:93], v[138:141], v[146:149], v[90:93]
	v_mfma_f32_16x16x32_bf16 v[126:129], v[134:137], v[174:177], v[126:129]
	v_mfma_f32_16x16x32_bf16 v[122:125], v[142:145], v[174:177], v[122:125]
	v_mfma_f32_16x16x32_bf16 v[118:121], v[134:137], v[166:169], v[118:121]
	v_mfma_f32_16x16x32_bf16 v[114:117], v[142:145], v[166:169], v[114:117]
	v_mfma_f32_16x16x32_bf16 v[110:113], v[134:137], v[158:161], v[110:113]
	v_mfma_f32_16x16x32_bf16 v[106:109], v[142:145], v[158:161], v[106:109]
	v_mfma_f32_16x16x32_bf16 v[94:97], v[134:137], v[150:153], v[94:97]
	v_mfma_f32_16x16x32_bf16 v[90:93], v[142:145], v[150:153], v[90:93]
	s_barrier
	s_and_b64 s[28:29], s[0:1], s[4:5]
	s_andn2_b64 vcc, exec, s[28:29]
	s_cbranch_vccnz .LBB0_1211
	v_mbcnt_lo_u32_b32 v0, -1, 0
	v_mbcnt_hi_u32_b32 v0, -1, v0
	v_mov_b32_e32 v189, v1
	v_or_b32_e32 v0, s75, v0
	v_ashrrev_i32_e32 v184, 31, v0
	v_lshrrev_b32_e32 v184, 26, v184
	v_lshlrev_b32_e32 v186, 4, v0
	v_add_u32_e32 v184, v0, v184
	v_bfe_i32 v0, v0, 27, 1
	v_lshrrev_b32_e32 v0, 22, v0
	v_add_u32_e32 v0, v186, v0
	v_and_b32_e32 v0, 0xfffffc00, v0
	v_sub_u32_e32 v0, v186, v0
	v_lshrrev_b32_e32 v185, 4, v0
	v_bitop3_b32 v0, v185, v0, 32 bitop3:0x6c
	v_ashrrev_i32_e32 v187, 31, v0
	v_ashrrev_i32_e32 v184, 6, v184
	v_lshrrev_b32_e32 v187, 26, v187
	v_lshlrev_b32_e32 v185, 3, v184
	v_add_u32_e32 v187, v0, v187
	v_and_b32_e32 v185, -16, v185
	v_ashrrev_i32_e32 v188, 6, v187
	v_add_u32_e32 v188, v188, v185
	v_and_b32_e32 v185, 0xc0, v187
	v_sub_u32_e32 v0, v0, v185
	v_lshlrev_b32_e32 v184, 5, v184
	v_ashrrev_i16_sdwa v0, v216, sext(v0) dst_sel:DWORD dst_unused:UNUSED_PAD src0_sel:DWORD src1_sel:BYTE_0
	v_and_b32_e32 v184, 32, v184
	v_bfe_i32 v0, v0, 0, 16
	v_add_lshl_u32 v0, v184, v0, 1
	v_add_u32_e32 v232, v188, v227
	v_min_i32_e32 v232, v232, v230
	v_add_u32_e32 v232, v232, v192
	v_ashrrev_i32_e32 v233, 31, v232
	v_lshl_add_u64 v[232:233], v[232:233], 2, s[10:11]
	global_load_dword v240, v[232:233], off
	v_add_u32_e32 v234, v188, v231
	v_min_i32_e32 v234, v234, v230
	v_add_u32_e32 v234, v234, v192
	v_ashrrev_i32_e32 v235, 31, v234
	v_lshl_add_u64 v[234:235], v[234:235], 2, s[10:11]
	global_load_dword v241, v[234:235], off
	v_add_u32_e32 v184, 0x2000, v186
	v_ashrrev_i32_e32 v185, 31, v184
	v_lshrrev_b32_e32 v185, 22, v185
	v_add_u32_e32 v185, v184, v185
	v_ashrrev_i32_e32 v185, 10, v185
	v_mul_i32_i24_e32 v186, 0x400, v185
	v_sub_u32_e32 v184, v184, v186
	v_lshrrev_b32_e32 v186, 4, v184
	v_bitop3_b32 v184, v186, v184, 32 bitop3:0x6c
	v_ashrrev_i32_e32 v187, 31, v184
	v_lshrrev_b32_e32 v187, 26, v187
	v_add_u32_e32 v187, v184, v187
	v_ashrrev_i32_e32 v188, 6, v187
	v_and_b32_e32 v187, 0xc0, v187
	v_lshlrev_b32_e32 v186, 3, v185
	v_sub_u32_e32 v184, v184, v187
	v_and_b32_e32 v186, -16, v186
	v_lshlrev_b32_e32 v185, 5, v185
	v_ashrrev_i16_sdwa v184, v216, sext(v184) dst_sel:DWORD dst_unused:UNUSED_PAD src0_sel:DWORD src1_sel:BYTE_0
	v_add_u32_e32 v186, v188, v186
	v_and_b32_e32 v185, 32, v185
	v_bfe_i32 v184, v184, 0, 16
	v_add_lshl_u32 v188, v185, v184, 1
	v_add_u32_e32 v236, v186, v227
	v_min_i32_e32 v236, v236, v230
	v_add_u32_e32 v236, v236, v192
	v_ashrrev_i32_e32 v237, 31, v236
	v_lshl_add_u64 v[236:237], v[236:237], 2, s[10:11]
	global_load_dword v242, v[236:237], off
	v_add_u32_e32 v238, v186, v231
	v_min_i32_e32 v238, v238, v230
	v_add_u32_e32 v238, v238, v192
	v_ashrrev_i32_e32 v239, 31, v238
	v_lshl_add_u64 v[238:239], v[238:239], 2, s[10:11]
	global_load_dword v243, v[238:239], off
	s_waitcnt vmcnt(0)
	v_lshl_add_u32 v200, v240, 11, v0
	v_lshl_add_u32 v0, v241, 11, v0
	v_mov_b64_e32 v[198:199], v[0:1]
	v_mov_b32_e32 v186, v0
	v_mov_b32_e32 v0, v200
	v_lshl_add_u32 v184, v242, 11, v188
	v_lshl_add_u32 v188, v243, 11, v188
	s_branch .LBB0_1212

; #define PG8_STAGE(bufoff, gbase, voff) do { _Pragma("unroll") for (int _i = 0; _i < 2; ++_i) \
;         __builtin_amdgcn_global_load_lds((const unsigned*)((const char*)(gbase) + (voff)[_i]), (LAS unsigned*)(lds + (bufoff) + ldsw + _i * 8192), 16, 0, 0); } while (0)
; #define PG8_LDA(dst, b, h) do { _Pragma("unroll") for (int m = 0; m < 4; ++m) _Pragma("unroll") for (int k = 0; k < 2; ++k) dst[m][k] = *(const LAS bf16x8*)(lds + PG8_SA(b, h) + aoff + m * 2048 + k * 1024); } while (0)
; #define PG8_LDB(dst, b, h) do { _Pragma("unroll") for (int n = 0; n < 2; ++n) _Pragma("unroll") for (int k = 0; k < 2; ++k) dst[n][k] = *(const LAS bf16x8*)(lds + PG8_SB(b, h) + boff + n * 2048 + k * 1024); } while (0)
; #define PG8_MMA(ai, bj, At, Bt) do { __builtin_amdgcn_s_setprio(1); _Pragma("unroll") for (int m = 0; m < 4; ++m) _Pragma("unroll") for (int n = 0; n < 2; ++n) _Pragma("unroll") for (int k = 0; k < 2; ++k) \
;         acc[ai][bj][m][n] = __builtin_amdgcn_mfma_f32_16x16x32_bf16(Bt[n][k], At[m][k], acc[ai][bj][m][n], 0, 0, 0); __builtin_amdgcn_s_setprio(0); } while (0)
; #define PG8_WAIT_V(n) asm volatile("s_waitcnt vmcnt(" #n ")" ::: "memory")
; #define PG8_WAIT_L(n) asm volatile("s_waitcnt lgkmcnt(" #n ")" ::: "memory")
; #define PG8_BAR __builtin_amdgcn_s_barrier()
; #define PG8_SCHED __builtin_amdgcn_sched_barrier(0)
; template <class Epi, class Sched>
; __device__ __forceinline__ void gemm_phase(LAS unsigned char* lds, const bf16_t* Abase, const int K, const Sched& S, const Epi& E, const int wvid) {
;     ...
;             const char* a2 = last ? Ab : Ab + (size_t)(t + 2) * kstep; const char* b2 = last ? nB : cB + (size_t)(t + 2) * kstep;
;             const char* a3 = a2 + kstep; const char* b3 = b2 + kstep;
;             PG8_LDB(B1, 0, 1); PG8_STAGE(PG8_SB(0, 0), b2, voffB);
;             PG8_BAR; PG8_WAIT_L(0); PG8_MMA(0, 1, At, B1); PG8_BAR;
;             PG8_LDA(At, 0, 1); PG8_STAGE(PG8_SA(0, 0), a2, voffA[0]);
;             PG8_BAR; PG8_WAIT_L(0); PG8_MMA(1, 0, At, B0); PG8_BAR; PG8_SCHED;
;             PG8_STAGE(PG8_SB(0, 1), b2 + hstep, voffB);
;             PG8_WAIT_V(6); PG8_BAR; PG8_MMA(1, 1, At, B1); PG8_BAR;
;             PG8_LDB(B0, 1, 0); PG8_SCHED; PG8_LDA(At, 1, 0); PG8_STAGE(PG8_SA(0, 1), a2, voffA[1]);
.LBB0_1212:
	s_add_u32 s28, s26, 0x100
	s_addc_u32 s29, s27, 0
	s_and_b64 s[30:31], s[4:5], exec
	s_cselect_b32 s30, 0, s28
	s_cselect_b32 s31, 0, s29
	s_add_u32 s30, s16, s30
	v_lshl_add_u64 v[236:237], v[196:197], 0, s[26:27]
	s_addc_u32 s31, s17, s31
	s_add_i32 s26, 0, 0x14000
	v_cndmask_b32_e64 v237, v237, v191, s[4:5]
	v_cndmask_b32_e64 v236, v236, v229, s[4:5]
	s_mov_b32 m0, s39
	v_add_u32_e32 v185, s26, v224
	v_lshl_add_u64 v[238:239], v[236:237], 0, v[180:181]
	ds_read_b128 v[200:203], v185
	ds_read_b128 v[206:209], v185 offset:1024
	ds_read_b128 v[210:213], v185 offset:2048
	ds_read_b128 v[232:235], v185 offset:3072
	global_load_lds_dwordx4 v[238:239], off
	v_lshl_add_u64 v[240:241], v[236:237], 0, v[182:183]
	s_mov_b32 m0, s42
	s_nop 0
	global_load_lds_dwordx4 v[240:241], off
	s_barrier
	s_waitcnt lgkmcnt(0)
	s_waitcnt lgkmcnt(0)
	v_mfma_f32_16x16x32_bf16 v[102:105], v[200:203], v[170:173], v[102:105]
	v_mfma_f32_16x16x32_bf16 v[98:101], v[210:213], v[170:173], v[98:101]
	v_mfma_f32_16x16x32_bf16 v[86:89], v[200:203], v[162:165], v[86:89]
	v_mfma_f32_16x16x32_bf16 v[82:85], v[210:213], v[162:165], v[82:85]
	v_mfma_f32_16x16x32_bf16 v[78:81], v[200:203], v[154:157], v[78:81]
	v_mfma_f32_16x16x32_bf16 v[74:77], v[210:213], v[154:157], v[74:77]
	v_mfma_f32_16x16x32_bf16 v[70:73], v[200:203], v[146:149], v[70:73]
	v_mfma_f32_16x16x32_bf16 v[66:69], v[210:213], v[146:149], v[66:69]
	v_mfma_f32_16x16x32_bf16 v[102:105], v[206:209], v[174:177], v[102:105]
	v_mfma_f32_16x16x32_bf16 v[98:101], v[232:235], v[174:177], v[98:101]
	v_mfma_f32_16x16x32_bf16 v[86:89], v[206:209], v[166:169], v[86:89]
	v_mfma_f32_16x16x32_bf16 v[82:85], v[232:235], v[166:169], v[82:85]
	v_mfma_f32_16x16x32_bf16 v[78:81], v[206:209], v[158:161], v[78:81]
	v_mfma_f32_16x16x32_bf16 v[74:77], v[232:235], v[158:161], v[74:77]
	v_mfma_f32_16x16x32_bf16 v[70:73], v[206:209], v[150:153], v[70:73]
	v_mfma_f32_16x16x32_bf16 v[66:69], v[232:235], v[150:153], v[66:69]
	s_mov_b32 m0, s25
	s_barrier
	ds_read_b128 v[146:149], v226 offset:16384
	ds_read_b128 v[150:153], v226 offset:17408
	ds_read_b128 v[154:157], v226 offset:18432
	ds_read_b128 v[158:161], v226 offset:19456
	ds_read_b128 v[162:165], v226 offset:20480
	ds_read_b128 v[166:169], v226 offset:21504
	ds_read_b128 v[170:173], v226 offset:22528
	ds_read_b128 v[174:177], v226 offset:23552
	global_load_lds_dwordx4 v0, s[30:31]
	s_mov_b32 m0, s43
	v_mov_b32_e32 v185, v1
	global_load_lds_dwordx4 v184, s[30:31]
	s_barrier
	s_waitcnt lgkmcnt(0)
	v_lshl_add_u64 v[242:243], s[30:31], 0, v[0:1]
	v_lshl_add_u64 v[244:245], s[30:31], 0, v[184:185]
	s_waitcnt lgkmcnt(0)
	v_mfma_f32_16x16x32_bf16 v[62:65], v[130:133], v[146:149], v[62:65]
	v_mfma_f32_16x16x32_bf16 v[58:61], v[138:141], v[146:149], v[58:61]
	v_mfma_f32_16x16x32_bf16 v[46:49], v[130:133], v[154:157], v[46:49]
	v_mfma_f32_16x16x32_bf16 v[42:45], v[138:141], v[154:157], v[42:45]
	v_mfma_f32_16x16x32_bf16 v[30:33], v[130:133], v[162:165], v[30:33]
	v_mfma_f32_16x16x32_bf16 v[26:29], v[138:141], v[162:165], v[26:29]
	v_mfma_f32_16x16x32_bf16 v[14:17], v[130:133], v[170:173], v[14:17]
	v_mfma_f32_16x16x32_bf16 v[10:13], v[138:141], v[170:173], v[10:13]
	v_mfma_f32_16x16x32_bf16 v[62:65], v[134:137], v[150:153], v[62:65]
	v_mfma_f32_16x16x32_bf16 v[58:61], v[142:145], v[150:153], v[58:61]
	v_mfma_f32_16x16x32_bf16 v[46:49], v[134:137], v[158:161], v[46:49]
	v_mfma_f32_16x16x32_bf16 v[42:45], v[142:145], v[158:161], v[42:45]
	v_mfma_f32_16x16x32_bf16 v[30:33], v[134:137], v[166:169], v[30:33]
	v_mfma_f32_16x16x32_bf16 v[26:29], v[142:145], v[166:169], v[26:29]
	v_mfma_f32_16x16x32_bf16 v[14:17], v[134:137], v[174:177], v[14:17]
	v_mfma_f32_16x16x32_bf16 v[10:13], v[142:145], v[174:177], v[10:13]
	s_barrier
	v_lshl_add_u64 v[130:131], v[236:237], 0, s[90:91]
	s_add_i32 s4, s26, s38
	v_lshl_add_u64 v[132:133], v[130:131], 0, v[180:181]
	s_mov_b32 m0, s4
	v_lshl_add_u64 v[130:131], v[130:131], 0, v[182:183]
	global_load_lds_dwordx4 v[132:133], off
	s_add_i32 m0, s4, 0x2000
	s_nop 0
	global_load_lds_dwordx4 v[130:131], off
	s_waitcnt vmcnt(6)
	s_barrier
	v_mfma_f32_16x16x32_bf16 v[54:57], v[200:203], v[146:149], v[54:57]
	v_mfma_f32_16x16x32_bf16 v[50:53], v[210:213], v[146:149], v[50:53]
	v_mfma_f32_16x16x32_bf16 v[38:41], v[200:203], v[154:157], v[38:41]
	v_mfma_f32_16x16x32_bf16 v[34:37], v[210:213], v[154:157], v[34:37]
	v_mfma_f32_16x16x32_bf16 v[22:25], v[200:203], v[162:165], v[22:25]
	v_mfma_f32_16x16x32_bf16 v[18:21], v[210:213], v[162:165], v[18:21]
	v_mfma_f32_16x16x32_bf16 v[6:9], v[200:203], v[170:173], v[6:9]
	v_mfma_f32_16x16x32_bf16 v[2:5], v[210:213], v[170:173], v[2:5]
	v_mfma_f32_16x16x32_bf16 v[54:57], v[206:209], v[150:153], v[54:57]
	v_mfma_f32_16x16x32_bf16 v[50:53], v[232:235], v[150:153], v[50:53]
	v_mfma_f32_16x16x32_bf16 v[38:41], v[206:209], v[158:161], v[38:41]
	v_mfma_f32_16x16x32_bf16 v[34:37], v[232:235], v[158:161], v[34:37]
	v_mfma_f32_16x16x32_bf16 v[22:25], v[206:209], v[166:169], v[22:25]
	v_mfma_f32_16x16x32_bf16 v[18:21], v[232:235], v[166:169], v[18:21]
	v_mfma_f32_16x16x32_bf16 v[6:9], v[206:209], v[174:177], v[6:9]
	v_mfma_f32_16x16x32_bf16 v[2:5], v[232:235], v[174:177], v[2:5]
	s_add_i32 s4, 0, 0x18000
	v_add_u32_e32 v142, s4, v224
	s_barrier
	ds_read_b128 v[130:133], v142
	ds_read_b128 v[134:137], v142 offset:1024
	ds_read_b128 v[138:141], v142 offset:2048
	ds_read_b128 v[142:145], v142 offset:3072
	s_mov_b32 m0, s46
	v_lshl_add_u64 v[198:199], s[30:31], 0, v[198:199]
	ds_read_b128 v[146:149], v226 offset:32768
	ds_read_b128 v[150:153], v226 offset:33792
	ds_read_b128 v[154:157], v226 offset:34816
	ds_read_b128 v[158:161], v226 offset:35840
	ds_read_b128 v[162:165], v226 offset:36864
	ds_read_b128 v[166:169], v226 offset:37888
	ds_read_b128 v[170:173], v226 offset:38912
	ds_read_b128 v[174:177], v226 offset:39936
	global_load_lds_dwordx4 v[198:199], off
	v_lshl_add_u64 v[198:199], s[30:31], 0, v[188:189]
	s_mov_b32 m0, s47
	s_nop 0
	global_load_lds_dwordx4 v[198:199], off
	s_waitcnt lgkmcnt(8)
	s_barrier
; #define PG8_STAGE(bufoff, gbase, voff) do { _Pragma("unroll") for (int _i = 0; _i < 2; ++_i) \
;         __builtin_amdgcn_global_load_lds((const unsigned*)((const char*)(gbase) + (voff)[_i]), (LAS unsigned*)(lds + (bufoff) + ldsw + _i * 8192), 16, 0, 0); } while (0)
; #define PG8_LDA(dst, b, h) do { _Pragma("unroll") for (int m = 0; m < 4; ++m) _Pragma("unroll") for (int k = 0; k < 2; ++k) dst[m][k] = *(const LAS bf16x8*)(lds + PG8_SA(b, h) + aoff + m * 2048 + k * 1024); } while (0)
; #define PG8_LDB(dst, b, h) do { _Pragma("unroll") for (int n = 0; n < 2; ++n) _Pragma("unroll") for (int k = 0; k < 2; ++k) dst[n][k] = *(const LAS bf16x8*)(lds + PG8_SB(b, h) + boff + n * 2048 + k * 1024); } while (0)
; #define PG8_MMA(ai, bj, At, Bt) do { __builtin_amdgcn_s_setprio(1); _Pragma("unroll") for (int m = 0; m < 4; ++m) _Pragma("unroll") for (int n = 0; n < 2; ++n) _Pragma("unroll") for (int k = 0; k < 2; ++k) \
;         acc[ai][bj][m][n] = __builtin_amdgcn_mfma_f32_16x16x32_bf16(Bt[n][k], At[m][k], acc[ai][bj][m][n], 0, 0, 0); __builtin_amdgcn_s_setprio(0); } while (0)
; #define PG8_WAIT_V(n) asm volatile("s_waitcnt vmcnt(" #n ")" ::: "memory")
; #define PG8_WAIT_L(n) asm volatile("s_waitcnt lgkmcnt(" #n ")" ::: "memory")
; #define PG8_BAR __builtin_amdgcn_s_barrier()
; #define PG8_SCHED __builtin_amdgcn_sched_barrier(0)
; template <class Epi, class Sched>
; __device__ __forceinline__ void gemm_phase(LAS unsigned char* lds, const bf16_t* Abase, const int K, const Sched& S, const Epi& E, const int wvid) {
;     ...
;             PG8_LDB(B0, 1, 0); PG8_SCHED; PG8_LDA(At, 1, 0); PG8_STAGE(PG8_SA(0, 1), a2, voffA[1]);
;             PG8_WAIT_L(8); PG8_BAR; PG8_WAIT_L(0); PG8_MMA(0, 0, At, B0); PG8_BAR; PG8_SCHED;
;             PG8_LDB(B1, 1, 1); PG8_STAGE(PG8_SB(1, 0), b3, voffB);
;             PG8_BAR; PG8_WAIT_L(0); PG8_MMA(0, 1, At, B1); PG8_BAR;
;             PG8_LDA(At, 1, 1); PG8_STAGE(PG8_SA(1, 0), a3, voffA[0]);
;             PG8_BAR; PG8_WAIT_L(0); PG8_MMA(1, 0, At, B0); PG8_BAR; PG8_SCHED;
;             PG8_STAGE(PG8_SB(1, 1), b3 + hstep, voffB);
;             PG8_WAIT_V(6); PG8_BAR; PG8_MMA(1, 1, At, B1); PG8_BAR;
;         }
	s_waitcnt lgkmcnt(0)
	s_waitcnt lgkmcnt(0)
	v_mfma_f32_16x16x32_bf16 v[126:129], v[130:133], v[146:149], v[126:129]
	v_mfma_f32_16x16x32_bf16 v[122:125], v[138:141], v[146:149], v[122:125]
	v_mfma_f32_16x16x32_bf16 v[118:121], v[130:133], v[154:157], v[118:121]
	v_mfma_f32_16x16x32_bf16 v[114:117], v[138:141], v[154:157], v[114:117]
	v_mfma_f32_16x16x32_bf16 v[110:113], v[130:133], v[162:165], v[110:113]
	v_mfma_f32_16x16x32_bf16 v[106:109], v[138:141], v[162:165], v[106:109]
	v_mfma_f32_16x16x32_bf16 v[94:97], v[130:133], v[170:173], v[94:97]
	v_mfma_f32_16x16x32_bf16 v[90:93], v[138:141], v[170:173], v[90:93]
	v_mfma_f32_16x16x32_bf16 v[126:129], v[134:137], v[150:153], v[126:129]
	v_mfma_f32_16x16x32_bf16 v[122:125], v[142:145], v[150:153], v[122:125]
	v_mfma_f32_16x16x32_bf16 v[118:121], v[134:137], v[158:161], v[118:121]
	v_mfma_f32_16x16x32_bf16 v[114:117], v[142:145], v[158:161], v[114:117]
	v_mfma_f32_16x16x32_bf16 v[110:113], v[134:137], v[166:169], v[110:113]
	v_mfma_f32_16x16x32_bf16 v[106:109], v[142:145], v[166:169], v[106:109]
	v_mfma_f32_16x16x32_bf16 v[94:97], v[134:137], v[174:177], v[94:97]
	v_mfma_f32_16x16x32_bf16 v[90:93], v[142:145], v[174:177], v[90:93]
	s_barrier
	s_add_i32 s5, 0, 0x1c000
	s_add_i32 s4, s4, s38
	v_add_u32_e32 v185, s5, v224
	v_lshl_add_u64 v[202:203], v[238:239], 0, s[12:13]
	s_mov_b32 m0, s4
	ds_read_b128 v[198:201], v185
	ds_read_b128 v[206:209], v185 offset:1024
	ds_read_b128 v[210:213], v185 offset:2048
	ds_read_b128 v[232:235], v185 offset:3072
	global_load_lds_dwordx4 v[202:203], off
	v_lshl_add_u64 v[202:203], v[240:241], 0, s[12:13]
	s_add_i32 m0, s4, 0x2000
	s_nop 0
	global_load_lds_dwordx4 v[202:203], off
	s_barrier
	s_waitcnt lgkmcnt(0)
	s_waitcnt lgkmcnt(0)
	v_mfma_f32_16x16x32_bf16 v[102:105], v[198:201], v[146:149], v[102:105]
	v_mfma_f32_16x16x32_bf16 v[98:101], v[210:213], v[146:149], v[98:101]
	v_mfma_f32_16x16x32_bf16 v[86:89], v[198:201], v[154:157], v[86:89]
	v_mfma_f32_16x16x32_bf16 v[82:85], v[210:213], v[154:157], v[82:85]
	v_mfma_f32_16x16x32_bf16 v[78:81], v[198:201], v[162:165], v[78:81]
	v_mfma_f32_16x16x32_bf16 v[74:77], v[210:213], v[162:165], v[74:77]
	v_mfma_f32_16x16x32_bf16 v[70:73], v[198:201], v[170:173], v[70:73]
	v_mfma_f32_16x16x32_bf16 v[66:69], v[210:213], v[170:173], v[66:69]
	v_mfma_f32_16x16x32_bf16 v[102:105], v[206:209], v[150:153], v[102:105]
	v_mfma_f32_16x16x32_bf16 v[98:101], v[232:235], v[150:153], v[98:101]
	v_mfma_f32_16x16x32_bf16 v[86:89], v[206:209], v[158:161], v[86:89]
	v_mfma_f32_16x16x32_bf16 v[82:85], v[232:235], v[158:161], v[82:85]
	v_mfma_f32_16x16x32_bf16 v[78:81], v[206:209], v[166:169], v[78:81]
	v_mfma_f32_16x16x32_bf16 v[74:77], v[232:235], v[166:169], v[74:77]
	v_mfma_f32_16x16x32_bf16 v[70:73], v[206:209], v[174:177], v[70:73]
	v_mfma_f32_16x16x32_bf16 v[66:69], v[232:235], v[174:177], v[66:69]
	s_mov_b32 m0, s48
	v_lshl_add_u64 v[202:203], v[242:243], 0, s[12:13]
	s_barrier
	ds_read_b128 v[146:149], v226 offset:49152
	ds_read_b128 v[150:153], v226 offset:50176
	ds_read_b128 v[154:157], v226 offset:51200
	ds_read_b128 v[158:161], v226 offset:52224
	ds_read_b128 v[162:165], v226 offset:53248
	ds_read_b128 v[166:169], v226 offset:54272
	ds_read_b128 v[170:173], v226 offset:55296
	ds_read_b128 v[174:177], v226 offset:56320
	global_load_lds_dwordx4 v[202:203], off
	v_lshl_add_u64 v[202:203], v[244:245], 0, s[12:13]
	s_mov_b32 m0, s49
	s_nop 0
	global_load_lds_dwordx4 v[202:203], off
	s_barrier
	s_waitcnt lgkmcnt(0)
	s_waitcnt lgkmcnt(0)
	v_mfma_f32_16x16x32_bf16 v[62:65], v[130:133], v[146:149], v[62:65]
	v_mfma_f32_16x16x32_bf16 v[58:61], v[138:141], v[146:149], v[58:61]
	v_mfma_f32_16x16x32_bf16 v[46:49], v[130:133], v[154:157], v[46:49]
	v_mfma_f32_16x16x32_bf16 v[42:45], v[138:141], v[154:157], v[42:45]
	v_mfma_f32_16x16x32_bf16 v[30:33], v[130:133], v[162:165], v[30:33]
	v_mfma_f32_16x16x32_bf16 v[26:29], v[138:141], v[162:165], v[26:29]
	v_mfma_f32_16x16x32_bf16 v[14:17], v[130:133], v[170:173], v[14:17]
	v_mfma_f32_16x16x32_bf16 v[10:13], v[138:141], v[170:173], v[10:13]
	v_mfma_f32_16x16x32_bf16 v[62:65], v[134:137], v[150:153], v[62:65]
	v_mfma_f32_16x16x32_bf16 v[58:61], v[142:145], v[150:153], v[58:61]
	v_mfma_f32_16x16x32_bf16 v[46:49], v[134:137], v[158:161], v[46:49]
	v_mfma_f32_16x16x32_bf16 v[42:45], v[142:145], v[158:161], v[42:45]
	v_mfma_f32_16x16x32_bf16 v[30:33], v[134:137], v[166:169], v[30:33]
	v_mfma_f32_16x16x32_bf16 v[26:29], v[142:145], v[166:169], v[26:29]
	v_mfma_f32_16x16x32_bf16 v[14:17], v[134:137], v[174:177], v[14:17]
	v_mfma_f32_16x16x32_bf16 v[10:13], v[142:145], v[174:177], v[10:13]
	s_barrier
	v_lshl_add_u64 v[130:131], v[236:237], 0, s[14:15]
	s_add_i32 s4, s5, s38
	v_lshl_add_u64 v[132:133], v[130:131], 0, v[180:181]
	s_mov_b32 m0, s4
	v_lshl_add_u64 v[130:131], v[130:131], 0, v[182:183]
	global_load_lds_dwordx4 v[132:133], off
	s_add_i32 m0, s4, 0x2000
	s_nop 0
	global_load_lds_dwordx4 v[130:131], off
	s_waitcnt vmcnt(6)
	s_barrier
	v_mfma_f32_16x16x32_bf16 v[54:57], v[198:201], v[146:149], v[54:57]
	v_mfma_f32_16x16x32_bf16 v[50:53], v[210:213], v[146:149], v[50:53]
	v_mfma_f32_16x16x32_bf16 v[38:41], v[198:201], v[154:157], v[38:41]
	v_mfma_f32_16x16x32_bf16 v[34:37], v[210:213], v[154:157], v[34:37]
	v_mfma_f32_16x16x32_bf16 v[22:25], v[198:201], v[162:165], v[22:25]
	v_mfma_f32_16x16x32_bf16 v[18:21], v[210:213], v[162:165], v[18:21]
	v_mfma_f32_16x16x32_bf16 v[6:9], v[198:201], v[170:173], v[6:9]
	v_mfma_f32_16x16x32_bf16 v[2:5], v[210:213], v[170:173], v[2:5]
	v_mfma_f32_16x16x32_bf16 v[54:57], v[206:209], v[150:153], v[54:57]
	v_mfma_f32_16x16x32_bf16 v[50:53], v[232:235], v[150:153], v[50:53]
	v_mfma_f32_16x16x32_bf16 v[38:41], v[206:209], v[158:161], v[38:41]
	v_mfma_f32_16x16x32_bf16 v[34:37], v[232:235], v[158:161], v[34:37]
	v_mfma_f32_16x16x32_bf16 v[22:25], v[206:209], v[166:169], v[22:25]
	v_mfma_f32_16x16x32_bf16 v[18:21], v[232:235], v[166:169], v[18:21]
	v_mfma_f32_16x16x32_bf16 v[6:9], v[206:209], v[174:177], v[6:9]
	v_mfma_f32_16x16x32_bf16 v[2:5], v[232:235], v[174:177], v[2:5]
	s_add_i32 s23, s23, 2
	s_cmp_gt_u32 s23, 13
	s_cbranch_scc1 .Lkexit2
	s_mov_b64 s[26:27], s[28:29]
	s_branch .Lkhead2
; __device__ __forceinline__ unsigned cvt_pk_bf16(float lo, float hi) { f32x2c v = {lo, hi}; bf16x2c b = __builtin_convertvector(v, bf16x2c); return __builtin_bit_cast(unsigned, b); }
;     __device__ __forceinline__ void operator()(const f32x4 (&acc)[2][2][4][2], const Unit& u, int wr, int wc, int fr, int fq) const {
;         const int row0 = u.row0 + wr * 64 + fr, col0 = (u.pn * BM + wc * 32 + 8 * fq) >> 1;
;         const int odd = fq & 1;
; #pragma unroll
;         for (int ai = 0; ai < 2; ++ai)
; #pragma unroll
;             for (int m = 0; m < 4; ++m) { const int row = row0 + ai * HALF + m * 16; bf16_t* rowp = A + (size_t)row * FF + col0;
;                 u32x2 w[2];
; #pragma unroll
;                 for (int bj = 0; bj < 2; ++bj) { const f32x4 a = acc[ai][bj][m][0], b = acc[ai][bj][m][1]; float o[4];
; #pragma unroll
;                     for (int j = 0; j < 4; ++j) o[j] = a[j] * __builtin_amdgcn_rcpf(1.0f + __expf(-a[j])) * b[j];
;                     w[bj].x = cvt_pk_bf16(o[0], o[1]); w[bj].y = cvt_pk_bf16(o[2], o[3]); }
;                 const auto rx = __builtin_amdgcn_permlane16_swap(w[0].x, w[1].x, false, false); const auto ry = __builtin_amdgcn_permlane16_swap(w[0].y, w[1].y, false, false);
;                 u32x4 v; v.x = rx[0]; v.y = ry[0]; v.z = rx[1]; v.w = ry[1];
;                 if (row < u.rend) *(u32x4*)(rowp + (odd ? HALF / 2 - 4 : 0)) = v; }
;     }
.Lkexit2:
	s_barrier
.LBB0_1214:
	v_mul_f32_e32 v133, 0xbfb8aa3b, v126
	v_exp_f32_e32 v133, v133
	v_lshl_or_b32 v130, s24, 8, v225
	v_ashrrev_i32_e32 v130, 1, v130
	v_add_u32_e32 v132, v228, v223
	v_add_f32_e32 v133, 1.0, v133
	v_rcp_f32_e32 v134, v133
	v_mul_f32_e32 v133, 0xbfb8aa3b, v127
	v_exp_f32_e32 v133, v133
	v_ashrrev_i32_e32 v131, 31, v130
	v_cmp_lt_i32_e32 vcc, v132, v179
	v_add_f32_e32 v133, 1.0, v133
	v_rcp_f32_e32 v135, v133
	s_nop 0
	v_pk_mul_f32 v[126:127], v[126:127], v[134:135]
	s_nop 0
	v_pk_mul_f32 v[122:123], v[122:123], v[126:127]
	v_mul_f32_e32 v126, 0xbfb8aa3b, v128
	v_mul_f32_e32 v127, 0xbfb8aa3b, v129
	v_exp_f32_e32 v126, v126
	v_exp_f32_e32 v127, v127
	v_cvt_pk_bf16_f32 v122, v122, v123
	v_add_f32_e32 v126, 1.0, v126
	v_add_f32_e32 v127, 1.0, v127
	v_rcp_f32_e32 v126, v126
	v_rcp_f32_e32 v127, v127
	s_nop 0
	v_pk_mul_f32 v[126:127], v[128:129], v[126:127]
	s_nop 0
	v_pk_mul_f32 v[124:125], v[124:125], v[126:127]
	s_nop 0
	v_cvt_pk_bf16_f32 v123, v124, v125
	v_mul_f32_e32 v124, 0xbfb8aa3b, v102
	v_mul_f32_e32 v125, 0xbfb8aa3b, v103
	v_exp_f32_e32 v124, v124
	v_exp_f32_e32 v125, v125
	v_add_f32_e32 v124, 1.0, v124
	v_add_f32_e32 v125, 1.0, v125
	v_rcp_f32_e32 v124, v124
	v_rcp_f32_e32 v125, v125
	s_nop 0
	v_pk_mul_f32 v[102:103], v[102:103], v[124:125]
	s_nop 0
	v_pk_mul_f32 v[98:99], v[98:99], v[102:103]
	v_mul_f32_e32 v102, 0xbfb8aa3b, v104
	v_mul_f32_e32 v103, 0xbfb8aa3b, v105
	v_exp_f32_e32 v102, v102
	v_exp_f32_e32 v103, v103
	v_cvt_pk_bf16_f32 v124, v98, v99
	s_nop 1
	v_permlane16_swap_b32_e32 v122, v124
	v_add_f32_e32 v102, 1.0, v102
	v_add_f32_e32 v103, 1.0, v103
	v_rcp_f32_e32 v102, v102
	v_rcp_f32_e32 v103, v103
	s_nop 0
	v_pk_mul_f32 v[102:103], v[104:105], v[102:103]
	s_nop 0
	v_pk_mul_f32 v[100:101], v[100:101], v[102:103]
	v_lshlrev_b32_e32 v102, 1, v178
	v_cvt_pk_bf16_f32 v125, v100, v101
	s_nop 1
	v_permlane16_swap_b32_e32 v123, v125
	s_and_saveexec_b64 s[0:1], vcc
	s_cbranch_execz .LBB0_1216
	v_ashrrev_i32_e32 v133, 31, v132
	v_lshlrev_b64 v[98:99], 10, v[132:133]
	v_lshl_add_u64 v[98:99], s[18:19], 0, v[98:99]
	v_lshl_add_u64 v[98:99], v[130:131], 1, v[98:99]
	v_mov_b32_e32 v103, v1
	v_lshl_add_u64 v[98:99], v[98:99], 0, v[102:103]
	global_store_dwordx4 v[98:99], v[122:125], off

;     __device__ __forceinline__ const char* b_ptr(const Unit& u) const { return (const char*)Bt + ((size_t)u.pn * BM * K + u.koff) * 2; }
;     __device__ __forceinline__ const char* b_ptr(const Unit& u) const { return (const char*)Bt + ((size_t)u.e * bstride + (size_t)u.pn * BM * K) * 2; }
; template <class Epi, class Sched>
; __device__ __forceinline__ void gemm_phase(LAS unsigned char* lds, const bf16_t* Abase, const int K, const Sched& S, const Epi& E, const int wvid) {
;     ...
;         const bool has_next = S.next(ui + 1, nxt);
;         const char* nB = has_next ? S.b_ptr(nxt) : cB;
;         const int nt = cur.kt;
;         for (int t = 0; t < nt; t += 2) {
;             const bool last = (t == nt - 2);
;     ...
; #pragma unroll
;         for (int a = 0; a < 2; ++a)
; #pragma unroll
;             for (int b = 0; b < 2; ++b)
; #pragma unroll
;                 for (int m = 0; m < 4; ++m)
; #pragma unroll
;                     for (int n = 0; n < 2; ++n) acc[a][b][m][n] = (f32x4){0.f, 0.f, 0.f, 0.f};
;         cur = nxt; cB = nB; ++ui;
.LBB0_1475:
	s_ashr_i32 s25, s24, 31
	s_lshl_b64 s[4:5], s[24:25], 18
	v_ashrrev_i32_e32 v191, 31, v190
	s_add_u32 s4, s36, s4
	v_lshlrev_b64 v[4:5], 20, v[190:191]
	s_addc_u32 s5, s37, s5
	v_lshl_add_u64 v[194:195], s[4:5], 0, v[4:5]
	s_mov_b64 s[4:5], 0x100
	v_cndmask_b32_e64 v229, v2, v194, s[0:1]
	v_lshl_add_u64 v[196:197], v[2:3], 0, s[4:5]
	v_mov_b32_e32 v2, 0
	v_cndmask_b32_e64 v191, v3, v195, s[0:1]
	v_add_u32_e32 v230, 0x80, v228
	s_mov_b32 s25, -2
	s_mov_b64 s[26:27], 0
	v_mov_b32_e32 v3, v2
	v_mov_b32_e32 v4, v2
	v_mov_b32_e32 v5, v2
	v_mov_b32_e32 v6, v2
	v_mov_b32_e32 v7, v2
	v_mov_b32_e32 v8, v2
	v_mov_b32_e32 v9, v2
	v_mov_b32_e32 v18, v2
	v_mov_b32_e32 v19, v2
	v_mov_b32_e32 v20, v2
	v_mov_b32_e32 v21, v2
	v_mov_b32_e32 v22, v2
	v_mov_b32_e32 v23, v2
	v_mov_b32_e32 v24, v2
	v_mov_b32_e32 v25, v2
	v_mov_b32_e32 v34, v2
	v_mov_b32_e32 v35, v2
	v_mov_b32_e32 v36, v2
	v_mov_b32_e32 v37, v2
	v_mov_b32_e32 v38, v2
	v_mov_b32_e32 v39, v2
	v_mov_b32_e32 v40, v2
	v_mov_b32_e32 v41, v2
	v_mov_b32_e32 v50, v2
	v_mov_b32_e32 v51, v2
	v_mov_b32_e32 v52, v2
	v_mov_b32_e32 v53, v2
	v_mov_b32_e32 v54, v2
	v_mov_b32_e32 v55, v2
	v_mov_b32_e32 v56, v2
	v_mov_b32_e32 v57, v2
	v_mov_b32_e32 v10, v2
	v_mov_b32_e32 v11, v2
	v_mov_b32_e32 v12, v2
	v_mov_b32_e32 v13, v2
	v_mov_b32_e32 v14, v2
	v_mov_b32_e32 v15, v2
	v_mov_b32_e32 v16, v2
	v_mov_b32_e32 v17, v2
	v_mov_b32_e32 v26, v2
	v_mov_b32_e32 v27, v2
	v_mov_b32_e32 v28, v2
	v_mov_b32_e32 v29, v2
	v_mov_b32_e32 v30, v2
	v_mov_b32_e32 v31, v2
	v_mov_b32_e32 v32, v2
	v_mov_b32_e32 v33, v2
	v_mov_b32_e32 v42, v2
	v_mov_b32_e32 v43, v2
	v_mov_b32_e32 v44, v2
	v_mov_b32_e32 v45, v2
	v_mov_b32_e32 v46, v2
	v_mov_b32_e32 v47, v2
	v_mov_b32_e32 v48, v2
	v_mov_b32_e32 v49, v2
	v_mov_b32_e32 v58, v2
	v_mov_b32_e32 v59, v2
	v_mov_b32_e32 v60, v2
	v_mov_b32_e32 v61, v2
	v_mov_b32_e32 v62, v2
	v_mov_b32_e32 v63, v2
	v_mov_b32_e32 v64, v2
	v_mov_b32_e32 v65, v2
	v_mov_b32_e32 v66, v2
	v_mov_b32_e32 v67, v2
	v_mov_b32_e32 v68, v2
	v_mov_b32_e32 v69, v2
	v_mov_b32_e32 v70, v2
	v_mov_b32_e32 v71, v2
	v_mov_b32_e32 v72, v2
	v_mov_b32_e32 v73, v2
	v_mov_b32_e32 v74, v2
	v_mov_b32_e32 v75, v2
	v_mov_b32_e32 v76, v2
	v_mov_b32_e32 v77, v2
	v_mov_b32_e32 v78, v2
	v_mov_b32_e32 v79, v2
	v_mov_b32_e32 v80, v2
	v_mov_b32_e32 v81, v2
	v_mov_b32_e32 v82, v2
	v_mov_b32_e32 v83, v2
	v_mov_b32_e32 v84, v2
	v_mov_b32_e32 v85, v2
	v_mov_b32_e32 v86, v2
	v_mov_b32_e32 v87, v2
	v_mov_b32_e32 v88, v2
	v_mov_b32_e32 v89, v2
	v_mov_b32_e32 v90, v2
	v_mov_b32_e32 v91, v2
	v_mov_b32_e32 v92, v2
	v_mov_b32_e32 v93, v2
	v_mov_b32_e32 v94, v2
	v_mov_b32_e32 v95, v2
	v_mov_b32_e32 v96, v2
	v_mov_b32_e32 v97, v2
	v_mov_b32_e32 v98, v2
	v_mov_b32_e32 v99, v2
	v_mov_b32_e32 v100, v2
	v_mov_b32_e32 v101, v2
	v_mov_b32_e32 v102, v2
	v_mov_b32_e32 v103, v2
	v_mov_b32_e32 v104, v2
	v_mov_b32_e32 v105, v2
	v_mov_b32_e32 v106, v2
	v_mov_b32_e32 v107, v2
	v_mov_b32_e32 v108, v2
	v_mov_b32_e32 v109, v2
	v_mov_b32_e32 v110, v2
	v_mov_b32_e32 v111, v2
	v_mov_b32_e32 v112, v2
	v_mov_b32_e32 v113, v2
	v_mov_b32_e32 v114, v2
	v_mov_b32_e32 v115, v2
	v_mov_b32_e32 v116, v2
	v_mov_b32_e32 v117, v2
	v_mov_b32_e32 v118, v2
	v_mov_b32_e32 v119, v2
	v_mov_b32_e32 v120, v2
	v_mov_b32_e32 v121, v2
	v_mov_b32_e32 v122, v2
	v_mov_b32_e32 v123, v2
	v_mov_b32_e32 v124, v2
	v_mov_b32_e32 v125, v2
	v_mov_b32_e32 v126, v2
	v_mov_b32_e32 v127, v2
	v_mov_b32_e32 v128, v2
	v_mov_b32_e32 v129, v2
	s_branch .LBB0_1476
.Lkhead3:
	s_barrier
; #define PG8_STAGE(bufoff, gbase, voff) do { _Pragma("unroll") for (int _i = 0; _i < 2; ++_i) \
;         __builtin_amdgcn_global_load_lds((const unsigned*)((const char*)(gbase) + (voff)[_i]), (LAS unsigned*)(lds + (bufoff) + ldsw + _i * 8192), 16, 0, 0); } while (0)
; #define PG8_LDA(dst, b, h) do { _Pragma("unroll") for (int m = 0; m < 4; ++m) _Pragma("unroll") for (int k = 0; k < 2; ++k) dst[m][k] = *(const LAS bf16x8*)(lds + PG8_SA(b, h) + aoff + m * 2048 + k * 1024); } while (0)
; #define PG8_LDB(dst, b, h) do { _Pragma("unroll") for (int n = 0; n < 2; ++n) _Pragma("unroll") for (int k = 0; k < 2; ++k) dst[n][k] = *(const LAS bf16x8*)(lds + PG8_SB(b, h) + boff + n * 2048 + k * 1024); } while (0)
; #define PG8_MMA(ai, bj, At, Bt) do { __builtin_amdgcn_s_setprio(1); _Pragma("unroll") for (int m = 0; m < 4; ++m) _Pragma("unroll") for (int n = 0; n < 2; ++n) _Pragma("unroll") for (int k = 0; k < 2; ++k) \
;         acc[ai][bj][m][n] = __builtin_amdgcn_mfma_f32_16x16x32_bf16(Bt[n][k], At[m][k], acc[ai][bj][m][n], 0, 0, 0); __builtin_amdgcn_s_setprio(0); } while (0)
; #define PG8_WAIT_L(n) asm volatile("s_waitcnt lgkmcnt(" #n ")" ::: "memory")
; #define PG8_BAR __builtin_amdgcn_s_barrier()
; #define PG8_SCHED __builtin_amdgcn_sched_barrier(0)
; #define PG8_AOFF(u) do { const int _t = lt_tid(wvid); _Pragma("unroll") for (int _i = 0; _i < 2; ++_i) { int _R, _C; stage_rc(_t * 16 + _i * 8192, _R, _C); \
;         _Pragma("unroll") for (int _h = 0; _h < 2; ++_h) voffA[_h][_i] = (S.a_row(u, _h * HALF + _R) * (unsigned)K + (unsigned)(_C + (u).koff)) * 2u; } } while (0)
; template <class Epi, class Sched>
; __device__ __forceinline__ void gemm_phase(LAS unsigned char* lds, const bf16_t* Abase, const int K, const Sched& S, const Epi& E, const int wvid) {
;     ...
;             PG8_LDB(B0, 0, 0); PG8_SCHED; PG8_LDA(At, 0, 0); PG8_STAGE(PG8_SA(1, 1), a1, voffA[1]);
;             PG8_WAIT_L(8); PG8_BAR; PG8_WAIT_L(0); PG8_MMA(0, 0, At, B0); PG8_BAR; PG8_SCHED;
;             if (last && has_next) PG8_AOFF(nxt);
.LBB0_1476:
	s_waitcnt vmcnt(0)
	v_add_u32_e32 v130, 0, v223
	v_add_u32_e32 v142, 0x10000, v130
	ds_read_b128 v[130:133], v142
	ds_read_b128 v[134:137], v142 offset:1024
	ds_read_b128 v[138:141], v142 offset:2048
	ds_read_b128 v[142:145], v142 offset:3072
	s_cmp_eq_u32 s25, 4
	s_cselect_b64 s[4:5], -1, 0
	s_add_i32 m0, s17, 0xc000
	s_add_u32 s28, s22, s26
	s_addc_u32 s29, s23, s27
	ds_read_b128 v[170:173], v225
	ds_read_b128 v[174:177], v225 offset:1024
	ds_read_b128 v[162:165], v225 offset:2048
	ds_read_b128 v[166:169], v225 offset:3072
	ds_read_b128 v[154:157], v225 offset:4096
	ds_read_b128 v[158:161], v225 offset:5120
	ds_read_b128 v[146:149], v225 offset:6144
	ds_read_b128 v[150:153], v225 offset:7168
	global_load_lds_dwordx4 v184, s[28:29]
	s_add_i32 m0, s17, 0xe000
	s_nop 0
	global_load_lds_dwordx4 v188, s[28:29]
	s_waitcnt lgkmcnt(8)
	s_barrier
	s_waitcnt lgkmcnt(0)
	s_waitcnt lgkmcnt(0)
	v_mfma_f32_16x16x32_bf16 v[126:129], v[130:133], v[170:173], v[126:129]
	v_mfma_f32_16x16x32_bf16 v[122:125], v[138:141], v[170:173], v[122:125]
	v_mfma_f32_16x16x32_bf16 v[118:121], v[130:133], v[162:165], v[118:121]
	v_mfma_f32_16x16x32_bf16 v[114:117], v[138:141], v[162:165], v[114:117]
	v_mfma_f32_16x16x32_bf16 v[110:113], v[130:133], v[154:157], v[110:113]
	v_mfma_f32_16x16x32_bf16 v[106:109], v[138:141], v[154:157], v[106:109]
	v_mfma_f32_16x16x32_bf16 v[102:105], v[130:133], v[146:149], v[102:105]
	v_mfma_f32_16x16x32_bf16 v[98:101], v[138:141], v[146:149], v[98:101]
	v_mfma_f32_16x16x32_bf16 v[126:129], v[134:137], v[174:177], v[126:129]
	v_mfma_f32_16x16x32_bf16 v[122:125], v[142:145], v[174:177], v[122:125]
	v_mfma_f32_16x16x32_bf16 v[118:121], v[134:137], v[166:169], v[118:121]
	v_mfma_f32_16x16x32_bf16 v[114:117], v[142:145], v[166:169], v[114:117]
	v_mfma_f32_16x16x32_bf16 v[110:113], v[134:137], v[158:161], v[110:113]
	v_mfma_f32_16x16x32_bf16 v[106:109], v[142:145], v[158:161], v[106:109]
	v_mfma_f32_16x16x32_bf16 v[102:105], v[134:137], v[150:153], v[102:105]
	v_mfma_f32_16x16x32_bf16 v[98:101], v[142:145], v[150:153], v[98:101]
	s_barrier
	s_and_b64 s[28:29], s[0:1], s[4:5]
	s_andn2_b64 vcc, exec, s[28:29]
	s_cbranch_vccnz .LBB0_1478
	v_mbcnt_lo_u32_b32 v0, -1, 0
	v_mbcnt_hi_u32_b32 v0, -1, v0
	s_nop 0
	v_or_b32_e32 v0, s75, v0
	v_ashrrev_i32_e32 v185, 31, v0
	v_lshrrev_b32_e32 v185, 26, v185
	v_lshlrev_b32_e32 v184, 4, v0
	v_add_u32_e32 v185, v0, v185
	v_bfe_i32 v0, v0, 27, 1
	v_lshrrev_b32_e32 v0, 22, v0
	v_add_u32_e32 v0, v184, v0
	v_and_b32_e32 v0, 0xfffffc00, v0
	v_sub_u32_e32 v0, v184, v0
	v_lshrrev_b32_e32 v186, 4, v0
	v_bitop3_b32 v0, v186, v0, 32 bitop3:0x6c
	v_ashrrev_i32_e32 v187, 31, v0
	v_lshrrev_b32_e32 v187, 26, v187
	v_add_u32_e32 v187, v0, v187
	v_ashrrev_i32_e32 v185, 6, v185
	v_ashrrev_i32_e32 v188, 6, v187
	v_and_b32_e32 v187, 0xc0, v187
	v_lshlrev_b32_e32 v186, 3, v185
	v_sub_u32_e32 v0, v0, v187
	v_and_b32_e32 v186, -16, v186
	v_lshlrev_b32_e32 v185, 5, v185
	v_ashrrev_i16_sdwa v0, v216, sext(v0) dst_sel:DWORD dst_unused:UNUSED_PAD src0_sel:DWORD src1_sel:BYTE_0
	v_add_u32_e32 v186, v188, v186
	v_and_b32_e32 v185, 32, v185
	v_bfe_i32 v0, v0, 0, 16
	v_add_lshl_u32 v0, v185, v0, 1
	v_add_u32_e32 v185, v186, v228
	v_add_u32_e32 v186, v186, v230
	v_add_u32_e32 v184, 0x2000, v184
	v_lshl_add_u32 v185, v185, 10, v0
	v_lshl_add_u32 v0, v186, 10, v0
	v_ashrrev_i32_e32 v186, 31, v184
	v_lshrrev_b32_e32 v186, 22, v186
	v_add_u32_e32 v186, v184, v186
	v_ashrrev_i32_e32 v186, 10, v186
	v_mul_i32_i24_e32 v187, 0x400, v186
	v_sub_u32_e32 v184, v184, v187
	v_lshrrev_b32_e32 v187, 4, v184
	v_bitop3_b32 v184, v187, v184, 32 bitop3:0x6c
	v_ashrrev_i32_e32 v188, 31, v184
	v_lshrrev_b32_e32 v188, 26, v188
	v_add_u32_e32 v188, v184, v188
	v_ashrrev_i32_e32 v189, 6, v188
	v_and_b32_e32 v188, 0xc0, v188
	v_lshlrev_b32_e32 v187, 3, v186
	v_sub_u32_e32 v184, v184, v188
	v_and_b32_e32 v187, -16, v187
	v_lshlrev_b32_e32 v186, 5, v186
	v_ashrrev_i16_sdwa v184, v216, sext(v184) dst_sel:DWORD dst_unused:UNUSED_PAD src0_sel:DWORD src1_sel:BYTE_0
	v_add_u32_e32 v187, v189, v187
	v_and_b32_e32 v186, 32, v186
	v_bfe_i32 v184, v184, 0, 16
	v_add_lshl_u32 v184, v186, v184, 1
	v_add_u32_e32 v186, v187, v228
	v_add_u32_e32 v187, v187, v230
	v_lshl_add_u32 v186, v186, 10, v184
	v_lshl_add_u32 v188, v187, 10, v184
	v_mov_b32_e32 v189, v1
	v_mov_b64_e32 v[198:199], v[0:1]
	v_mov_b32_e32 v184, v0
	v_mov_b32_e32 v0, v185
	s_branch .LBB0_1479

; #define PG8_STAGE(bufoff, gbase, voff) do { _Pragma("unroll") for (int _i = 0; _i < 2; ++_i) \
;         __builtin_amdgcn_global_load_lds((const unsigned*)((const char*)(gbase) + (voff)[_i]), (LAS unsigned*)(lds + (bufoff) + ldsw + _i * 8192), 16, 0, 0); } while (0)
; #define PG8_LDA(dst, b, h) do { _Pragma("unroll") for (int m = 0; m < 4; ++m) _Pragma("unroll") for (int k = 0; k < 2; ++k) dst[m][k] = *(const LAS bf16x8*)(lds + PG8_SA(b, h) + aoff + m * 2048 + k * 1024); } while (0)
; #define PG8_LDB(dst, b, h) do { _Pragma("unroll") for (int n = 0; n < 2; ++n) _Pragma("unroll") for (int k = 0; k < 2; ++k) dst[n][k] = *(const LAS bf16x8*)(lds + PG8_SB(b, h) + boff + n * 2048 + k * 1024); } while (0)
; #define PG8_MMA(ai, bj, At, Bt) do { __builtin_amdgcn_s_setprio(1); _Pragma("unroll") for (int m = 0; m < 4; ++m) _Pragma("unroll") for (int n = 0; n < 2; ++n) _Pragma("unroll") for (int k = 0; k < 2; ++k) \
;         acc[ai][bj][m][n] = __builtin_amdgcn_mfma_f32_16x16x32_bf16(Bt[n][k], At[m][k], acc[ai][bj][m][n], 0, 0, 0); __builtin_amdgcn_s_setprio(0); } while (0)
; #define PG8_WAIT_V(n) asm volatile("s_waitcnt vmcnt(" #n ")" ::: "memory")
; #define PG8_WAIT_L(n) asm volatile("s_waitcnt lgkmcnt(" #n ")" ::: "memory")
; #define PG8_BAR __builtin_amdgcn_s_barrier()
; #define PG8_SCHED __builtin_amdgcn_sched_barrier(0)
; template <class Epi, class Sched>
; __device__ __forceinline__ void gemm_phase(LAS unsigned char* lds, const bf16_t* Abase, const int K, const Sched& S, const Epi& E, const int wvid) {
;     ...
;             const char* a2 = last ? Ab : Ab + (size_t)(t + 2) * kstep; const char* b2 = last ? nB : cB + (size_t)(t + 2) * kstep;
;             const char* a3 = a2 + kstep; const char* b3 = b2 + kstep;
;             PG8_LDB(B1, 0, 1); PG8_STAGE(PG8_SB(0, 0), b2, voffB);
;             PG8_BAR; PG8_WAIT_L(0); PG8_MMA(0, 1, At, B1); PG8_BAR;
;             PG8_LDA(At, 0, 1); PG8_STAGE(PG8_SA(0, 0), a2, voffA[0]);
;             PG8_BAR; PG8_WAIT_L(0); PG8_MMA(1, 0, At, B0); PG8_BAR; PG8_SCHED;
;             PG8_STAGE(PG8_SB(0, 1), b2 + hstep, voffB);
;             PG8_WAIT_V(6); PG8_BAR; PG8_MMA(1, 1, At, B1); PG8_BAR;
;             PG8_LDB(B0, 1, 0); PG8_SCHED; PG8_LDA(At, 1, 0); PG8_STAGE(PG8_SA(0, 1), a2, voffA[1]);
.LBB0_1479:
	s_add_u32 s28, s26, 0x100
	s_addc_u32 s29, s27, 0
	s_and_b64 s[30:31], s[4:5], exec
	s_cselect_b32 s30, 0, s28
	s_cselect_b32 s31, 0, s29
	s_add_u32 s30, s10, s30
	v_lshl_add_u64 v[236:237], v[196:197], 0, s[26:27]
	s_addc_u32 s31, s11, s31
	s_add_i32 s26, 0, 0x14000
	v_cndmask_b32_e64 v237, v237, v191, s[4:5]
	v_cndmask_b32_e64 v236, v236, v229, s[4:5]
	s_mov_b32 m0, s39
	v_add_u32_e32 v185, s26, v223
	v_lshl_add_u64 v[238:239], v[236:237], 0, v[180:181]
	ds_read_b128 v[200:203], v185
	ds_read_b128 v[206:209], v185 offset:1024
	ds_read_b128 v[210:213], v185 offset:2048
	ds_read_b128 v[232:235], v185 offset:3072
	global_load_lds_dwordx4 v[238:239], off
	v_lshl_add_u64 v[240:241], v[236:237], 0, v[182:183]
	s_mov_b32 m0, s42
	s_nop 0
	global_load_lds_dwordx4 v[240:241], off
	s_barrier
	s_waitcnt lgkmcnt(0)
	s_waitcnt lgkmcnt(0)
	v_mfma_f32_16x16x32_bf16 v[94:97], v[200:203], v[170:173], v[94:97]
	v_mfma_f32_16x16x32_bf16 v[90:93], v[210:213], v[170:173], v[90:93]
	v_mfma_f32_16x16x32_bf16 v[86:89], v[200:203], v[162:165], v[86:89]
	v_mfma_f32_16x16x32_bf16 v[82:85], v[210:213], v[162:165], v[82:85]
	v_mfma_f32_16x16x32_bf16 v[78:81], v[200:203], v[154:157], v[78:81]
	v_mfma_f32_16x16x32_bf16 v[74:77], v[210:213], v[154:157], v[74:77]
	v_mfma_f32_16x16x32_bf16 v[70:73], v[200:203], v[146:149], v[70:73]
	v_mfma_f32_16x16x32_bf16 v[66:69], v[210:213], v[146:149], v[66:69]
	v_mfma_f32_16x16x32_bf16 v[94:97], v[206:209], v[174:177], v[94:97]
	v_mfma_f32_16x16x32_bf16 v[90:93], v[232:235], v[174:177], v[90:93]
	v_mfma_f32_16x16x32_bf16 v[86:89], v[206:209], v[166:169], v[86:89]
	v_mfma_f32_16x16x32_bf16 v[82:85], v[232:235], v[166:169], v[82:85]
	v_mfma_f32_16x16x32_bf16 v[78:81], v[206:209], v[158:161], v[78:81]
	v_mfma_f32_16x16x32_bf16 v[74:77], v[232:235], v[158:161], v[74:77]
	v_mfma_f32_16x16x32_bf16 v[70:73], v[206:209], v[150:153], v[70:73]
	v_mfma_f32_16x16x32_bf16 v[66:69], v[232:235], v[150:153], v[66:69]
	s_mov_b32 m0, s17
	s_barrier
	ds_read_b128 v[146:149], v225 offset:16384
	ds_read_b128 v[150:153], v225 offset:17408
	ds_read_b128 v[154:157], v225 offset:18432
	ds_read_b128 v[158:161], v225 offset:19456
	ds_read_b128 v[162:165], v225 offset:20480
	ds_read_b128 v[166:169], v225 offset:21504
	ds_read_b128 v[170:173], v225 offset:22528
	ds_read_b128 v[174:177], v225 offset:23552
	global_load_lds_dwordx4 v0, s[30:31]
	s_mov_b32 m0, s43
	v_mov_b32_e32 v187, v1
	global_load_lds_dwordx4 v186, s[30:31]
	s_barrier
	s_waitcnt lgkmcnt(0)
	v_lshl_add_u64 v[242:243], s[30:31], 0, v[0:1]
	v_lshl_add_u64 v[244:245], s[30:31], 0, v[186:187]
	s_waitcnt lgkmcnt(0)
	v_mfma_f32_16x16x32_bf16 v[62:65], v[130:133], v[146:149], v[62:65]
	v_mfma_f32_16x16x32_bf16 v[58:61], v[138:141], v[146:149], v[58:61]
	v_mfma_f32_16x16x32_bf16 v[46:49], v[130:133], v[154:157], v[46:49]
	v_mfma_f32_16x16x32_bf16 v[42:45], v[138:141], v[154:157], v[42:45]
	v_mfma_f32_16x16x32_bf16 v[30:33], v[130:133], v[162:165], v[30:33]
	v_mfma_f32_16x16x32_bf16 v[26:29], v[138:141], v[162:165], v[26:29]
	v_mfma_f32_16x16x32_bf16 v[14:17], v[130:133], v[170:173], v[14:17]
	v_mfma_f32_16x16x32_bf16 v[10:13], v[138:141], v[170:173], v[10:13]
	v_mfma_f32_16x16x32_bf16 v[62:65], v[134:137], v[150:153], v[62:65]
	v_mfma_f32_16x16x32_bf16 v[58:61], v[142:145], v[150:153], v[58:61]
	v_mfma_f32_16x16x32_bf16 v[46:49], v[134:137], v[158:161], v[46:49]
	v_mfma_f32_16x16x32_bf16 v[42:45], v[142:145], v[158:161], v[42:45]
	v_mfma_f32_16x16x32_bf16 v[30:33], v[134:137], v[166:169], v[30:33]
	v_mfma_f32_16x16x32_bf16 v[26:29], v[142:145], v[166:169], v[26:29]
	v_mfma_f32_16x16x32_bf16 v[14:17], v[134:137], v[174:177], v[14:17]
	v_mfma_f32_16x16x32_bf16 v[10:13], v[142:145], v[174:177], v[10:13]
	s_barrier
	v_lshl_add_u64 v[130:131], v[236:237], 0, s[68:69]
	s_add_i32 s4, s26, s38
	v_lshl_add_u64 v[132:133], v[130:131], 0, v[180:181]
	s_mov_b32 m0, s4
	v_lshl_add_u64 v[130:131], v[130:131], 0, v[182:183]
	global_load_lds_dwordx4 v[132:133], off
	s_add_i32 m0, s4, 0x2000
	s_nop 0
	global_load_lds_dwordx4 v[130:131], off
	s_waitcnt vmcnt(6)
	s_barrier
	v_mfma_f32_16x16x32_bf16 v[54:57], v[200:203], v[146:149], v[54:57]
	v_mfma_f32_16x16x32_bf16 v[50:53], v[210:213], v[146:149], v[50:53]
	v_mfma_f32_16x16x32_bf16 v[38:41], v[200:203], v[154:157], v[38:41]
	v_mfma_f32_16x16x32_bf16 v[34:37], v[210:213], v[154:157], v[34:37]
	v_mfma_f32_16x16x32_bf16 v[22:25], v[200:203], v[162:165], v[22:25]
	v_mfma_f32_16x16x32_bf16 v[18:21], v[210:213], v[162:165], v[18:21]
	v_mfma_f32_16x16x32_bf16 v[6:9], v[200:203], v[170:173], v[6:9]
	v_mfma_f32_16x16x32_bf16 v[2:5], v[210:213], v[170:173], v[2:5]
	v_mfma_f32_16x16x32_bf16 v[54:57], v[206:209], v[150:153], v[54:57]
	v_mfma_f32_16x16x32_bf16 v[50:53], v[232:235], v[150:153], v[50:53]
	v_mfma_f32_16x16x32_bf16 v[38:41], v[206:209], v[158:161], v[38:41]
	v_mfma_f32_16x16x32_bf16 v[34:37], v[232:235], v[158:161], v[34:37]
	v_mfma_f32_16x16x32_bf16 v[22:25], v[206:209], v[166:169], v[22:25]
	v_mfma_f32_16x16x32_bf16 v[18:21], v[232:235], v[166:169], v[18:21]
	v_mfma_f32_16x16x32_bf16 v[6:9], v[206:209], v[174:177], v[6:9]
	v_mfma_f32_16x16x32_bf16 v[2:5], v[232:235], v[174:177], v[2:5]
	s_add_i32 s4, 0, 0x18000
	v_add_u32_e32 v142, s4, v223
	s_barrier
	ds_read_b128 v[130:133], v142
	ds_read_b128 v[134:137], v142 offset:1024
	ds_read_b128 v[138:141], v142 offset:2048
	ds_read_b128 v[142:145], v142 offset:3072
	s_mov_b32 m0, s46
	v_lshl_add_u64 v[198:199], s[30:31], 0, v[198:199]
	ds_read_b128 v[146:149], v225 offset:32768
	ds_read_b128 v[150:153], v225 offset:33792
	ds_read_b128 v[154:157], v225 offset:34816
	ds_read_b128 v[158:161], v225 offset:35840
	ds_read_b128 v[162:165], v225 offset:36864
	ds_read_b128 v[166:169], v225 offset:37888
	ds_read_b128 v[170:173], v225 offset:38912
	ds_read_b128 v[174:177], v225 offset:39936
	global_load_lds_dwordx4 v[198:199], off
	v_lshl_add_u64 v[198:199], s[30:31], 0, v[188:189]
	s_mov_b32 m0, s47
	s_nop 0
	global_load_lds_dwordx4 v[198:199], off
	s_waitcnt lgkmcnt(8)
	s_barrier
; #define PG8_STAGE(bufoff, gbase, voff) do { _Pragma("unroll") for (int _i = 0; _i < 2; ++_i) \
;         __builtin_amdgcn_global_load_lds((const unsigned*)((const char*)(gbase) + (voff)[_i]), (LAS unsigned*)(lds + (bufoff) + ldsw + _i * 8192), 16, 0, 0); } while (0)
; #define PG8_LDA(dst, b, h) do { _Pragma("unroll") for (int m = 0; m < 4; ++m) _Pragma("unroll") for (int k = 0; k < 2; ++k) dst[m][k] = *(const LAS bf16x8*)(lds + PG8_SA(b, h) + aoff + m * 2048 + k * 1024); } while (0)
; #define PG8_LDB(dst, b, h) do { _Pragma("unroll") for (int n = 0; n < 2; ++n) _Pragma("unroll") for (int k = 0; k < 2; ++k) dst[n][k] = *(const LAS bf16x8*)(lds + PG8_SB(b, h) + boff + n * 2048 + k * 1024); } while (0)
; #define PG8_MMA(ai, bj, At, Bt) do { __builtin_amdgcn_s_setprio(1); _Pragma("unroll") for (int m = 0; m < 4; ++m) _Pragma("unroll") for (int n = 0; n < 2; ++n) _Pragma("unroll") for (int k = 0; k < 2; ++k) \
;         acc[ai][bj][m][n] = __builtin_amdgcn_mfma_f32_16x16x32_bf16(Bt[n][k], At[m][k], acc[ai][bj][m][n], 0, 0, 0); __builtin_amdgcn_s_setprio(0); } while (0)
; #define PG8_WAIT_V(n) asm volatile("s_waitcnt vmcnt(" #n ")" ::: "memory")
; #define PG8_WAIT_L(n) asm volatile("s_waitcnt lgkmcnt(" #n ")" ::: "memory")
; #define PG8_BAR __builtin_amdgcn_s_barrier()
; #define PG8_SCHED __builtin_amdgcn_sched_barrier(0)
; template <class Epi, class Sched>
; __device__ __forceinline__ void gemm_phase(LAS unsigned char* lds, const bf16_t* Abase, const int K, const Sched& S, const Epi& E, const int wvid) {
;     ...
;             PG8_LDB(B0, 1, 0); PG8_SCHED; PG8_LDA(At, 1, 0); PG8_STAGE(PG8_SA(0, 1), a2, voffA[1]);
;             PG8_WAIT_L(8); PG8_BAR; PG8_WAIT_L(0); PG8_MMA(0, 0, At, B0); PG8_BAR; PG8_SCHED;
;             PG8_LDB(B1, 1, 1); PG8_STAGE(PG8_SB(1, 0), b3, voffB);
;             PG8_BAR; PG8_WAIT_L(0); PG8_MMA(0, 1, At, B1); PG8_BAR;
;             PG8_LDA(At, 1, 1); PG8_STAGE(PG8_SA(1, 0), a3, voffA[0]);
;             PG8_BAR; PG8_WAIT_L(0); PG8_MMA(1, 0, At, B0); PG8_BAR; PG8_SCHED;
;             PG8_STAGE(PG8_SB(1, 1), b3 + hstep, voffB);
;             PG8_WAIT_V(6); PG8_BAR; PG8_MMA(1, 1, At, B1); PG8_BAR;
;         }
	s_waitcnt lgkmcnt(0)
	s_waitcnt lgkmcnt(0)
	v_mfma_f32_16x16x32_bf16 v[126:129], v[130:133], v[146:149], v[126:129]
	v_mfma_f32_16x16x32_bf16 v[122:125], v[138:141], v[146:149], v[122:125]
	v_mfma_f32_16x16x32_bf16 v[118:121], v[130:133], v[154:157], v[118:121]
	v_mfma_f32_16x16x32_bf16 v[114:117], v[138:141], v[154:157], v[114:117]
	v_mfma_f32_16x16x32_bf16 v[110:113], v[130:133], v[162:165], v[110:113]
	v_mfma_f32_16x16x32_bf16 v[106:109], v[138:141], v[162:165], v[106:109]
	v_mfma_f32_16x16x32_bf16 v[102:105], v[130:133], v[170:173], v[102:105]
	v_mfma_f32_16x16x32_bf16 v[98:101], v[138:141], v[170:173], v[98:101]
	v_mfma_f32_16x16x32_bf16 v[126:129], v[134:137], v[150:153], v[126:129]
	v_mfma_f32_16x16x32_bf16 v[122:125], v[142:145], v[150:153], v[122:125]
	v_mfma_f32_16x16x32_bf16 v[118:121], v[134:137], v[158:161], v[118:121]
	v_mfma_f32_16x16x32_bf16 v[114:117], v[142:145], v[158:161], v[114:117]
	v_mfma_f32_16x16x32_bf16 v[110:113], v[134:137], v[166:169], v[110:113]
	v_mfma_f32_16x16x32_bf16 v[106:109], v[142:145], v[166:169], v[106:109]
	v_mfma_f32_16x16x32_bf16 v[102:105], v[134:137], v[174:177], v[102:105]
	v_mfma_f32_16x16x32_bf16 v[98:101], v[142:145], v[174:177], v[98:101]
	s_barrier
	s_add_i32 s5, 0, 0x1c000
	s_add_i32 s4, s4, s38
	v_add_u32_e32 v185, s5, v223
	v_lshl_add_u64 v[202:203], v[238:239], 0, s[12:13]
	s_mov_b32 m0, s4
	ds_read_b128 v[198:201], v185
	ds_read_b128 v[206:209], v185 offset:1024
	ds_read_b128 v[210:213], v185 offset:2048
	ds_read_b128 v[232:235], v185 offset:3072
	global_load_lds_dwordx4 v[202:203], off
	v_lshl_add_u64 v[202:203], v[240:241], 0, s[12:13]
	s_add_i32 m0, s4, 0x2000
	s_nop 0
	global_load_lds_dwordx4 v[202:203], off
	s_barrier
	s_waitcnt lgkmcnt(0)
	s_waitcnt lgkmcnt(0)
	v_mfma_f32_16x16x32_bf16 v[94:97], v[198:201], v[146:149], v[94:97]
	v_mfma_f32_16x16x32_bf16 v[90:93], v[210:213], v[146:149], v[90:93]
	v_mfma_f32_16x16x32_bf16 v[86:89], v[198:201], v[154:157], v[86:89]
	v_mfma_f32_16x16x32_bf16 v[82:85], v[210:213], v[154:157], v[82:85]
	v_mfma_f32_16x16x32_bf16 v[78:81], v[198:201], v[162:165], v[78:81]
	v_mfma_f32_16x16x32_bf16 v[74:77], v[210:213], v[162:165], v[74:77]
	v_mfma_f32_16x16x32_bf16 v[70:73], v[198:201], v[170:173], v[70:73]
	v_mfma_f32_16x16x32_bf16 v[66:69], v[210:213], v[170:173], v[66:69]
	v_mfma_f32_16x16x32_bf16 v[94:97], v[206:209], v[150:153], v[94:97]
	v_mfma_f32_16x16x32_bf16 v[90:93], v[232:235], v[150:153], v[90:93]
	v_mfma_f32_16x16x32_bf16 v[86:89], v[206:209], v[158:161], v[86:89]
	v_mfma_f32_16x16x32_bf16 v[82:85], v[232:235], v[158:161], v[82:85]
	v_mfma_f32_16x16x32_bf16 v[78:81], v[206:209], v[166:169], v[78:81]
	v_mfma_f32_16x16x32_bf16 v[74:77], v[232:235], v[166:169], v[74:77]
	v_mfma_f32_16x16x32_bf16 v[70:73], v[206:209], v[174:177], v[70:73]
	v_mfma_f32_16x16x32_bf16 v[66:69], v[232:235], v[174:177], v[66:69]
	s_mov_b32 m0, s48
	v_lshl_add_u64 v[202:203], v[242:243], 0, s[12:13]
	s_barrier
	ds_read_b128 v[146:149], v225 offset:49152
	ds_read_b128 v[150:153], v225 offset:50176
	ds_read_b128 v[154:157], v225 offset:51200
	ds_read_b128 v[158:161], v225 offset:52224
	ds_read_b128 v[162:165], v225 offset:53248
	ds_read_b128 v[166:169], v225 offset:54272
	ds_read_b128 v[170:173], v225 offset:55296
	ds_read_b128 v[174:177], v225 offset:56320
	global_load_lds_dwordx4 v[202:203], off
	v_lshl_add_u64 v[202:203], v[244:245], 0, s[12:13]
	s_mov_b32 m0, s49
	s_nop 0
	global_load_lds_dwordx4 v[202:203], off
	s_barrier
	s_waitcnt lgkmcnt(0)
	s_waitcnt lgkmcnt(0)
	v_mfma_f32_16x16x32_bf16 v[62:65], v[130:133], v[146:149], v[62:65]
	v_mfma_f32_16x16x32_bf16 v[58:61], v[138:141], v[146:149], v[58:61]
	v_mfma_f32_16x16x32_bf16 v[46:49], v[130:133], v[154:157], v[46:49]
	v_mfma_f32_16x16x32_bf16 v[42:45], v[138:141], v[154:157], v[42:45]
	v_mfma_f32_16x16x32_bf16 v[30:33], v[130:133], v[162:165], v[30:33]
	v_mfma_f32_16x16x32_bf16 v[26:29], v[138:141], v[162:165], v[26:29]
	v_mfma_f32_16x16x32_bf16 v[14:17], v[130:133], v[170:173], v[14:17]
	v_mfma_f32_16x16x32_bf16 v[10:13], v[138:141], v[170:173], v[10:13]
	v_mfma_f32_16x16x32_bf16 v[62:65], v[134:137], v[150:153], v[62:65]
	v_mfma_f32_16x16x32_bf16 v[58:61], v[142:145], v[150:153], v[58:61]
	v_mfma_f32_16x16x32_bf16 v[46:49], v[134:137], v[158:161], v[46:49]
	v_mfma_f32_16x16x32_bf16 v[42:45], v[142:145], v[158:161], v[42:45]
	v_mfma_f32_16x16x32_bf16 v[30:33], v[134:137], v[166:169], v[30:33]
	v_mfma_f32_16x16x32_bf16 v[26:29], v[142:145], v[166:169], v[26:29]
	v_mfma_f32_16x16x32_bf16 v[14:17], v[134:137], v[174:177], v[14:17]
	v_mfma_f32_16x16x32_bf16 v[10:13], v[142:145], v[174:177], v[10:13]
	s_barrier
	v_lshl_add_u64 v[130:131], v[236:237], 0, s[84:85]
	s_add_i32 s4, s5, s38
	v_lshl_add_u64 v[132:133], v[130:131], 0, v[180:181]
	s_mov_b32 m0, s4
	v_lshl_add_u64 v[130:131], v[130:131], 0, v[182:183]
	global_load_lds_dwordx4 v[132:133], off
	s_add_i32 m0, s4, 0x2000
	s_nop 0
	global_load_lds_dwordx4 v[130:131], off
	s_waitcnt vmcnt(6)
	s_barrier
	v_mfma_f32_16x16x32_bf16 v[54:57], v[198:201], v[146:149], v[54:57]
	v_mfma_f32_16x16x32_bf16 v[50:53], v[210:213], v[146:149], v[50:53]
	v_mfma_f32_16x16x32_bf16 v[38:41], v[198:201], v[154:157], v[38:41]
	v_mfma_f32_16x16x32_bf16 v[34:37], v[210:213], v[154:157], v[34:37]
	v_mfma_f32_16x16x32_bf16 v[22:25], v[198:201], v[162:165], v[22:25]
	v_mfma_f32_16x16x32_bf16 v[18:21], v[210:213], v[162:165], v[18:21]
	v_mfma_f32_16x16x32_bf16 v[6:9], v[198:201], v[170:173], v[6:9]
	v_mfma_f32_16x16x32_bf16 v[2:5], v[210:213], v[170:173], v[2:5]
	v_mfma_f32_16x16x32_bf16 v[54:57], v[206:209], v[150:153], v[54:57]
	v_mfma_f32_16x16x32_bf16 v[50:53], v[232:235], v[150:153], v[50:53]
	v_mfma_f32_16x16x32_bf16 v[38:41], v[206:209], v[158:161], v[38:41]
	v_mfma_f32_16x16x32_bf16 v[34:37], v[232:235], v[158:161], v[34:37]
	v_mfma_f32_16x16x32_bf16 v[22:25], v[206:209], v[166:169], v[22:25]
	v_mfma_f32_16x16x32_bf16 v[18:21], v[232:235], v[166:169], v[18:21]
	v_mfma_f32_16x16x32_bf16 v[6:9], v[206:209], v[174:177], v[6:9]
	v_mfma_f32_16x16x32_bf16 v[2:5], v[232:235], v[174:177], v[2:5]
	s_add_i32 s25, s25, 2
	s_cmp_gt_u32 s25, 5
	s_cbranch_scc1 .Lkexit3
	s_mov_b64 s[26:27], s[28:29]
	s_branch .Lkhead3
; __device__ __forceinline__ unsigned cvt_pk_bf16(float lo, float hi) { f32x2c v = {lo, hi}; bf16x2c b = __builtin_convertvector(v, bf16x2c); return __builtin_bit_cast(unsigned, b); }
;     __device__ __forceinline__ void operator()(const f32x4 (&acc)[2][2][4][2], const Unit& u, int wr, int wc, int fr, int fq) const {
;         const int row0 = u.row0 + wr * 64 + fr, col0 = u.pn * BM + wc * 32 + 8 * fq;
;         float gt[2][4];
; #pragma unroll
;         for (int ai = 0; ai < 2; ++ai)
; #pragma unroll
;             for (int m = 0; m < 4; ++m) gt[ai][m] = gate[u.loff + min(row0 + ai * HALF + m * 16, u.rend - 1)];
; #pragma unroll
;         for (int ai = 0; ai < 2; ++ai)
; #pragma unroll
;             for (int m = 0; m < 4; ++m) { const int row = row0 + ai * HALF + m * 16; if (row < u.rend) { const float g = gt[ai][m]; bf16_t* rowp = Y + (size_t)row * D + col0;
; #pragma unroll
;                 for (int bj = 0; bj < 2; ++bj) { const f32x4 v0 = acc[ai][bj][m][0] * g, v1 = acc[ai][bj][m][1] * g;
;                     u32x4 w; w.x = cvt_pk_bf16(v0[0], v0[1]); w.y = cvt_pk_bf16(v0[2], v0[3]); w.z = cvt_pk_bf16(v1[0], v1[1]); w.w = cvt_pk_bf16(v1[2], v1[3]);
;                     *(u32x4*)(rowp + bj * HALF) = w; } } }
.Lkexit3:
	s_barrier
.LBB0_1481:
	v_add_u32_e32 v160, v227, v178
	v_add_u32_e32 v133, -1, v179
	v_add_u32_e32 v158, 16, v160
	v_min_i32_e32 v130, v158, v133
	v_add_u32_e32 v130, v226, v130
	v_ashrrev_i32_e32 v131, 31, v130
	v_lshl_add_u64 v[130:131], v[130:131], 2, s[20:21]
	v_add_u32_e32 v154, 32, v160
	global_load_dword v156, v[130:131], off
	v_min_i32_e32 v130, v154, v133
	v_add_u32_e32 v130, v226, v130
	v_ashrrev_i32_e32 v131, 31, v130
	v_lshl_add_u64 v[130:131], v[130:131], 2, s[20:21]
	v_add_u32_e32 v150, 48, v160
	global_load_dword v152, v[130:131], off
	v_min_i32_e32 v130, v150, v133
	v_add_u32_e32 v130, v226, v130
	v_ashrrev_i32_e32 v131, 31, v130
	v_lshl_add_u64 v[130:131], v[130:131], 2, s[20:21]
	v_add_u32_e32 v146, 0x80, v160
	global_load_dword v148, v[130:131], off
	v_min_i32_e32 v130, v146, v133
	v_add_u32_e32 v130, v226, v130
	v_ashrrev_i32_e32 v131, 31, v130
	v_lshl_add_u64 v[130:131], v[130:131], 2, s[20:21]
	v_add_u32_e32 v142, 0x90, v160
	global_load_dword v144, v[130:131], off
	v_min_i32_e32 v130, v142, v133
	v_add_u32_e32 v130, v226, v130
	v_ashrrev_i32_e32 v131, 31, v130
	v_lshl_add_u64 v[130:131], v[130:131], 2, s[20:21]
	v_add_u32_e32 v138, 0xa0, v160
	global_load_dword v140, v[130:131], off
	v_min_i32_e32 v130, v138, v133
	v_add_u32_e32 v130, v226, v130
	v_ashrrev_i32_e32 v131, 31, v130
	v_lshl_add_u64 v[130:131], v[130:131], 2, s[20:21]
	v_add_u32_e32 v132, 0xb0, v160
	global_load_dword v134, v[130:131], off
	v_min_i32_e32 v130, v132, v133
	v_add_u32_e32 v130, v226, v130
	v_ashrrev_i32_e32 v131, 31, v130
	v_lshl_add_u64 v[130:131], v[130:131], 2, s[20:21]
	global_load_dword v130, v[130:131], off
	v_lshl_or_b32 v136, s16, 8, v224
	v_ashrrev_i32_e32 v137, 31, v136
	v_cmp_lt_i32_e32 vcc, v160, v179
	s_and_saveexec_b64 s[0:1], vcc
	s_cbranch_execnz .LBB0_1489
	s_or_b64 exec, exec, s[0:1]
	v_cmp_lt_i32_e32 vcc, v158, v179
	s_and_saveexec_b64 s[0:1], vcc
	s_cbranch_execnz .LBB0_1490
